# P7: second-pass LN1 gamma/beta preload issued before the first-pass top-2 picks (latency hidden under the picks) instead of right before its wait
# baseline (speedup 1.0000x reference)
; __global__ void __launch_bounds__(NTHREADS, 2) hybrid_fwd(Args a) {
;     ...
;             for (int v = bid; v < 256; v += G) {
;                 u32x2 raw[2][8];
; #pragma unroll
;                 for (int q = 0; q < 2; ++q)
; #pragma unroll
;                     for (int j = 0; j < 8; ++j) raw[q][j] = __builtin_nontemporal_load((const u32x2*)(YB + (size_t)(v * 32 + wave + 8 * q) * DM + j * 256 + lane * 4));
;                 __syncthreads();
;                 if (tid < 16) hist[tid] = 0;
;                 __syncthreads();
;                 asm volatile("s_waitcnt vmcnt(0)" ::: "memory"); __syncthreads();
.LBB0_887:
	s_add_i32 s6, s22, s51
	s_ashr_i32 s7, s6, 31
	s_add_i32 s8, s6, 8
	s_lshl_b64 s[12:13], s[6:7], 12
	s_ashr_i32 s9, s8, 31
	v_lshl_add_u64 v[16:17], v[26:27], 0, s[12:13]
	s_lshl_b64 s[10:11], s[8:9], 12
	flat_load_dwordx2 v[58:59], v[16:17] nt
	flat_load_dwordx2 v[56:57], v[16:17] offset:512 nt
	flat_load_dwordx2 v[54:55], v[16:17] offset:1024 nt
	flat_load_dwordx2 v[52:53], v[16:17] offset:1536 nt
	flat_load_dwordx2 v[50:51], v[16:17] offset:2048 nt
	flat_load_dwordx2 v[48:49], v[16:17] offset:2560 nt
	flat_load_dwordx2 v[46:47], v[16:17] offset:3072 nt
	flat_load_dwordx2 v[44:45], v[16:17] offset:3584 nt
	v_lshl_add_u64 v[16:17], v[26:27], 0, s[10:11]
	flat_load_dwordx2 v[42:43], v[16:17] nt
	flat_load_dwordx2 v[40:41], v[16:17] offset:512 nt
	flat_load_dwordx2 v[38:39], v[16:17] offset:1024 nt
	flat_load_dwordx2 v[36:37], v[16:17] offset:1536 nt
	flat_load_dwordx2 v[22:23], v[16:17] offset:2048 nt
	flat_load_dwordx2 v[20:21], v[16:17] offset:2560 nt
	flat_load_dwordx2 v[18:19], v[16:17] offset:3072 nt
	s_nop 0
	flat_load_dwordx2 v[16:17], v[16:17] offset:3584 nt
	s_waitcnt vmcnt(0) lgkmcnt(0)
	s_barrier
	s_and_saveexec_b64 s[14:15], s[0:1]
	ds_write_b32 v156, v193
	s_or_b64 exec, exec, s[14:15]
	s_waitcnt lgkmcnt(0)
	s_barrier
	s_waitcnt vmcnt(0)
	s_add_i32 s38, s6, 16
	s_barrier
	s_mov_b64 s[14:15], s[34:35]
	v_lshlrev_b32_e32 v192, 2, v24
	s_mov_b64 s[16:17], s[36:37]
	v_lshl_add_u64 v[94:95], s[14:15], 0, v[192:193]
	v_lshlrev_b32_e32 v66, 16, v58
	v_lshl_add_u64 v[96:97], s[16:17], 0, v[192:193]
	s_nop 0
	v_and_b32_e32 v67, 0xffff0000, v58
	v_lshlrev_b32_e32 v64, 16, v59
	v_and_b32_e32 v65, 0xffff0000, v59
	v_add_f32_e32 v35, v66, v67
	v_add_f32_e32 v58, v64, v65
	v_lshlrev_b32_e32 v74, 16, v56
	v_and_b32_e32 v75, 0xffff0000, v56
	v_lshlrev_b32_e32 v72, 16, v57
	v_and_b32_e32 v73, 0xffff0000, v57
	v_add_f32_e32 v35, v35, v58
	v_add_f32_e32 v56, v74, v75
	v_add_f32_e32 v57, v72, v73
	v_lshlrev_b32_e32 v68, 16, v54
	v_and_b32_e32 v69, 0xffff0000, v54
	v_lshlrev_b32_e32 v70, 16, v55
	v_and_b32_e32 v71, 0xffff0000, v55
	v_add_f32_e32 v35, 0, v35
	v_add_f32_e32 v56, v56, v57
	v_add_f32_e32 v54, v68, v69
	v_add_f32_e32 v55, v70, v71
	v_lshlrev_b32_e32 v60, 16, v52
	v_and_b32_e32 v61, 0xffff0000, v52
	v_lshlrev_b32_e32 v62, 16, v53
	v_and_b32_e32 v63, 0xffff0000, v53
	v_add_f32_e32 v35, v35, v56
	v_add_f32_e32 v54, v54, v55
	v_add_f32_e32 v52, v60, v61
	v_add_f32_e32 v53, v62, v63
	v_add_f32_e32 v35, v35, v54
	v_add_f32_e32 v52, v52, v53
	v_lshlrev_b32_e32 v56, 16, v50
	v_and_b32_e32 v57, 0xffff0000, v50
	v_lshlrev_b32_e32 v58, 16, v51
	v_and_b32_e32 v59, 0xffff0000, v51
	v_add_f32_e32 v35, v35, v52
	v_add_f32_e32 v50, v56, v57
	v_add_f32_e32 v51, v58, v59
	v_lshlrev_b32_e32 v52, 16, v48
	v_and_b32_e32 v53, 0xffff0000, v48
	v_lshlrev_b32_e32 v54, 16, v49
	v_and_b32_e32 v55, 0xffff0000, v49
	v_add_f32_e32 v50, v50, v51
	v_add_f32_e32 v48, v52, v53
	v_add_f32_e32 v49, v54, v55
	v_add_f32_e32 v35, v35, v50
	v_add_f32_e32 v48, v48, v49
	v_add_f32_e32 v35, v35, v48
	v_lshlrev_b32_e32 v48, 16, v46
	v_and_b32_e32 v49, 0xffff0000, v46
	v_lshlrev_b32_e32 v50, 16, v47
	v_and_b32_e32 v51, 0xffff0000, v47
	v_add_f32_e32 v46, v48, v49
	v_add_f32_e32 v47, v50, v51
	v_add_f32_e32 v46, v46, v47
	v_add_f32_e32 v35, v35, v46
	v_lshlrev_b32_e32 v46, 16, v44
	v_and_b32_e32 v47, 0xffff0000, v44
	v_lshlrev_b32_e32 v44, 16, v45
	v_and_b32_e32 v45, 0xffff0000, v45
	v_add_f32_e32 v76, v46, v47
	v_add_f32_e32 v77, v44, v45
	v_add_f32_e32 v76, v76, v77
	v_add_f32_e32 v35, v35, v76
	s_lshl_b64 s[14:15], s[6:7], 11
	s_nop 0
	v_add_f32_dpp v35, v35, v35 quad_perm:[1,0,3,2] row_mask:0xf bank_mask:0xf bound_ctrl:1
	s_nop 1
	v_add_f32_dpp v35, v35, v35 quad_perm:[2,3,0,1] row_mask:0xf bank_mask:0xf bound_ctrl:1
	s_nop 1
	v_add_f32_dpp v35, v35, v35 row_ror:4 row_mask:0xf bank_mask:0xf bound_ctrl:1
	s_nop 1
	v_add_f32_dpp v35, v35, v35 row_ror:8 row_mask:0xf bank_mask:0xf bound_ctrl:1
	v_mov_b32_e32 v76, v35
	s_nop 1
	v_permlane16_swap_b32_e32 v35, v76
	v_add_f32_e32 v35, v35, v76
	v_mov_b32_e32 v76, v35
	s_nop 1
	v_permlane32_swap_b32_e32 v35, v76
	v_add_f32_e32 v35, v35, v76
	v_fmac_f32_e32 v65, 0xba000000, v35
	v_fmac_f32_e32 v67, 0xba000000, v35
	v_fmac_f32_e32 v64, 0xba000000, v35
	v_fmac_f32_e32 v66, 0xba000000, v35
	v_mul_f32_e32 v76, v67, v67
	v_mul_f32_e32 v77, v65, v65
	v_fmac_f32_e32 v76, v66, v66
	v_fmac_f32_e32 v77, v64, v64
	v_fmac_f32_e32 v73, 0xba000000, v35
	v_fmac_f32_e32 v75, 0xba000000, v35
	v_add_f32_e32 v76, v76, v77
	v_fmac_f32_e32 v72, 0xba000000, v35
	v_fmac_f32_e32 v74, 0xba000000, v35
	v_mul_f32_e32 v77, v75, v75
	v_mul_f32_e32 v78, v73, v73
	v_fmac_f32_e32 v77, v74, v74
	v_fmac_f32_e32 v78, v72, v72
	v_add_f32_e32 v77, v77, v78
	v_fmac_f32_e32 v71, 0xba000000, v35
	v_fmac_f32_e32 v69, 0xba000000, v35
	v_add_f32_e32 v76, v76, v77
	v_fmac_f32_e32 v70, 0xba000000, v35
	v_fmac_f32_e32 v68, 0xba000000, v35
	v_mul_f32_e32 v77, v69, v69
	v_mul_f32_e32 v78, v71, v71
	v_fmac_f32_e32 v77, v68, v68
	v_fmac_f32_e32 v78, v70, v70
	v_add_f32_e32 v77, v77, v78
	v_fmac_f32_e32 v63, 0xba000000, v35
	v_fmac_f32_e32 v61, 0xba000000, v35
	v_add_f32_e32 v76, v76, v77
	v_fmac_f32_e32 v62, 0xba000000, v35
	v_fmac_f32_e32 v60, 0xba000000, v35
	v_mul_f32_e32 v77, v61, v61
	v_mul_f32_e32 v78, v63, v63
	v_fmac_f32_e32 v77, v60, v60
	v_fmac_f32_e32 v78, v62, v62
	v_add_f32_e32 v77, v77, v78
	v_fmac_f32_e32 v59, 0xba000000, v35
	v_fmac_f32_e32 v57, 0xba000000, v35
	v_add_f32_e32 v76, v76, v77
	v_fmac_f32_e32 v58, 0xba000000, v35
	v_fmac_f32_e32 v56, 0xba000000, v35
	v_mul_f32_e32 v77, v57, v57
	v_mul_f32_e32 v78, v59, v59
	v_fmac_f32_e32 v77, v56, v56
	v_fmac_f32_e32 v78, v58, v58
	v_add_f32_e32 v77, v77, v78
	v_fmac_f32_e32 v55, 0xba000000, v35
	v_fmac_f32_e32 v53, 0xba000000, v35
	v_add_f32_e32 v76, v76, v77
	v_fmac_f32_e32 v54, 0xba000000, v35
	v_fmac_f32_e32 v52, 0xba000000, v35
	v_mul_f32_e32 v77, v53, v53
	v_mul_f32_e32 v78, v55, v55
	v_fmac_f32_e32 v77, v52, v52
	v_fmac_f32_e32 v78, v54, v54
	v_add_f32_e32 v77, v77, v78
	v_fmac_f32_e32 v51, 0xba000000, v35
	v_fmac_f32_e32 v49, 0xba000000, v35
	v_add_f32_e32 v76, v76, v77
	v_fmac_f32_e32 v50, 0xba000000, v35
	v_fmac_f32_e32 v48, 0xba000000, v35
	v_mul_f32_e32 v77, v49, v49
	v_mul_f32_e32 v78, v51, v51
	v_fmac_f32_e32 v77, v48, v48
	v_fmac_f32_e32 v78, v50, v50
	v_add_f32_e32 v77, v77, v78
	v_fmac_f32_e32 v45, 0xba000000, v35
	v_fmac_f32_e32 v47, 0xba000000, v35
	v_add_f32_e32 v76, v76, v77
	v_fmac_f32_e32 v44, 0xba000000, v35
	v_fmac_f32_e32 v46, 0xba000000, v35
	v_mul_f32_e32 v35, v47, v47
	v_mul_f32_e32 v77, v45, v45
	v_fmac_f32_e32 v35, v46, v46
	v_fmac_f32_e32 v77, v44, v44
	v_add_f32_e32 v35, v35, v77
	v_add_f32_e32 v35, v76, v35
	v_lshl_add_u64 v[78:79], v[30:31], 0, s[14:15]
	s_nop 0
	v_add_f32_dpp v35, v35, v35 quad_perm:[1,0,3,2] row_mask:0xf bank_mask:0xf bound_ctrl:1
	s_nop 1
	v_add_f32_dpp v35, v35, v35 quad_perm:[2,3,0,1] row_mask:0xf bank_mask:0xf bound_ctrl:1
	s_nop 1
	v_add_f32_dpp v35, v35, v35 row_ror:4 row_mask:0xf bank_mask:0xf bound_ctrl:1
	s_nop 1
	v_add_f32_dpp v35, v35, v35 row_ror:8 row_mask:0xf bank_mask:0xf bound_ctrl:1
	v_mov_b32_e32 v76, v35
	s_nop 1
	v_permlane16_swap_b32_e32 v35, v76
	v_add_f32_e32 v35, v35, v76
	v_mov_b32_e32 v76, v35
	s_nop 1
	v_permlane32_swap_b32_e32 v35, v76
	v_add_f32_e32 v35, v35, v76
	v_fmamk_f32 v35, v35, 0x3a000000, v207
	v_rsq_f32_e32 v84, v35
	v_lshl_add_u64 v[76:77], v[28:29], 0, s[12:13]
	v_pk_mul_f32 v[66:67], v[84:85], v[66:67] op_sel_hi:[0,1]
	v_pk_mul_f32 v[90:91], v[84:85], v[64:65] op_sel_hi:[0,1]
	s_waitcnt vmcnt(0) lgkmcnt(0)
	v_pk_fma_f32 v[64:65], v[158:159], v[66:67], v[198:199]
	v_mov_b32_e32 v85, 0
	v_med3_f32 v35, v64, s69, v208
	v_med3_f32 v66, v65, s69, v208
	v_cvt_pk_fp8_f32 v85, v35, v66
	v_pk_fma_f32 v[66:67], v[160:161], v[90:91], v[200:201]
	s_nop 0
	v_med3_f32 v35, v66, s69, v208
	v_med3_f32 v80, v67, s69, v208
	v_cvt_pk_fp8_f32 v85, v35, v80 op_sel:[0,0,1]
	v_cvt_pk_bf16_f32 v80, v64, v65
	v_cvt_pk_bf16_f32 v81, v66, v67
	global_store_dwordx2 v[76:77], v[80:81], off nt
	global_store_dword v[78:79], v85, off nt
	s_nop 0
	s_nop 0
	v_pk_mul_f32 v[74:75], v[84:85], v[74:75] op_sel_hi:[0,1]
	v_pk_mul_f32 v[90:91], v[84:85], v[72:73] op_sel_hi:[0,1]
	v_mov_b32_e32 v85, 0
	s_nop 0
	v_pk_fma_f32 v[72:73], v[162:163], v[74:75], v[202:203]
	s_nop 0
	v_med3_f32 v35, v72, s69, v208
	v_med3_f32 v74, v73, s69, v208
	v_cvt_pk_fp8_f32 v85, v35, v74
	v_pk_fma_f32 v[74:75], v[164:165], v[90:91], v[204:205]
	s_nop 0
	v_med3_f32 v35, v74, s69, v208
	v_med3_f32 v80, v75, s69, v208
	v_cvt_pk_fp8_f32 v85, v35, v80 op_sel:[0,0,1]
	v_cvt_pk_bf16_f32 v80, v72, v73
	v_cvt_pk_bf16_f32 v81, v74, v75
	global_store_dwordx2 v[76:77], v[80:81], off offset:512 nt
	global_store_dword v[78:79], v85, off offset:256 nt
	s_nop 0
	v_pk_mul_f32 v[68:69], v[84:85], v[68:69] op_sel_hi:[0,1]
	v_mov_b32_e32 v35, 0
	v_pk_mul_f32 v[70:71], v[84:85], v[70:71] op_sel_hi:[0,1]
	v_pk_mul_f32 v[60:61], v[84:85], v[60:61] op_sel_hi:[0,1]
	v_pk_mul_f32 v[62:63], v[84:85], v[62:63] op_sel_hi:[0,1]
	v_pk_mul_f32 v[56:57], v[84:85], v[56:57] op_sel_hi:[0,1]
	v_pk_mul_f32 v[58:59], v[84:85], v[58:59] op_sel_hi:[0,1]
	v_pk_mul_f32 v[52:53], v[84:85], v[52:53] op_sel_hi:[0,1]
	v_pk_mul_f32 v[54:55], v[84:85], v[54:55] op_sel_hi:[0,1]
	v_pk_mul_f32 v[48:49], v[84:85], v[48:49] op_sel_hi:[0,1]
	v_pk_mul_f32 v[50:51], v[84:85], v[50:51] op_sel_hi:[0,1]
	v_pk_mul_f32 v[46:47], v[84:85], v[46:47] op_sel_hi:[0,1]
	v_pk_mul_f32 v[44:45], v[84:85], v[44:45] op_sel_hi:[0,1]
	s_nop 0
	v_pk_fma_f32 v[82:83], v[166:167], v[68:69], v[216:217]
	s_nop 0
	v_med3_f32 v68, v82, s69, v208
	v_med3_f32 v69, v83, s69, v208
	v_cvt_pk_fp8_f32 v35, v68, v69
	v_pk_fma_f32 v[80:81], v[168:169], v[70:71], v[218:219]
	v_add_co_u32_e32 v90, vcc, s33, v94
	v_med3_f32 v68, v80, s69, v208
	v_med3_f32 v69, v81, s69, v208
	v_cvt_pk_fp8_f32 v35, v68, v69 op_sel:[0,0,1]
	v_cvt_pk_bf16_f32 v68, v82, v83
	v_cvt_pk_bf16_f32 v69, v80, v81
	global_store_dwordx2 v[76:77], v[68:69], off offset:1024 nt
	global_store_dword v[78:79], v35, off offset:512 nt
	s_nop 0
	s_nop 0
	v_addc_co_u32_e32 v91, vcc, 0, v95, vcc
	v_mov_b32_e32 v35, 0
	v_add_co_u32_e32 v96, vcc, s33, v96
	s_nop 0
	v_pk_fma_f32 v[94:95], v[170:171], v[60:61], v[220:221]
	s_nop 0
	v_med3_f32 v60, v94, s69, v208
	v_med3_f32 v61, v95, s69, v208
	v_cvt_pk_fp8_f32 v35, v60, v61
	v_pk_fma_f32 v[92:93], v[172:173], v[62:63], v[222:223]
	v_addc_co_u32_e32 v97, vcc, 0, v97, vcc
	v_med3_f32 v60, v92, s69, v208
	v_med3_f32 v61, v93, s69, v208
	v_cvt_pk_fp8_f32 v35, v60, v61 op_sel:[0,0,1]
	v_cvt_pk_bf16_f32 v60, v94, v95
	v_cvt_pk_bf16_f32 v61, v92, v93
	global_store_dwordx2 v[76:77], v[60:61], off offset:1536 nt
	global_store_dword v[78:79], v35, off offset:768 nt
	s_nop 0
	s_nop 0
	v_mov_b32_e32 v35, 0
	s_nop 0
	v_pk_fma_f32 v[114:115], v[174:175], v[56:57], v[224:225]
	s_nop 0
	v_med3_f32 v56, v114, s69, v208
	v_med3_f32 v57, v115, s69, v208
	v_cvt_pk_fp8_f32 v35, v56, v57
	v_pk_fma_f32 v[112:113], v[176:177], v[58:59], v[226:227]
	s_nop 0
	v_med3_f32 v56, v112, s69, v208
	v_med3_f32 v57, v113, s69, v208
	v_cvt_pk_fp8_f32 v35, v56, v57 op_sel:[0,0,1]
	v_cvt_pk_bf16_f32 v56, v114, v115
	v_cvt_pk_bf16_f32 v57, v112, v113
	global_store_dwordx2 v[76:77], v[56:57], off offset:2048 nt
	global_store_dword v[78:79], v35, off offset:1024 nt
	s_nop 0
	s_nop 0
	v_mov_b32_e32 v35, 0
	s_nop 0
	v_pk_fma_f32 v[118:119], v[178:179], v[52:53], v[228:229]
	s_nop 0
	v_med3_f32 v52, v118, s69, v208
	v_med3_f32 v53, v119, s69, v208
	v_cvt_pk_fp8_f32 v35, v52, v53
	v_pk_fma_f32 v[116:117], v[180:181], v[54:55], v[230:231]
	s_nop 0
	v_med3_f32 v52, v116, s69, v208
	v_med3_f32 v53, v117, s69, v208
	v_cvt_pk_fp8_f32 v35, v52, v53 op_sel:[0,0,1]
	v_cvt_pk_bf16_f32 v52, v118, v119
	v_cvt_pk_bf16_f32 v53, v116, v117
	global_store_dwordx2 v[76:77], v[52:53], off offset:2560 nt
	global_store_dword v[78:79], v35, off offset:1280 nt
	s_nop 0
	s_nop 0
	v_mov_b32_e32 v35, 0
	s_nop 0
	v_pk_fma_f32 v[122:123], v[182:183], v[48:49], v[232:233]
	s_nop 0
	v_med3_f32 v48, v122, s69, v208
	v_med3_f32 v49, v123, s69, v208
	v_cvt_pk_fp8_f32 v35, v48, v49
	v_pk_fma_f32 v[120:121], v[184:185], v[50:51], v[234:235]
	s_nop 0
	v_med3_f32 v48, v120, s69, v208
	v_med3_f32 v49, v121, s69, v208
	v_cvt_pk_fp8_f32 v35, v48, v49 op_sel:[0,0,1]
	v_cvt_pk_bf16_f32 v48, v122, v123
	v_cvt_pk_bf16_f32 v49, v120, v121
	global_store_dwordx2 v[76:77], v[48:49], off offset:3072 nt
	global_store_dword v[78:79], v35, off offset:1536 nt
	s_nop 0
	s_nop 0
	v_mov_b32_e32 v35, 0
	s_nop 0
	v_pk_fma_f32 v[124:125], v[186:187], v[46:47], v[246:247]
	s_nop 0
	v_med3_f32 v46, v124, s69, v208
	v_med3_f32 v47, v125, s69, v208
	v_mov_b32_e32 v48, 0
	v_cvt_pk_fp8_f32 v48, v46, v47
	v_pk_fma_f32 v[126:127], v[188:189], v[44:45], v[248:249]
	s_nop 0
	v_med3_f32 v44, v126, s69, v208
	v_med3_f32 v45, v127, s69, v208
	v_cvt_pk_fp8_f32 v48, v44, v45 op_sel:[0,0,1]
	v_cvt_pk_bf16_f32 v44, v124, v125
	v_cvt_pk_bf16_f32 v45, v126, v127
	global_store_dwordx2 v[76:77], v[44:45], off offset:3584 nt
	global_store_dword v[78:79], v48, off offset:1792 nt
	v_lshlrev_b32_e32 v84, 16, v42
	v_and_b32_e32 v85, 0xffff0000, v42
	v_lshlrev_b32_e32 v78, 16, v43
	v_and_b32_e32 v79, 0xffff0000, v43
	v_add_f32_e32 v42, v84, v85
	v_add_f32_e32 v43, v78, v79
	v_lshlrev_b32_e32 v76, 16, v40
	v_and_b32_e32 v77, 0xffff0000, v40
	v_lshlrev_b32_e32 v70, 16, v41
	v_and_b32_e32 v71, 0xffff0000, v41
	v_add_f32_e32 v42, v42, v43
	v_add_f32_e32 v40, v76, v77
	v_add_f32_e32 v41, v70, v71
	v_lshlrev_b32_e32 v62, 16, v38
	v_and_b32_e32 v63, 0xffff0000, v38
	v_lshlrev_b32_e32 v68, 16, v39
	v_and_b32_e32 v69, 0xffff0000, v39
	v_add_f32_e32 v42, 0, v42
	v_add_f32_e32 v40, v40, v41
	v_add_f32_e32 v38, v62, v63
	v_add_f32_e32 v39, v68, v69
	v_lshlrev_b32_e32 v58, 16, v36
	v_and_b32_e32 v59, 0xffff0000, v36
	v_lshlrev_b32_e32 v60, 16, v37
	v_and_b32_e32 v61, 0xffff0000, v37
	v_add_f32_e32 v40, v42, v40
	v_add_f32_e32 v38, v38, v39
	v_add_f32_e32 v36, v58, v59
	v_add_f32_e32 v37, v60, v61
	v_lshlrev_b32_e32 v50, 16, v22
	v_and_b32_e32 v51, 0xffff0000, v22
	v_lshlrev_b32_e32 v52, 16, v23
	v_and_b32_e32 v53, 0xffff0000, v23
	v_add_f32_e32 v38, v40, v38
	v_add_f32_e32 v36, v36, v37
	v_add_f32_e32 v22, v50, v51
	v_add_f32_e32 v23, v52, v53
	v_lshlrev_b32_e32 v46, 16, v20
	v_and_b32_e32 v47, 0xffff0000, v20
	v_lshlrev_b32_e32 v48, 16, v21
	v_and_b32_e32 v49, 0xffff0000, v21
	v_add_f32_e32 v36, v38, v36
	v_add_f32_e32 v22, v22, v23
	v_add_f32_e32 v20, v46, v47
	v_add_f32_e32 v21, v48, v49
	v_lshlrev_b32_e32 v40, 16, v18
	v_and_b32_e32 v41, 0xffff0000, v18
	v_lshlrev_b32_e32 v42, 16, v19
	v_and_b32_e32 v43, 0xffff0000, v19
	v_add_f32_e32 v22, v36, v22
	v_add_f32_e32 v20, v20, v21
	v_add_f32_e32 v18, v40, v41
	v_add_f32_e32 v19, v42, v43
	v_lshlrev_b32_e32 v38, 16, v16
	v_and_b32_e32 v39, 0xffff0000, v16
	v_lshlrev_b32_e32 v36, 16, v17
	v_and_b32_e32 v37, 0xffff0000, v17
	v_add_f32_e32 v20, v22, v20
	v_add_f32_e32 v18, v18, v19
	v_add_f32_e32 v16, v38, v39
	v_add_f32_e32 v17, v36, v37
	v_add_f32_e32 v18, v20, v18
	v_add_f32_e32 v16, v16, v17
	v_add_f32_e32 v16, v18, v16
	s_mov_b64 s[12:13], s[34:35]
	s_mov_b64 s[14:15], s[36:37]
	v_add_f32_dpp v16, v16, v16 quad_perm:[1,0,3,2] row_mask:0xf bank_mask:0xf bound_ctrl:1
	v_lshl_add_u64 v[100:101], s[12:13], 0, v[192:193]
	v_lshl_add_u64 v[56:57], v[28:29], 0, s[10:11]
	v_add_f32_dpp v16, v16, v16 quad_perm:[2,3,0,1] row_mask:0xf bank_mask:0xf bound_ctrl:1
	v_lshl_add_u64 v[86:87], s[14:15], 0, v[192:193]
	s_lshl_b64 s[8:9], s[8:9], 11
	v_add_f32_dpp v16, v16, v16 row_ror:4 row_mask:0xf bank_mask:0xf bound_ctrl:1
	v_lshl_add_u64 v[54:55], v[30:31], 0, s[8:9]
	s_nop 0
	v_add_f32_dpp v16, v16, v16 row_ror:8 row_mask:0xf bank_mask:0xf bound_ctrl:1
	v_mov_b32_e32 v17, v16
	s_nop 1
	v_permlane16_swap_b32_e32 v16, v17
	v_add_f32_e32 v16, v16, v17
	v_mov_b32_e32 v17, v16
	s_nop 1
	v_permlane32_swap_b32_e32 v16, v17
	v_add_f32_e32 v16, v16, v17
	v_fmac_f32_e32 v79, 0xba000000, v16
	v_fmac_f32_e32 v85, 0xba000000, v16
	v_fmac_f32_e32 v78, 0xba000000, v16
	v_fmac_f32_e32 v84, 0xba000000, v16
	v_mul_f32_e32 v17, v85, v85
	v_mul_f32_e32 v18, v79, v79
	v_fmac_f32_e32 v17, v84, v84
	v_fmac_f32_e32 v18, v78, v78
	v_fmac_f32_e32 v71, 0xba000000, v16
	v_fmac_f32_e32 v77, 0xba000000, v16
	v_add_f32_e32 v17, v17, v18
	v_fmac_f32_e32 v70, 0xba000000, v16
	v_fmac_f32_e32 v76, 0xba000000, v16
	v_mul_f32_e32 v18, v77, v77
	v_mul_f32_e32 v19, v71, v71
	v_fmac_f32_e32 v18, v76, v76
	v_fmac_f32_e32 v19, v70, v70
	v_add_f32_e32 v18, v18, v19
	v_fmac_f32_e32 v69, 0xba000000, v16
	v_fmac_f32_e32 v63, 0xba000000, v16
	v_add_f32_e32 v17, v17, v18
	v_fmac_f32_e32 v68, 0xba000000, v16
	v_fmac_f32_e32 v62, 0xba000000, v16
	v_mul_f32_e32 v18, v63, v63
	v_mul_f32_e32 v19, v69, v69
	v_fmac_f32_e32 v18, v62, v62
	v_fmac_f32_e32 v19, v68, v68
	v_add_f32_e32 v18, v18, v19
	v_fmac_f32_e32 v61, 0xba000000, v16
	v_fmac_f32_e32 v59, 0xba000000, v16
	v_add_f32_e32 v17, v17, v18
	v_fmac_f32_e32 v60, 0xba000000, v16
	v_fmac_f32_e32 v58, 0xba000000, v16
	v_mul_f32_e32 v18, v59, v59
	v_mul_f32_e32 v19, v61, v61
	v_fmac_f32_e32 v18, v58, v58
	v_fmac_f32_e32 v19, v60, v60
	v_add_f32_e32 v18, v18, v19
	v_fmac_f32_e32 v53, 0xba000000, v16
	v_fmac_f32_e32 v51, 0xba000000, v16
	v_add_f32_e32 v17, v17, v18
	v_fmac_f32_e32 v52, 0xba000000, v16
	v_fmac_f32_e32 v50, 0xba000000, v16
	v_mul_f32_e32 v18, v51, v51
	v_mul_f32_e32 v19, v53, v53
	v_fmac_f32_e32 v18, v50, v50
	v_fmac_f32_e32 v19, v52, v52
	v_add_f32_e32 v18, v18, v19
	v_fmac_f32_e32 v49, 0xba000000, v16
	v_fmac_f32_e32 v47, 0xba000000, v16
	v_add_f32_e32 v17, v17, v18
	v_fmac_f32_e32 v48, 0xba000000, v16
	v_fmac_f32_e32 v46, 0xba000000, v16
	v_mul_f32_e32 v18, v47, v47
	v_mul_f32_e32 v19, v49, v49
	v_fmac_f32_e32 v18, v46, v46
	v_fmac_f32_e32 v19, v48, v48
	v_add_f32_e32 v18, v18, v19
	v_fmac_f32_e32 v43, 0xba000000, v16
	v_fmac_f32_e32 v41, 0xba000000, v16
	v_add_f32_e32 v17, v17, v18
	v_fmac_f32_e32 v42, 0xba000000, v16
	v_fmac_f32_e32 v40, 0xba000000, v16
	v_mul_f32_e32 v18, v41, v41
	v_mul_f32_e32 v19, v43, v43
	v_fmac_f32_e32 v18, v40, v40
	v_fmac_f32_e32 v19, v42, v42
	v_add_f32_e32 v18, v18, v19
	v_fmac_f32_e32 v37, 0xba000000, v16
	v_fmac_f32_e32 v39, 0xba000000, v16
	v_add_f32_e32 v17, v17, v18
	v_fmac_f32_e32 v36, 0xba000000, v16
	v_fmac_f32_e32 v38, 0xba000000, v16
	v_mul_f32_e32 v16, v39, v39
	v_mul_f32_e32 v18, v37, v37
	v_fmac_f32_e32 v16, v38, v38
	v_fmac_f32_e32 v18, v36, v36
	v_add_f32_e32 v16, v16, v18
	v_add_f32_e32 v16, v17, v16
	s_nop 1
	v_add_f32_dpp v16, v16, v16 quad_perm:[1,0,3,2] row_mask:0xf bank_mask:0xf bound_ctrl:1
	s_nop 1
	v_add_f32_dpp v16, v16, v16 quad_perm:[2,3,0,1] row_mask:0xf bank_mask:0xf bound_ctrl:1
	s_nop 1
	v_add_f32_dpp v16, v16, v16 row_ror:4 row_mask:0xf bank_mask:0xf bound_ctrl:1
	s_nop 1
	v_add_f32_dpp v16, v16, v16 row_ror:8 row_mask:0xf bank_mask:0xf bound_ctrl:1
	v_mov_b32_e32 v17, v16
	s_nop 1
	v_permlane16_swap_b32_e32 v16, v17
	v_add_f32_e32 v16, v16, v17
	v_mov_b32_e32 v17, v16
	s_nop 1
	v_permlane32_swap_b32_e32 v16, v17
	v_add_f32_e32 v16, v16, v17
	v_fmamk_f32 v16, v16, 0x3a000000, v207
	v_rsq_f32_e32 v44, v16
	s_nop 0
	v_pk_mul_f32 v[84:85], v[44:45], v[84:85] op_sel_hi:[0,1]
	v_pk_mul_f32 v[78:79], v[44:45], v[78:79] op_sel_hi:[0,1]
	v_pk_mul_f32 v[76:77], v[44:45], v[76:77] op_sel_hi:[0,1]
	v_pk_mul_f32 v[70:71], v[44:45], v[70:71] op_sel_hi:[0,1]
	v_pk_mul_f32 v[62:63], v[44:45], v[62:63] op_sel_hi:[0,1]
	v_pk_mul_f32 v[68:69], v[44:45], v[68:69] op_sel_hi:[0,1]
	v_pk_mul_f32 v[58:59], v[44:45], v[58:59] op_sel_hi:[0,1]
	v_pk_mul_f32 v[60:61], v[44:45], v[60:61] op_sel_hi:[0,1]
	v_pk_mul_f32 v[50:51], v[44:45], v[50:51] op_sel_hi:[0,1]
	v_pk_mul_f32 v[52:53], v[44:45], v[52:53] op_sel_hi:[0,1]
	v_mov_b32_e32 v45, 0
	s_waitcnt lgkmcnt(0)
	v_pk_fma_f32 v[128:129], v[160:161], v[78:79], v[200:201]
	v_pk_fma_f32 v[130:131], v[158:159], v[84:85], v[198:199]
	v_mov_b32_e32 v20, 0
	v_cvt_pk_bf16_f32 v16, v130, v131
	v_cvt_pk_bf16_f32 v17, v128, v129
	global_store_dwordx2 v[56:57], v[16:17], off nt
	v_med3_f32 v16, v130, s69, v208
	v_med3_f32 v17, v131, s69, v208
	v_cvt_pk_fp8_f32 v20, v16, v17
	v_med3_f32 v18, v128, s69, v208
	v_med3_f32 v19, v129, s69, v208
	v_cvt_pk_fp8_f32 v20, v18, v19 op_sel:[0,0,1]
	global_store_dword v[54:55], v20, off nt
	s_nop 0
	s_nop 0
	s_nop 0
	v_pk_fma_f32 v[104:105], v[164:165], v[70:71], v[204:205]
	v_pk_fma_f32 v[106:107], v[162:163], v[76:77], v[202:203]
	v_mov_b32_e32 v20, 0
	v_cvt_pk_bf16_f32 v16, v106, v107
	v_cvt_pk_bf16_f32 v17, v104, v105
	global_store_dwordx2 v[56:57], v[16:17], off offset:512 nt
	v_med3_f32 v16, v106, s69, v208
	v_med3_f32 v17, v107, s69, v208
	v_cvt_pk_fp8_f32 v20, v16, v17
	v_med3_f32 v18, v104, s69, v208
	v_med3_f32 v19, v105, s69, v208
	v_cvt_pk_fp8_f32 v20, v18, v19 op_sel:[0,0,1]
	global_store_dword v[54:55], v20, off offset:256 nt
	s_nop 0
	s_nop 0
	s_nop 0
	v_pk_fma_f32 v[96:97], v[168:169], v[68:69], v[218:219]
	v_pk_fma_f32 v[98:99], v[166:167], v[62:63], v[216:217]
	v_mov_b32_e32 v20, 0
	v_cvt_pk_bf16_f32 v16, v98, v99
	v_cvt_pk_bf16_f32 v17, v96, v97
	global_store_dwordx2 v[56:57], v[16:17], off offset:1024 nt
	v_med3_f32 v16, v98, s69, v208
	v_med3_f32 v17, v99, s69, v208
	v_cvt_pk_fp8_f32 v20, v16, v17
	v_med3_f32 v18, v96, s69, v208
	v_med3_f32 v19, v97, s69, v208
	v_cvt_pk_fp8_f32 v20, v18, v19 op_sel:[0,0,1]
	global_store_dword v[54:55], v20, off offset:512 nt
	s_nop 0
	s_nop 0
	s_nop 0
	v_pk_fma_f32 v[88:89], v[172:173], v[60:61], v[222:223]
	v_pk_fma_f32 v[90:91], v[170:171], v[58:59], v[220:221]
	v_mov_b32_e32 v20, 0
	v_cvt_pk_bf16_f32 v16, v90, v91
	v_cvt_pk_bf16_f32 v17, v88, v89
	global_store_dwordx2 v[56:57], v[16:17], off offset:1536 nt
	v_med3_f32 v16, v90, s69, v208
	v_med3_f32 v17, v91, s69, v208
	v_cvt_pk_fp8_f32 v20, v16, v17
	v_med3_f32 v18, v88, s69, v208
	v_med3_f32 v19, v89, s69, v208
	v_add_co_u32_e32 v16, vcc, s33, v100
	v_cvt_pk_fp8_f32 v20, v18, v19 op_sel:[0,0,1]
	s_nop 0
	v_addc_co_u32_e32 v17, vcc, 0, v101, vcc
	v_add_co_u32_e32 v18, vcc, s33, v86
	global_store_dword v[54:55], v20, off offset:768 nt
	s_nop 0
	v_addc_co_u32_e32 v19, vcc, 0, v87, vcc
	s_nop 0
	s_nop 0
	v_pk_fma_f32 v[84:85], v[176:177], v[52:53], v[226:227]
	v_pk_fma_f32 v[86:87], v[174:175], v[50:51], v[224:225]
	v_med3_f32 v22, v84, s69, v208
	v_cvt_pk_bf16_f32 v20, v86, v87
	v_cvt_pk_bf16_f32 v21, v84, v85
	global_store_dwordx2 v[56:57], v[20:21], off offset:2048 nt
	v_med3_f32 v20, v86, s69, v208
	v_med3_f32 v21, v87, s69, v208
	v_cvt_pk_fp8_f32 v45, v20, v21
	v_med3_f32 v23, v85, s69, v208
; #define LAS __attribute__((address_space(3)))
; __global__ void __launch_bounds__(NTHREADS, 2) hybrid_fwd(Args a) {
;     ...
;                         for (int q = 0; q < 2; ++q)
; #pragma unroll
;                             for (int j = 0; j < 8; ++j) raw[q][j] = __builtin_nontemporal_load((const u32x2*)(YB + (size_t)(v * 32 + wave + 8 * (2 + q)) * DM + j * 256 + lane * 4));
;                         __builtin_amdgcn_sched_barrier(0);
;                     }
;                     f32x2 y2[8][4];
; #pragma unroll
;                     for (int j = 0; j < 8; ++j)
; #pragma unroll
;                         for (int c = 0; c < 4; ++c) y2[j][c] = (f32x2){ya[j][c], yb[j][c]};
;                     f32x2 acc2[16];
; #pragma unroll
;                     for (int e = 0; e < 16; ++e) acc2[e] = (f32x2){0.f, 0.f};
; #pragma unroll
;                     for (int j = 0; j < 8; ++j) {
; #pragma unroll
;                         for (int e = 0; e < 16; ++e) { const f32x4 w = *(const LAS f32x4*)(rwT + e * 2052 + j * 256 + lane * 4);
;                             acc2[e] += y2[j][0] * (f32x2){w[0], w[0]}; acc2[e] += y2[j][1] * (f32x2){w[1], w[1]};
;                             acc2[e] += y2[j][2] * (f32x2){w[2], w[2]}; acc2[e] += y2[j][3] * (f32x2){w[3], w[3]}; }
	v_cvt_pk_fp8_f32 v45, v22, v23 op_sel:[0,0,1]
	global_store_dword v[54:55], v45, off offset:1024 nt
	s_nop 0
	v_pk_mul_f32 v[46:47], v[44:45], v[46:47] op_sel_hi:[0,1]
	v_pk_mul_f32 v[48:49], v[44:45], v[48:49] op_sel_hi:[0,1]
	v_mov_b32_e32 v45, 0
	s_nop 0
	v_pk_fma_f32 v[76:77], v[180:181], v[48:49], v[230:231]
	v_pk_fma_f32 v[78:79], v[178:179], v[46:47], v[228:229]
	v_med3_f32 v22, v76, s69, v208
	v_cvt_pk_bf16_f32 v20, v78, v79
	v_cvt_pk_bf16_f32 v21, v76, v77
	global_store_dwordx2 v[56:57], v[20:21], off offset:2560 nt
	v_med3_f32 v20, v78, s69, v208
	v_med3_f32 v21, v79, s69, v208
	v_cvt_pk_fp8_f32 v45, v20, v21
	v_med3_f32 v23, v77, s69, v208
	v_cvt_pk_fp8_f32 v45, v22, v23 op_sel:[0,0,1]
	global_store_dword v[54:55], v45, off offset:1280 nt
	s_nop 0
	v_pk_mul_f32 v[40:41], v[44:45], v[40:41] op_sel_hi:[0,1]
	v_pk_mul_f32 v[42:43], v[44:45], v[42:43] op_sel_hi:[0,1]
	v_pk_mul_f32 v[38:39], v[44:45], v[38:39] op_sel_hi:[0,1]
	v_pk_mul_f32 v[36:37], v[44:45], v[36:37] op_sel_hi:[0,1]
	s_nop 0
	v_pk_fma_f32 v[68:69], v[184:185], v[42:43], v[234:235]
	v_pk_fma_f32 v[70:71], v[182:183], v[40:41], v[232:233]
	v_mov_b32_e32 v40, 0
	v_cvt_pk_bf16_f32 v20, v70, v71
	v_cvt_pk_bf16_f32 v21, v68, v69
	global_store_dwordx2 v[56:57], v[20:21], off offset:3072 nt
	v_med3_f32 v20, v70, s69, v208
	v_med3_f32 v21, v71, s69, v208
	v_cvt_pk_fp8_f32 v40, v20, v21
	v_med3_f32 v22, v68, s69, v208
	v_med3_f32 v23, v69, s69, v208
	v_cvt_pk_fp8_f32 v40, v22, v23 op_sel:[0,0,1]
	global_store_dword v[54:55], v40, off offset:1536 nt
	s_nop 0
	s_nop 0
	s_nop 0
	v_pk_fma_f32 v[60:61], v[188:189], v[36:37], v[248:249]
	v_pk_fma_f32 v[62:63], v[186:187], v[38:39], v[246:247]
	v_mov_b32_e32 v20, 0
	v_cvt_pk_bf16_f32 v16, v62, v63
	v_cvt_pk_bf16_f32 v17, v60, v61
	global_store_dwordx2 v[56:57], v[16:17], off offset:3584 nt
	v_med3_f32 v16, v62, s69, v208
	v_med3_f32 v17, v63, s69, v208
	v_cvt_pk_fp8_f32 v20, v16, v17
	v_med3_f32 v18, v60, s69, v208
	v_med3_f32 v19, v61, s69, v208
	v_cvt_pk_fp8_f32 v20, v18, v19 op_sel:[0,0,1]
	global_store_dword v[54:55], v20, off offset:1792 nt
	s_ashr_i32 s39, s38, 31
	s_add_i32 s40, s6, 24
	s_lshl_b64 s[44:45], s[38:39], 12
	s_ashr_i32 s41, s40, 31
	v_lshl_add_u64 v[16:17], v[26:27], 0, s[44:45]
	s_lshl_b64 s[42:43], s[40:41], 12
	flat_load_dwordx2 v[58:59], v[16:17] nt
	flat_load_dwordx2 v[56:57], v[16:17] offset:512 nt
	flat_load_dwordx2 v[54:55], v[16:17] offset:1024 nt
	flat_load_dwordx2 v[52:53], v[16:17] offset:1536 nt
	flat_load_dwordx2 v[50:51], v[16:17] offset:2048 nt
	flat_load_dwordx2 v[48:49], v[16:17] offset:2560 nt
	flat_load_dwordx2 v[46:47], v[16:17] offset:3072 nt
	flat_load_dwordx2 v[44:45], v[16:17] offset:3584 nt
	v_lshl_add_u64 v[16:17], v[26:27], 0, s[42:43]
	flat_load_dwordx2 v[42:43], v[16:17] nt
	flat_load_dwordx2 v[40:41], v[16:17] offset:512 nt
	flat_load_dwordx2 v[38:39], v[16:17] offset:1024 nt
	flat_load_dwordx2 v[36:37], v[16:17] offset:1536 nt
	flat_load_dwordx2 v[22:23], v[16:17] offset:2048 nt
	flat_load_dwordx2 v[20:21], v[16:17] offset:2560 nt
	flat_load_dwordx2 v[18:19], v[16:17] offset:3072 nt
	s_nop 0
	flat_load_dwordx2 v[16:17], v[16:17] offset:3584 nt
	v_add_u32_e32 v238, 0x10000, v25
	ds_read_b128 v[158:161], v25 offset:0
	ds_read_b128 v[162:165], v25 offset:8208
	ds_read_b128 v[166:169], v25 offset:16416
	ds_read_b128 v[170:173], v25 offset:24624
	ds_read_b128 v[174:177], v25 offset:32832
	ds_read_b128 v[178:181], v25 offset:41040
	ds_read_b128 v[182:185], v25 offset:49248
	ds_read_b128 v[186:189], v25 offset:57456
	v_mov_b32_e32 v100, v94
	v_mov_b32_e32 v101, v90
	v_mov_b32_e32 v90, v95
	v_mov_b32_e32 v102, v92
	v_mov_b32_e32 v103, v88
	v_mov_b32_e32 v88, v93
	v_mov_b32_e32 v92, v114
	v_mov_b32_e32 v93, v86
	v_mov_b32_e32 v86, v115
	v_mov_b32_e32 v94, v112
	v_mov_b32_e32 v95, v84
	v_mov_b32_e32 v84, v113
	ds_read_b128 v[198:201], v238 offset:128
	v_mov_b32_e32 v136, v64
	v_mov_b32_e32 v137, v130
	v_mov_b32_e32 v130, v65
	v_mov_b32_e32 v108, v82
	v_mov_b32_e32 v109, v98
	v_mov_b32_e32 v98, v83
	v_mov_b32_e32 v82, v116
	v_mov_b32_e32 v83, v76
	v_mov_b32_e32 v76, v117
	s_waitcnt lgkmcnt(8)
	v_pk_fma_f32 v[116:117], v[136:137], v[158:159], 0 op_sel_hi:[1,0,0]
	v_mov_b32_e32 v138, v66
	v_mov_b32_e32 v139, v128
	v_pk_fma_f32 v[112:113], v[158:159], v[130:131], v[116:117] op_sel:[1,0,0]
	v_mov_b32_e32 v128, v67
	v_pk_fma_f32 v[112:113], v[160:161], v[138:139], v[112:113] op_sel_hi:[0,1,1]
	v_mov_b32_e32 v114, v161
	v_pk_fma_f32 v[112:113], v[114:115], v[128:129], v[112:113] op_sel_hi:[0,1,1]
	ds_read_b128 v[202:205], v238 offset:8336
	v_mov_b32_e32 v110, v80
	v_mov_b32_e32 v111, v96
	v_mov_b32_e32 v96, v81
	v_mov_b32_e32 v80, v118
	v_mov_b32_e32 v81, v78
	v_mov_b32_e32 v78, v119
	s_waitcnt lgkmcnt(8)
	v_pk_fma_f32 v[118:119], v[136:137], v[162:163], 0 op_sel_hi:[1,0,0]
	v_mov_b32_e32 v134, v74
	v_pk_fma_f32 v[114:115], v[162:163], v[130:131], v[118:119] op_sel:[1,0,0]
	v_mov_b32_e32 v135, v104
	v_pk_fma_f32 v[114:115], v[164:165], v[138:139], v[114:115] op_sel_hi:[0,1,1]
	v_mov_b32_e32 v116, v165
	v_pk_fma_f32 v[152:153], v[116:117], v[128:129], v[114:115] op_sel_hi:[0,1,1]
	ds_read_b128 v[216:219], v238 offset:16544
	v_mov_b32_e32 v104, v75
	v_mov_b32_e32 v74, v120
	v_mov_b32_e32 v75, v68
	v_mov_b32_e32 v68, v121
	s_waitcnt lgkmcnt(8)
	v_pk_fma_f32 v[118:119], v[136:137], v[166:167], 0 op_sel_hi:[1,0,0]
	v_mov_b32_e32 v132, v72
	v_pk_fma_f32 v[114:115], v[166:167], v[130:131], v[118:119] op_sel:[1,0,0]
	v_mov_b32_e32 v133, v106
	v_pk_fma_f32 v[114:115], v[168:169], v[138:139], v[114:115] op_sel_hi:[0,1,1]
	v_mov_b32_e32 v116, v169
	v_pk_fma_f32 v[154:155], v[116:117], v[128:129], v[114:115] op_sel_hi:[0,1,1]
	ds_read_b128 v[220:223], v238 offset:24752
	v_mov_b32_e32 v106, v73
	v_mov_b32_e32 v72, v122
	v_mov_b32_e32 v73, v70
	v_mov_b32_e32 v70, v123
	s_waitcnt lgkmcnt(8)
; #define LAS __attribute__((address_space(3)))
; __global__ void __launch_bounds__(NTHREADS, 2) hybrid_fwd(Args a) {
;     ...
; #pragma unroll
;                     for (int j = 0; j < 8; ++j) {
; #pragma unroll
;                         for (int e = 0; e < 16; ++e) { const f32x4 w = *(const LAS f32x4*)(rwT + e * 2052 + j * 256 + lane * 4);
;                             acc2[e] += y2[j][0] * (f32x2){w[0], w[0]}; acc2[e] += y2[j][1] * (f32x2){w[1], w[1]};
;                             acc2[e] += y2[j][2] * (f32x2){w[2], w[2]}; acc2[e] += y2[j][3] * (f32x2){w[3], w[3]}; }
;                         __builtin_amdgcn_sched_barrier(0);
;                     }
	v_pk_fma_f32 v[118:119], v[136:137], v[170:171], 0 op_sel_hi:[1,0,0]
	v_mov_b32_e32 v66, v124
	v_pk_fma_f32 v[114:115], v[170:171], v[130:131], v[118:119] op_sel:[1,0,0]
	v_mov_b32_e32 v67, v62
	v_pk_fma_f32 v[114:115], v[172:173], v[138:139], v[114:115] op_sel_hi:[0,1,1]
	v_mov_b32_e32 v116, v173
	v_pk_fma_f32 v[114:115], v[116:117], v[128:129], v[114:115] op_sel_hi:[0,1,1]
	ds_read_b128 v[224:227], v238 offset:32960
	v_mov_b32_e32 v62, v125
	v_mov_b32_e32 v64, v126
	v_mov_b32_e32 v65, v60
	v_mov_b32_e32 v60, v127
	s_waitcnt lgkmcnt(8)
	v_pk_fma_f32 v[120:121], v[136:137], v[174:175], 0 op_sel_hi:[1,0,0]
	s_nop 0
	v_pk_fma_f32 v[116:117], v[174:175], v[130:131], v[120:121] op_sel:[1,0,0]
	s_nop 0
	v_pk_fma_f32 v[116:117], v[176:177], v[138:139], v[116:117] op_sel_hi:[0,1,1]
	v_mov_b32_e32 v118, v177
	v_pk_fma_f32 v[116:117], v[118:119], v[128:129], v[116:117] op_sel_hi:[0,1,1]
	ds_read_b128 v[228:231], v238 offset:41168
	s_waitcnt lgkmcnt(8)
	v_pk_fma_f32 v[122:123], v[136:137], v[178:179], 0 op_sel_hi:[1,0,0]
	s_nop 0
	v_pk_fma_f32 v[118:119], v[178:179], v[130:131], v[122:123] op_sel:[1,0,0]
	s_nop 0
	v_pk_fma_f32 v[118:119], v[180:181], v[138:139], v[118:119] op_sel_hi:[0,1,1]
	v_mov_b32_e32 v120, v181
	v_pk_fma_f32 v[118:119], v[120:121], v[128:129], v[118:119] op_sel_hi:[0,1,1]
	ds_read_b128 v[232:235], v238 offset:49376
	s_waitcnt lgkmcnt(8)
	v_pk_fma_f32 v[124:125], v[136:137], v[182:183], 0 op_sel_hi:[1,0,0]
	s_nop 0
	v_pk_fma_f32 v[120:121], v[182:183], v[130:131], v[124:125] op_sel:[1,0,0]
	s_nop 0
	v_pk_fma_f32 v[120:121], v[184:185], v[138:139], v[120:121] op_sel_hi:[0,1,1]
	v_mov_b32_e32 v122, v185
	v_pk_fma_f32 v[120:121], v[122:123], v[128:129], v[120:121] op_sel_hi:[0,1,1]
	ds_read_b128 v[242:245], v238 offset:57584
	s_waitcnt lgkmcnt(8)
	v_pk_fma_f32 v[126:127], v[136:137], v[186:187], 0 op_sel_hi:[1,0,0]
	s_nop 0
	v_pk_fma_f32 v[122:123], v[186:187], v[130:131], v[126:127] op_sel:[1,0,0]
	s_nop 0
	v_pk_fma_f32 v[122:123], v[188:189], v[138:139], v[122:123] op_sel_hi:[0,1,1]
	v_mov_b32_e32 v124, v189
	v_pk_fma_f32 v[122:123], v[124:125], v[128:129], v[122:123] op_sel_hi:[0,1,1]
	ds_read_b128 v[246:249], v25 offset:1024
	s_waitcnt lgkmcnt(8)
	v_pk_fma_f32 v[140:141], v[136:137], v[198:199], 0 op_sel_hi:[1,0,0]
	s_nop 0
	v_pk_fma_f32 v[124:125], v[198:199], v[130:131], v[140:141] op_sel:[1,0,0]
	ds_read_b128 v[250:253], v25 offset:9232
	v_pk_fma_f32 v[124:125], v[200:201], v[138:139], v[124:125] op_sel_hi:[0,1,1]
	v_mov_b32_e32 v126, v201
	v_pk_fma_f32 v[124:125], v[126:127], v[128:129], v[124:125] op_sel_hi:[0,1,1]
	s_waitcnt lgkmcnt(8)
	v_pk_fma_f32 v[126:127], v[136:137], v[202:203], 0 op_sel_hi:[1,0,0]
	s_nop 0
	v_pk_fma_f32 v[126:127], v[202:203], v[130:131], v[126:127] op_sel:[1,0,0]
	v_mov_b32_e32 v140, v205
	v_pk_fma_f32 v[126:127], v[204:205], v[138:139], v[126:127] op_sel_hi:[0,1,1]
	v_pk_fma_f32 v[126:127], v[140:141], v[128:129], v[126:127] op_sel_hi:[0,1,1]
	ds_read_b128 v[158:161], v25 offset:17440
	s_waitcnt lgkmcnt(8)
	v_pk_fma_f32 v[144:145], v[136:137], v[216:217], 0 op_sel_hi:[1,0,0]
	s_nop 0
	v_pk_fma_f32 v[140:141], v[216:217], v[130:131], v[144:145] op_sel:[1,0,0]
	s_nop 0
	v_pk_fma_f32 v[140:141], v[218:219], v[138:139], v[140:141] op_sel_hi:[0,1,1]
	v_mov_b32_e32 v142, v219
	v_pk_fma_f32 v[140:141], v[142:143], v[128:129], v[140:141] op_sel_hi:[0,1,1]
	ds_read_b128 v[162:165], v25 offset:25648
	s_waitcnt lgkmcnt(8)
	v_pk_fma_f32 v[146:147], v[136:137], v[220:221], 0 op_sel_hi:[1,0,0]
	s_nop 0
	v_pk_fma_f32 v[142:143], v[220:221], v[130:131], v[146:147] op_sel:[1,0,0]
	s_nop 0
	v_pk_fma_f32 v[142:143], v[222:223], v[138:139], v[142:143] op_sel_hi:[0,1,1]
	v_mov_b32_e32 v144, v223
	v_pk_fma_f32 v[142:143], v[144:145], v[128:129], v[142:143] op_sel_hi:[0,1,1]
	ds_read_b128 v[166:169], v25 offset:33856
	s_waitcnt lgkmcnt(8)
	v_pk_fma_f32 v[148:149], v[136:137], v[224:225], 0 op_sel_hi:[1,0,0]
	s_nop 0
	v_pk_fma_f32 v[144:145], v[224:225], v[130:131], v[148:149] op_sel:[1,0,0]
	s_nop 0
	v_pk_fma_f32 v[144:145], v[226:227], v[138:139], v[144:145] op_sel_hi:[0,1,1]
	v_mov_b32_e32 v146, v227
	v_pk_fma_f32 v[144:145], v[146:147], v[128:129], v[144:145] op_sel_hi:[0,1,1]
	ds_read_b128 v[170:173], v25 offset:42064
	s_waitcnt lgkmcnt(8)
	v_pk_fma_f32 v[150:151], v[136:137], v[228:229], 0 op_sel_hi:[1,0,0]
	s_nop 0
	v_pk_fma_f32 v[146:147], v[228:229], v[130:131], v[150:151] op_sel:[1,0,0]
	s_nop 0
	v_pk_fma_f32 v[146:147], v[230:231], v[138:139], v[146:147] op_sel_hi:[0,1,1]
	v_mov_b32_e32 v148, v231
	v_pk_fma_f32 v[146:147], v[148:149], v[128:129], v[146:147] op_sel_hi:[0,1,1]
	ds_read_b128 v[174:177], v25 offset:50272
	s_waitcnt lgkmcnt(8)
	v_pk_fma_f32 v[194:195], v[136:137], v[232:233], 0 op_sel_hi:[1,0,0]
	s_nop 0
	v_pk_fma_f32 v[148:149], v[232:233], v[130:131], v[194:195] op_sel:[1,0,0]
	ds_read_b128 v[178:181], v25 offset:58480
	v_pk_fma_f32 v[148:149], v[234:235], v[138:139], v[148:149] op_sel_hi:[0,1,1]
	v_mov_b32_e32 v150, v235
	v_pk_fma_f32 v[148:149], v[150:151], v[128:129], v[148:149] op_sel_hi:[0,1,1]
	s_waitcnt lgkmcnt(8)
	v_pk_fma_f32 v[136:137], v[136:137], v[242:243], 0 op_sel_hi:[1,0,0]
	s_nop 0
	v_pk_fma_f32 v[130:131], v[242:243], v[130:131], v[136:137] op_sel:[1,0,0]
	v_mov_b32_e32 v136, v245
	v_pk_fma_f32 v[130:131], v[244:245], v[138:139], v[130:131] op_sel_hi:[0,1,1]
	v_pk_fma_f32 v[150:151], v[136:137], v[128:129], v[130:131] op_sel_hi:[0,1,1]
	ds_read_b128 v[182:185], v238 offset:1152
	s_waitcnt lgkmcnt(8)
; #define LAS __attribute__((address_space(3)))
; __global__ void __launch_bounds__(NTHREADS, 2) hybrid_fwd(Args a) {
;     ...
; #pragma unroll
;                     for (int j = 0; j < 8; ++j) {
; #pragma unroll
;                         for (int e = 0; e < 16; ++e) { const f32x4 w = *(const LAS f32x4*)(rwT + e * 2052 + j * 256 + lane * 4);
;                             acc2[e] += y2[j][0] * (f32x2){w[0], w[0]}; acc2[e] += y2[j][1] * (f32x2){w[1], w[1]};
;                             acc2[e] += y2[j][2] * (f32x2){w[2], w[2]}; acc2[e] += y2[j][3] * (f32x2){w[3], w[3]}; }
;                         __builtin_amdgcn_sched_barrier(0);
;                     }
	v_pk_fma_f32 v[112:113], v[132:133], v[246:247], v[112:113] op_sel_hi:[1,0,1]
	s_nop 0
	v_pk_fma_f32 v[112:113], v[246:247], v[106:107], v[112:113] op_sel:[1,0,0]
	v_mov_b32_e32 v128, v249
	v_pk_fma_f32 v[112:113], v[248:249], v[134:135], v[112:113] op_sel_hi:[0,1,1]
	v_pk_fma_f32 v[112:113], v[128:129], v[104:105], v[112:113] op_sel_hi:[0,1,1]
	ds_read_b128 v[186:189], v238 offset:9360
	s_waitcnt lgkmcnt(8)
	v_pk_fma_f32 v[136:137], v[132:133], v[250:251], v[152:153] op_sel_hi:[1,0,1]
	s_nop 0
	v_pk_fma_f32 v[128:129], v[250:251], v[106:107], v[136:137] op_sel:[1,0,0]
	s_nop 0
	v_pk_fma_f32 v[128:129], v[252:253], v[134:135], v[128:129] op_sel_hi:[0,1,1]
	v_mov_b32_e32 v130, v253
	v_pk_fma_f32 v[152:153], v[130:131], v[104:105], v[128:129] op_sel_hi:[0,1,1]
	ds_read_b128 v[198:201], v238 offset:17568
	s_waitcnt lgkmcnt(8)
	v_pk_fma_f32 v[136:137], v[132:133], v[158:159], v[154:155] op_sel_hi:[1,0,1]
	s_nop 0
	v_pk_fma_f32 v[128:129], v[158:159], v[106:107], v[136:137] op_sel:[1,0,0]
	ds_read_b128 v[202:205], v238 offset:25776
	v_pk_fma_f32 v[128:129], v[160:161], v[134:135], v[128:129] op_sel_hi:[0,1,1]
	v_mov_b32_e32 v130, v161
	v_pk_fma_f32 v[128:129], v[130:131], v[104:105], v[128:129] op_sel_hi:[0,1,1]
	s_waitcnt lgkmcnt(8)
	v_pk_fma_f32 v[114:115], v[132:133], v[162:163], v[114:115] op_sel_hi:[1,0,1]
	s_nop 0
	v_pk_fma_f32 v[114:115], v[162:163], v[106:107], v[114:115] op_sel:[1,0,0]
	v_mov_b32_e32 v130, v165
	v_pk_fma_f32 v[114:115], v[164:165], v[134:135], v[114:115] op_sel_hi:[0,1,1]
	ds_read_b128 v[216:219], v238 offset:33984
	v_pk_fma_f32 v[114:115], v[130:131], v[104:105], v[114:115] op_sel_hi:[0,1,1]
	s_waitcnt lgkmcnt(8)
	v_pk_fma_f32 v[116:117], v[132:133], v[166:167], v[116:117] op_sel_hi:[1,0,1]
	s_nop 0
	v_pk_fma_f32 v[116:117], v[166:167], v[106:107], v[116:117] op_sel:[1,0,0]
	v_mov_b32_e32 v130, v169
	v_pk_fma_f32 v[116:117], v[168:169], v[134:135], v[116:117] op_sel_hi:[0,1,1]
	ds_read_b128 v[220:223], v238 offset:42192
	v_pk_fma_f32 v[116:117], v[130:131], v[104:105], v[116:117] op_sel_hi:[0,1,1]
	s_waitcnt lgkmcnt(8)
	v_pk_fma_f32 v[118:119], v[132:133], v[170:171], v[118:119] op_sel_hi:[1,0,1]
	s_nop 0
	v_pk_fma_f32 v[118:119], v[170:171], v[106:107], v[118:119] op_sel:[1,0,0]
	v_mov_b32_e32 v130, v173
	v_pk_fma_f32 v[118:119], v[172:173], v[134:135], v[118:119] op_sel_hi:[0,1,1]
	ds_read_b128 v[224:227], v238 offset:50400
	v_pk_fma_f32 v[118:119], v[130:131], v[104:105], v[118:119] op_sel_hi:[0,1,1]
	s_waitcnt lgkmcnt(8)
	v_pk_fma_f32 v[120:121], v[132:133], v[174:175], v[120:121] op_sel_hi:[1,0,1]
	s_nop 0
	v_pk_fma_f32 v[120:121], v[174:175], v[106:107], v[120:121] op_sel:[1,0,0]
	v_mov_b32_e32 v130, v177
	v_pk_fma_f32 v[120:121], v[176:177], v[134:135], v[120:121] op_sel_hi:[0,1,1]
	ds_read_b128 v[228:231], v238 offset:58608
	v_pk_fma_f32 v[120:121], v[130:131], v[104:105], v[120:121] op_sel_hi:[0,1,1]
	s_waitcnt lgkmcnt(8)
	v_pk_fma_f32 v[122:123], v[132:133], v[178:179], v[122:123] op_sel_hi:[1,0,1]
	s_nop 0
	v_pk_fma_f32 v[122:123], v[178:179], v[106:107], v[122:123] op_sel:[1,0,0]
	v_mov_b32_e32 v130, v181
	v_pk_fma_f32 v[122:123], v[180:181], v[134:135], v[122:123] op_sel_hi:[0,1,1]
	ds_read_b128 v[232:235], v25 offset:2048
	v_pk_fma_f32 v[122:123], v[130:131], v[104:105], v[122:123] op_sel_hi:[0,1,1]
	s_waitcnt lgkmcnt(8)
	v_pk_fma_f32 v[124:125], v[132:133], v[182:183], v[124:125] op_sel_hi:[1,0,1]
	s_nop 0
	v_pk_fma_f32 v[124:125], v[182:183], v[106:107], v[124:125] op_sel:[1,0,0]
	v_mov_b32_e32 v130, v185
	v_pk_fma_f32 v[124:125], v[184:185], v[134:135], v[124:125] op_sel_hi:[0,1,1]
	ds_read_b128 v[242:245], v25 offset:10256
	v_pk_fma_f32 v[124:125], v[130:131], v[104:105], v[124:125] op_sel_hi:[0,1,1]
	s_waitcnt lgkmcnt(8)
	v_pk_fma_f32 v[126:127], v[132:133], v[186:187], v[126:127] op_sel_hi:[1,0,1]
	s_nop 0
	v_pk_fma_f32 v[126:127], v[186:187], v[106:107], v[126:127] op_sel:[1,0,0]
	v_mov_b32_e32 v130, v189
	v_pk_fma_f32 v[126:127], v[188:189], v[134:135], v[126:127] op_sel_hi:[0,1,1]
	ds_read_b128 v[246:249], v25 offset:18464
	v_pk_fma_f32 v[126:127], v[130:131], v[104:105], v[126:127] op_sel_hi:[0,1,1]
	s_waitcnt lgkmcnt(8)
	v_pk_fma_f32 v[130:131], v[132:133], v[198:199], v[140:141] op_sel_hi:[1,0,1]
	s_nop 0
	v_pk_fma_f32 v[130:131], v[198:199], v[106:107], v[130:131] op_sel:[1,0,0]
	v_mov_b32_e32 v136, v201
	v_pk_fma_f32 v[130:131], v[200:201], v[134:135], v[130:131] op_sel_hi:[0,1,1]
	v_pk_fma_f32 v[130:131], v[136:137], v[104:105], v[130:131] op_sel_hi:[0,1,1]
	ds_read_b128 v[250:253], v25 offset:26672
	s_waitcnt lgkmcnt(8)
	v_pk_fma_f32 v[140:141], v[132:133], v[202:203], v[142:143] op_sel_hi:[1,0,1]
	s_nop 0
	v_pk_fma_f32 v[136:137], v[202:203], v[106:107], v[140:141] op_sel:[1,0,0]
	s_nop 0
	v_pk_fma_f32 v[136:137], v[204:205], v[134:135], v[136:137] op_sel_hi:[0,1,1]
	v_mov_b32_e32 v138, v205
	v_pk_fma_f32 v[136:137], v[138:139], v[104:105], v[136:137] op_sel_hi:[0,1,1]
	ds_read_b128 v[162:165], v25 offset:34880
	s_waitcnt lgkmcnt(8)
	v_pk_fma_f32 v[142:143], v[132:133], v[216:217], v[144:145] op_sel_hi:[1,0,1]
	s_nop 0
	v_pk_fma_f32 v[138:139], v[216:217], v[106:107], v[142:143] op_sel:[1,0,0]
	s_nop 0
	v_pk_fma_f32 v[138:139], v[218:219], v[134:135], v[138:139] op_sel_hi:[0,1,1]
	v_mov_b32_e32 v140, v219
	v_pk_fma_f32 v[138:139], v[140:141], v[104:105], v[138:139] op_sel_hi:[0,1,1]
	ds_read_b128 v[166:169], v25 offset:43088
	s_waitcnt lgkmcnt(8)
	v_pk_fma_f32 v[144:145], v[132:133], v[220:221], v[146:147] op_sel_hi:[1,0,1]
	s_nop 0
	v_pk_fma_f32 v[140:141], v[220:221], v[106:107], v[144:145] op_sel:[1,0,0]
	s_nop 0
	v_pk_fma_f32 v[140:141], v[222:223], v[134:135], v[140:141] op_sel_hi:[0,1,1]
	v_mov_b32_e32 v142, v223
	v_pk_fma_f32 v[140:141], v[142:143], v[104:105], v[140:141] op_sel_hi:[0,1,1]
	ds_read_b128 v[170:173], v25 offset:51296
	s_waitcnt lgkmcnt(8)
; #define LAS __attribute__((address_space(3)))
; __global__ void __launch_bounds__(NTHREADS, 2) hybrid_fwd(Args a) {
;     ...
; #pragma unroll
;                     for (int j = 0; j < 8; ++j) {
; #pragma unroll
;                         for (int e = 0; e < 16; ++e) { const f32x4 w = *(const LAS f32x4*)(rwT + e * 2052 + j * 256 + lane * 4);
;                             acc2[e] += y2[j][0] * (f32x2){w[0], w[0]}; acc2[e] += y2[j][1] * (f32x2){w[1], w[1]};
;                             acc2[e] += y2[j][2] * (f32x2){w[2], w[2]}; acc2[e] += y2[j][3] * (f32x2){w[3], w[3]}; }
;                         __builtin_amdgcn_sched_barrier(0);
;                     }
	v_pk_fma_f32 v[146:147], v[132:133], v[224:225], v[148:149] op_sel_hi:[1,0,1]
	s_nop 0
	v_pk_fma_f32 v[142:143], v[224:225], v[106:107], v[146:147] op_sel:[1,0,0]
	s_nop 0
	v_pk_fma_f32 v[142:143], v[226:227], v[134:135], v[142:143] op_sel_hi:[0,1,1]
	v_mov_b32_e32 v144, v227
	v_pk_fma_f32 v[142:143], v[144:145], v[104:105], v[142:143] op_sel_hi:[0,1,1]
	ds_read_b128 v[174:177], v25 offset:59504
	s_waitcnt lgkmcnt(8)
	v_pk_fma_f32 v[132:133], v[132:133], v[228:229], v[150:151] op_sel_hi:[1,0,1]
	s_nop 0
	v_pk_fma_f32 v[106:107], v[228:229], v[106:107], v[132:133] op_sel:[1,0,0]
	v_mov_b32_e32 v132, v231
	v_pk_fma_f32 v[106:107], v[230:231], v[134:135], v[106:107] op_sel_hi:[0,1,1]
	v_pk_fma_f32 v[144:145], v[132:133], v[104:105], v[106:107] op_sel_hi:[0,1,1]
	ds_read_b128 v[178:181], v238 offset:2176
	ds_read_b128 v[182:185], v238 offset:10384
	s_waitcnt lgkmcnt(8)
	v_pk_fma_f32 v[112:113], v[108:109], v[232:233], v[112:113] op_sel_hi:[1,0,1]
	s_nop 0
	v_pk_fma_f32 v[104:105], v[232:233], v[98:99], v[112:113] op_sel:[1,0,0]
	v_mov_b32_e32 v112, v245
	v_pk_fma_f32 v[104:105], v[234:235], v[110:111], v[104:105] op_sel_hi:[0,1,1]
	v_mov_b32_e32 v106, v235
	v_pk_fma_f32 v[104:105], v[106:107], v[96:97], v[104:105] op_sel_hi:[0,1,1]
	v_pk_fma_f32 v[106:107], v[108:109], v[242:243], v[152:153] op_sel_hi:[1,0,1]
	s_nop 0
	v_pk_fma_f32 v[106:107], v[242:243], v[98:99], v[106:107] op_sel:[1,0,0]
	s_nop 0
	v_pk_fma_f32 v[106:107], v[244:245], v[110:111], v[106:107] op_sel_hi:[0,1,1]
	ds_read_b128 v[186:189], v238 offset:18592
	v_pk_fma_f32 v[146:147], v[112:113], v[96:97], v[106:107] op_sel_hi:[0,1,1]
	s_waitcnt lgkmcnt(8)
	v_pk_fma_f32 v[106:107], v[108:109], v[246:247], v[128:129] op_sel_hi:[1,0,1]
	s_nop 0
	v_pk_fma_f32 v[106:107], v[246:247], v[98:99], v[106:107] op_sel:[1,0,0]
	v_mov_b32_e32 v112, v249
	v_pk_fma_f32 v[106:107], v[248:249], v[110:111], v[106:107] op_sel_hi:[0,1,1]
	ds_read_b128 v[158:161], v238 offset:26800
	v_pk_fma_f32 v[106:107], v[112:113], v[96:97], v[106:107] op_sel_hi:[0,1,1]
	s_waitcnt lgkmcnt(8)
	v_pk_fma_f32 v[112:113], v[108:109], v[250:251], v[114:115] op_sel_hi:[1,0,1]
	s_nop 0
	v_pk_fma_f32 v[112:113], v[250:251], v[98:99], v[112:113] op_sel:[1,0,0]
	v_mov_b32_e32 v114, v253
	v_pk_fma_f32 v[112:113], v[252:253], v[110:111], v[112:113] op_sel_hi:[0,1,1]
	ds_read_b128 v[198:201], v238 offset:35008
	v_pk_fma_f32 v[112:113], v[114:115], v[96:97], v[112:113] op_sel_hi:[0,1,1]
	s_waitcnt lgkmcnt(8)
	v_pk_fma_f32 v[114:115], v[108:109], v[162:163], v[116:117] op_sel_hi:[1,0,1]
	s_nop 0
	v_pk_fma_f32 v[114:115], v[162:163], v[98:99], v[114:115] op_sel:[1,0,0]
	v_mov_b32_e32 v116, v165
	v_pk_fma_f32 v[114:115], v[164:165], v[110:111], v[114:115] op_sel_hi:[0,1,1]
	ds_read_b128 v[202:205], v238 offset:43216
	v_pk_fma_f32 v[114:115], v[116:117], v[96:97], v[114:115] op_sel_hi:[0,1,1]
	s_waitcnt lgkmcnt(8)
	v_pk_fma_f32 v[116:117], v[108:109], v[166:167], v[118:119] op_sel_hi:[1,0,1]
	s_nop 0
	v_pk_fma_f32 v[116:117], v[166:167], v[98:99], v[116:117] op_sel:[1,0,0]
	v_mov_b32_e32 v118, v169
	v_pk_fma_f32 v[116:117], v[168:169], v[110:111], v[116:117] op_sel_hi:[0,1,1]
	ds_read_b128 v[216:219], v238 offset:51424
	v_pk_fma_f32 v[116:117], v[118:119], v[96:97], v[116:117] op_sel_hi:[0,1,1]
	s_waitcnt lgkmcnt(8)
	v_pk_fma_f32 v[118:119], v[108:109], v[170:171], v[120:121] op_sel_hi:[1,0,1]
	s_nop 0
	v_pk_fma_f32 v[118:119], v[170:171], v[98:99], v[118:119] op_sel:[1,0,0]
	v_mov_b32_e32 v120, v173
	v_pk_fma_f32 v[118:119], v[172:173], v[110:111], v[118:119] op_sel_hi:[0,1,1]
	ds_read_b128 v[220:223], v238 offset:59632
	v_pk_fma_f32 v[118:119], v[120:121], v[96:97], v[118:119] op_sel_hi:[0,1,1]
	s_waitcnt lgkmcnt(8)
	v_pk_fma_f32 v[120:121], v[108:109], v[174:175], v[122:123] op_sel_hi:[1,0,1]
	s_nop 0
	v_pk_fma_f32 v[120:121], v[174:175], v[98:99], v[120:121] op_sel:[1,0,0]
	v_mov_b32_e32 v122, v177
	v_pk_fma_f32 v[120:121], v[176:177], v[110:111], v[120:121] op_sel_hi:[0,1,1]
	ds_read_b128 v[224:227], v25 offset:3072
	v_pk_fma_f32 v[120:121], v[122:123], v[96:97], v[120:121] op_sel_hi:[0,1,1]
	s_waitcnt lgkmcnt(8)
	v_pk_fma_f32 v[122:123], v[108:109], v[178:179], v[124:125] op_sel_hi:[1,0,1]
	s_nop 0
	v_pk_fma_f32 v[122:123], v[178:179], v[98:99], v[122:123] op_sel:[1,0,0]
	v_mov_b32_e32 v124, v181
	v_pk_fma_f32 v[122:123], v[180:181], v[110:111], v[122:123] op_sel_hi:[0,1,1]
	ds_read_b128 v[228:231], v25 offset:11280
	v_pk_fma_f32 v[122:123], v[124:125], v[96:97], v[122:123] op_sel_hi:[0,1,1]
	s_waitcnt lgkmcnt(8)
	v_pk_fma_f32 v[124:125], v[108:109], v[182:183], v[126:127] op_sel_hi:[1,0,1]
	s_nop 0
	v_pk_fma_f32 v[124:125], v[182:183], v[98:99], v[124:125] op_sel:[1,0,0]
	v_mov_b32_e32 v126, v185
	v_pk_fma_f32 v[124:125], v[184:185], v[110:111], v[124:125] op_sel_hi:[0,1,1]
	v_pk_fma_f32 v[124:125], v[126:127], v[96:97], v[124:125] op_sel_hi:[0,1,1]
	ds_read_b128 v[232:235], v25 offset:19488
	s_waitcnt lgkmcnt(8)
	v_pk_fma_f32 v[130:131], v[108:109], v[186:187], v[130:131] op_sel_hi:[1,0,1]
	s_nop 0
	v_pk_fma_f32 v[126:127], v[186:187], v[98:99], v[130:131] op_sel:[1,0,0]
	s_nop 0
	v_pk_fma_f32 v[126:127], v[188:189], v[110:111], v[126:127] op_sel_hi:[0,1,1]
	v_mov_b32_e32 v128, v189
	v_pk_fma_f32 v[126:127], v[128:129], v[96:97], v[126:127] op_sel_hi:[0,1,1]
	ds_read_b128 v[242:245], v25 offset:27696
	s_waitcnt lgkmcnt(8)
	v_pk_fma_f32 v[132:133], v[108:109], v[158:159], v[136:137] op_sel_hi:[1,0,1]
	s_nop 0
	v_pk_fma_f32 v[128:129], v[158:159], v[98:99], v[132:133] op_sel:[1,0,0]
	s_nop 0
	v_pk_fma_f32 v[128:129], v[160:161], v[110:111], v[128:129] op_sel_hi:[0,1,1]
	v_mov_b32_e32 v130, v161
	v_pk_fma_f32 v[128:129], v[130:131], v[96:97], v[128:129] op_sel_hi:[0,1,1]
	ds_read_b128 v[246:249], v25 offset:35904
	s_waitcnt lgkmcnt(8)
; #define LAS __attribute__((address_space(3)))
; __global__ void __launch_bounds__(NTHREADS, 2) hybrid_fwd(Args a) {
;     ...
; #pragma unroll
;                     for (int j = 0; j < 8; ++j) {
; #pragma unroll
;                         for (int e = 0; e < 16; ++e) { const f32x4 w = *(const LAS f32x4*)(rwT + e * 2052 + j * 256 + lane * 4);
;                             acc2[e] += y2[j][0] * (f32x2){w[0], w[0]}; acc2[e] += y2[j][1] * (f32x2){w[1], w[1]};
;                             acc2[e] += y2[j][2] * (f32x2){w[2], w[2]}; acc2[e] += y2[j][3] * (f32x2){w[3], w[3]}; }
;                         __builtin_amdgcn_sched_barrier(0);
;                     }
	v_pk_fma_f32 v[134:135], v[108:109], v[198:199], v[138:139] op_sel_hi:[1,0,1]
	s_nop 0
	v_pk_fma_f32 v[130:131], v[198:199], v[98:99], v[134:135] op_sel:[1,0,0]
	s_nop 0
	v_pk_fma_f32 v[130:131], v[200:201], v[110:111], v[130:131] op_sel_hi:[0,1,1]
	v_mov_b32_e32 v132, v201
	v_pk_fma_f32 v[130:131], v[132:133], v[96:97], v[130:131] op_sel_hi:[0,1,1]
	ds_read_b128 v[250:253], v25 offset:44112
	s_waitcnt lgkmcnt(8)
	v_pk_fma_f32 v[136:137], v[108:109], v[202:203], v[140:141] op_sel_hi:[1,0,1]
	s_nop 0
	v_pk_fma_f32 v[132:133], v[202:203], v[98:99], v[136:137] op_sel:[1,0,0]
	s_nop 0
	v_pk_fma_f32 v[132:133], v[204:205], v[110:111], v[132:133] op_sel_hi:[0,1,1]
	v_mov_b32_e32 v134, v205
	v_pk_fma_f32 v[132:133], v[134:135], v[96:97], v[132:133] op_sel_hi:[0,1,1]
	ds_read_b128 v[162:165], v25 offset:52320
	s_waitcnt lgkmcnt(8)
	v_pk_fma_f32 v[138:139], v[108:109], v[216:217], v[142:143] op_sel_hi:[1,0,1]
	s_nop 0
	v_pk_fma_f32 v[134:135], v[216:217], v[98:99], v[138:139] op_sel:[1,0,0]
	s_nop 0
	v_pk_fma_f32 v[134:135], v[218:219], v[110:111], v[134:135] op_sel_hi:[0,1,1]
	v_mov_b32_e32 v136, v219
	v_pk_fma_f32 v[134:135], v[136:137], v[96:97], v[134:135] op_sel_hi:[0,1,1]
	ds_read_b128 v[166:169], v25 offset:60528
	s_waitcnt lgkmcnt(8)
	v_pk_fma_f32 v[108:109], v[108:109], v[220:221], v[144:145] op_sel_hi:[1,0,1]
	s_nop 0
	v_pk_fma_f32 v[98:99], v[220:221], v[98:99], v[108:109] op_sel:[1,0,0]
	v_mov_b32_e32 v108, v223
	v_pk_fma_f32 v[98:99], v[222:223], v[110:111], v[98:99] op_sel_hi:[0,1,1]
	v_pk_fma_f32 v[136:137], v[108:109], v[96:97], v[98:99] op_sel_hi:[0,1,1]
	ds_read_b128 v[170:173], v238 offset:3200
	ds_read_b128 v[174:177], v238 offset:11408
	s_waitcnt lgkmcnt(8)
	v_pk_fma_f32 v[104:105], v[100:101], v[224:225], v[104:105] op_sel_hi:[1,0,1]
	s_nop 0
	v_pk_fma_f32 v[96:97], v[224:225], v[90:91], v[104:105] op_sel:[1,0,0]
	v_mov_b32_e32 v104, v231
	v_pk_fma_f32 v[96:97], v[226:227], v[102:103], v[96:97] op_sel_hi:[0,1,1]
	v_mov_b32_e32 v98, v227
	v_pk_fma_f32 v[96:97], v[98:99], v[88:89], v[96:97] op_sel_hi:[0,1,1]
	v_pk_fma_f32 v[98:99], v[100:101], v[228:229], v[146:147] op_sel_hi:[1,0,1]
	s_nop 0
	v_pk_fma_f32 v[98:99], v[228:229], v[90:91], v[98:99] op_sel:[1,0,0]
	s_nop 0
	v_pk_fma_f32 v[98:99], v[230:231], v[102:103], v[98:99] op_sel_hi:[0,1,1]
	ds_read_b128 v[178:181], v238 offset:19616
	v_pk_fma_f32 v[138:139], v[104:105], v[88:89], v[98:99] op_sel_hi:[0,1,1]
	s_waitcnt lgkmcnt(8)
	v_pk_fma_f32 v[98:99], v[100:101], v[232:233], v[106:107] op_sel_hi:[1,0,1]
	s_nop 0
	v_pk_fma_f32 v[98:99], v[232:233], v[90:91], v[98:99] op_sel:[1,0,0]
	v_mov_b32_e32 v104, v235
	v_pk_fma_f32 v[98:99], v[234:235], v[102:103], v[98:99] op_sel_hi:[0,1,1]
	v_pk_fma_f32 v[98:99], v[104:105], v[88:89], v[98:99] op_sel_hi:[0,1,1]
	ds_read_b128 v[182:185], v238 offset:27824
	s_waitcnt lgkmcnt(8)
	v_pk_fma_f32 v[108:109], v[100:101], v[242:243], v[112:113] op_sel_hi:[1,0,1]
	s_nop 0
	v_pk_fma_f32 v[104:105], v[242:243], v[90:91], v[108:109] op_sel:[1,0,0]
	s_nop 0
	v_pk_fma_f32 v[104:105], v[244:245], v[102:103], v[104:105] op_sel_hi:[0,1,1]
	v_mov_b32_e32 v106, v245
	v_pk_fma_f32 v[104:105], v[106:107], v[88:89], v[104:105] op_sel_hi:[0,1,1]
	ds_read_b128 v[186:189], v238 offset:36032
	s_waitcnt lgkmcnt(8)
	v_pk_fma_f32 v[110:111], v[100:101], v[246:247], v[114:115] op_sel_hi:[1,0,1]
	s_nop 0
	v_pk_fma_f32 v[106:107], v[246:247], v[90:91], v[110:111] op_sel:[1,0,0]
	s_nop 0
	v_pk_fma_f32 v[106:107], v[248:249], v[102:103], v[106:107] op_sel_hi:[0,1,1]
	v_mov_b32_e32 v108, v249
	v_pk_fma_f32 v[106:107], v[108:109], v[88:89], v[106:107] op_sel_hi:[0,1,1]
	ds_read_b128 v[158:161], v238 offset:44240
	s_waitcnt lgkmcnt(8)
	v_pk_fma_f32 v[112:113], v[100:101], v[250:251], v[116:117] op_sel_hi:[1,0,1]
	s_nop 0
	v_pk_fma_f32 v[108:109], v[250:251], v[90:91], v[112:113] op_sel:[1,0,0]
	s_nop 0
	v_pk_fma_f32 v[108:109], v[252:253], v[102:103], v[108:109] op_sel_hi:[0,1,1]
	v_mov_b32_e32 v110, v253
	v_pk_fma_f32 v[108:109], v[110:111], v[88:89], v[108:109] op_sel_hi:[0,1,1]
	ds_read_b128 v[198:201], v238 offset:52448
	s_waitcnt lgkmcnt(8)
	v_pk_fma_f32 v[114:115], v[100:101], v[162:163], v[118:119] op_sel_hi:[1,0,1]
	s_nop 0
	v_pk_fma_f32 v[110:111], v[162:163], v[90:91], v[114:115] op_sel:[1,0,0]
	s_nop 0
	v_pk_fma_f32 v[110:111], v[164:165], v[102:103], v[110:111] op_sel_hi:[0,1,1]
	v_mov_b32_e32 v112, v165
	v_pk_fma_f32 v[110:111], v[112:113], v[88:89], v[110:111] op_sel_hi:[0,1,1]
	ds_read_b128 v[202:205], v238 offset:60656
	s_waitcnt lgkmcnt(8)
	v_pk_fma_f32 v[116:117], v[100:101], v[166:167], v[120:121] op_sel_hi:[1,0,1]
	s_nop 0
	v_pk_fma_f32 v[112:113], v[166:167], v[90:91], v[116:117] op_sel:[1,0,0]
	s_nop 0
	v_pk_fma_f32 v[112:113], v[168:169], v[102:103], v[112:113] op_sel_hi:[0,1,1]
	v_mov_b32_e32 v114, v169
	v_pk_fma_f32 v[112:113], v[114:115], v[88:89], v[112:113] op_sel_hi:[0,1,1]
	ds_read_b128 v[216:219], v25 offset:4096
	s_waitcnt lgkmcnt(8)
	v_pk_fma_f32 v[118:119], v[100:101], v[170:171], v[122:123] op_sel_hi:[1,0,1]
	s_nop 0
	v_pk_fma_f32 v[114:115], v[170:171], v[90:91], v[118:119] op_sel:[1,0,0]
	s_nop 0
	v_pk_fma_f32 v[114:115], v[172:173], v[102:103], v[114:115] op_sel_hi:[0,1,1]
	v_mov_b32_e32 v116, v173
	v_pk_fma_f32 v[114:115], v[116:117], v[88:89], v[114:115] op_sel_hi:[0,1,1]
	ds_read_b128 v[220:223], v25 offset:12304
	s_waitcnt lgkmcnt(8)
	v_pk_fma_f32 v[120:121], v[100:101], v[174:175], v[124:125] op_sel_hi:[1,0,1]
	s_nop 0
	v_pk_fma_f32 v[116:117], v[174:175], v[90:91], v[120:121] op_sel:[1,0,0]
	s_nop 0
	v_pk_fma_f32 v[116:117], v[176:177], v[102:103], v[116:117] op_sel_hi:[0,1,1]
	v_mov_b32_e32 v118, v177
	v_pk_fma_f32 v[116:117], v[118:119], v[88:89], v[116:117] op_sel_hi:[0,1,1]
	ds_read_b128 v[224:227], v25 offset:20512
	s_waitcnt lgkmcnt(8)
; #define LAS __attribute__((address_space(3)))
; __global__ void __launch_bounds__(NTHREADS, 2) hybrid_fwd(Args a) {
;     ...
; #pragma unroll
;                     for (int j = 0; j < 8; ++j) {
; #pragma unroll
;                         for (int e = 0; e < 16; ++e) { const f32x4 w = *(const LAS f32x4*)(rwT + e * 2052 + j * 256 + lane * 4);
;                             acc2[e] += y2[j][0] * (f32x2){w[0], w[0]}; acc2[e] += y2[j][1] * (f32x2){w[1], w[1]};
;                             acc2[e] += y2[j][2] * (f32x2){w[2], w[2]}; acc2[e] += y2[j][3] * (f32x2){w[3], w[3]}; }
;                         __builtin_amdgcn_sched_barrier(0);
;                     }
	v_pk_fma_f32 v[122:123], v[100:101], v[178:179], v[126:127] op_sel_hi:[1,0,1]
	s_nop 0
	v_pk_fma_f32 v[118:119], v[178:179], v[90:91], v[122:123] op_sel:[1,0,0]
	s_nop 0
	v_pk_fma_f32 v[118:119], v[180:181], v[102:103], v[118:119] op_sel_hi:[0,1,1]
	v_mov_b32_e32 v120, v181
	v_pk_fma_f32 v[118:119], v[120:121], v[88:89], v[118:119] op_sel_hi:[0,1,1]
	ds_read_b128 v[228:231], v25 offset:28720
	s_waitcnt lgkmcnt(8)
	v_pk_fma_f32 v[124:125], v[100:101], v[182:183], v[128:129] op_sel_hi:[1,0,1]
	s_nop 0
	v_pk_fma_f32 v[120:121], v[182:183], v[90:91], v[124:125] op_sel:[1,0,0]
	s_nop 0
	v_pk_fma_f32 v[120:121], v[184:185], v[102:103], v[120:121] op_sel_hi:[0,1,1]
	v_mov_b32_e32 v122, v185
	v_pk_fma_f32 v[120:121], v[122:123], v[88:89], v[120:121] op_sel_hi:[0,1,1]
	ds_read_b128 v[232:235], v25 offset:36928
	s_waitcnt lgkmcnt(8)
	v_pk_fma_f32 v[126:127], v[100:101], v[186:187], v[130:131] op_sel_hi:[1,0,1]
	s_nop 0
	v_pk_fma_f32 v[122:123], v[186:187], v[90:91], v[126:127] op_sel:[1,0,0]
	s_nop 0
	v_pk_fma_f32 v[122:123], v[188:189], v[102:103], v[122:123] op_sel_hi:[0,1,1]
	v_mov_b32_e32 v124, v189
	v_pk_fma_f32 v[122:123], v[124:125], v[88:89], v[122:123] op_sel_hi:[0,1,1]
	ds_read_b128 v[242:245], v25 offset:45136
	s_waitcnt lgkmcnt(8)
	v_pk_fma_f32 v[128:129], v[100:101], v[158:159], v[132:133] op_sel_hi:[1,0,1]
	s_nop 0
	v_pk_fma_f32 v[124:125], v[158:159], v[90:91], v[128:129] op_sel:[1,0,0]
	s_nop 0
	v_pk_fma_f32 v[124:125], v[160:161], v[102:103], v[124:125] op_sel_hi:[0,1,1]
	v_mov_b32_e32 v126, v161
	v_pk_fma_f32 v[124:125], v[126:127], v[88:89], v[124:125] op_sel_hi:[0,1,1]
	ds_read_b128 v[246:249], v25 offset:53344
	s_waitcnt lgkmcnt(8)
	v_pk_fma_f32 v[130:131], v[100:101], v[198:199], v[134:135] op_sel_hi:[1,0,1]
	s_nop 0
	v_pk_fma_f32 v[126:127], v[198:199], v[90:91], v[130:131] op_sel:[1,0,0]
	s_nop 0
	v_pk_fma_f32 v[126:127], v[200:201], v[102:103], v[126:127] op_sel_hi:[0,1,1]
	v_mov_b32_e32 v128, v201
	v_pk_fma_f32 v[126:127], v[128:129], v[88:89], v[126:127] op_sel_hi:[0,1,1]
	ds_read_b128 v[250:253], v25 offset:61552
	s_waitcnt lgkmcnt(8)
	v_pk_fma_f32 v[100:101], v[100:101], v[202:203], v[136:137] op_sel_hi:[1,0,1]
	s_nop 0
	v_pk_fma_f32 v[90:91], v[202:203], v[90:91], v[100:101] op_sel:[1,0,0]
	v_mov_b32_e32 v100, v205
	v_pk_fma_f32 v[90:91], v[204:205], v[102:103], v[90:91] op_sel_hi:[0,1,1]
	v_pk_fma_f32 v[128:129], v[100:101], v[88:89], v[90:91] op_sel_hi:[0,1,1]
	ds_read_b128 v[162:165], v238 offset:4224
	ds_read_b128 v[166:169], v238 offset:12432
	s_waitcnt lgkmcnt(8)
	v_pk_fma_f32 v[96:97], v[92:93], v[216:217], v[96:97] op_sel_hi:[1,0,1]
	s_nop 0
	v_pk_fma_f32 v[88:89], v[216:217], v[86:87], v[96:97] op_sel:[1,0,0]
	v_mov_b32_e32 v96, v223
	v_pk_fma_f32 v[88:89], v[218:219], v[94:95], v[88:89] op_sel_hi:[0,1,1]
	v_mov_b32_e32 v90, v219
	v_pk_fma_f32 v[88:89], v[90:91], v[84:85], v[88:89] op_sel_hi:[0,1,1]
	v_pk_fma_f32 v[90:91], v[92:93], v[220:221], v[138:139] op_sel_hi:[1,0,1]
	s_nop 0
	v_pk_fma_f32 v[90:91], v[220:221], v[86:87], v[90:91] op_sel:[1,0,0]
	s_nop 0
	v_pk_fma_f32 v[90:91], v[222:223], v[94:95], v[90:91] op_sel_hi:[0,1,1]
	ds_read_b128 v[170:173], v238 offset:20640
	v_pk_fma_f32 v[130:131], v[96:97], v[84:85], v[90:91] op_sel_hi:[0,1,1]
	s_waitcnt lgkmcnt(8)
	v_pk_fma_f32 v[90:91], v[92:93], v[224:225], v[98:99] op_sel_hi:[1,0,1]
	s_nop 0
	v_pk_fma_f32 v[90:91], v[224:225], v[86:87], v[90:91] op_sel:[1,0,0]
	v_mov_b32_e32 v96, v227
	v_pk_fma_f32 v[90:91], v[226:227], v[94:95], v[90:91] op_sel_hi:[0,1,1]
	v_pk_fma_f32 v[90:91], v[96:97], v[84:85], v[90:91] op_sel_hi:[0,1,1]
	ds_read_b128 v[174:177], v238 offset:28848
	s_waitcnt lgkmcnt(8)
	v_pk_fma_f32 v[100:101], v[92:93], v[228:229], v[104:105] op_sel_hi:[1,0,1]
	s_nop 0
	v_pk_fma_f32 v[96:97], v[228:229], v[86:87], v[100:101] op_sel:[1,0,0]
	s_nop 0
	v_pk_fma_f32 v[96:97], v[230:231], v[94:95], v[96:97] op_sel_hi:[0,1,1]
	v_mov_b32_e32 v98, v231
	v_pk_fma_f32 v[96:97], v[98:99], v[84:85], v[96:97] op_sel_hi:[0,1,1]
	ds_read_b128 v[178:181], v238 offset:37056
	s_waitcnt lgkmcnt(8)
	v_pk_fma_f32 v[102:103], v[92:93], v[232:233], v[106:107] op_sel_hi:[1,0,1]
	s_nop 0
	v_pk_fma_f32 v[98:99], v[232:233], v[86:87], v[102:103] op_sel:[1,0,0]
	s_nop 0
	v_pk_fma_f32 v[98:99], v[234:235], v[94:95], v[98:99] op_sel_hi:[0,1,1]
	v_mov_b32_e32 v100, v235
	v_pk_fma_f32 v[98:99], v[100:101], v[84:85], v[98:99] op_sel_hi:[0,1,1]
	ds_read_b128 v[182:185], v238 offset:45264
	s_waitcnt lgkmcnt(8)
	v_pk_fma_f32 v[104:105], v[92:93], v[242:243], v[108:109] op_sel_hi:[1,0,1]
	s_nop 0
	v_pk_fma_f32 v[100:101], v[242:243], v[86:87], v[104:105] op_sel:[1,0,0]
	s_nop 0
	v_pk_fma_f32 v[100:101], v[244:245], v[94:95], v[100:101] op_sel_hi:[0,1,1]
	v_mov_b32_e32 v102, v245
	v_pk_fma_f32 v[100:101], v[102:103], v[84:85], v[100:101] op_sel_hi:[0,1,1]
	ds_read_b128 v[186:189], v238 offset:53472
	s_waitcnt lgkmcnt(8)
	v_pk_fma_f32 v[106:107], v[92:93], v[246:247], v[110:111] op_sel_hi:[1,0,1]
	s_nop 0
	v_pk_fma_f32 v[102:103], v[246:247], v[86:87], v[106:107] op_sel:[1,0,0]
	s_nop 0
	v_pk_fma_f32 v[102:103], v[248:249], v[94:95], v[102:103] op_sel_hi:[0,1,1]
	v_mov_b32_e32 v104, v249
	v_pk_fma_f32 v[102:103], v[104:105], v[84:85], v[102:103] op_sel_hi:[0,1,1]
	ds_read_b128 v[158:161], v238 offset:61680
	s_waitcnt lgkmcnt(8)
	v_pk_fma_f32 v[108:109], v[92:93], v[250:251], v[112:113] op_sel_hi:[1,0,1]
	s_nop 0
	v_pk_fma_f32 v[104:105], v[250:251], v[86:87], v[108:109] op_sel:[1,0,0]
	s_nop 0
	v_pk_fma_f32 v[104:105], v[252:253], v[94:95], v[104:105] op_sel_hi:[0,1,1]
	v_mov_b32_e32 v106, v253
	v_pk_fma_f32 v[104:105], v[106:107], v[84:85], v[104:105] op_sel_hi:[0,1,1]
	ds_read_b128 v[198:201], v25 offset:5120
	s_waitcnt lgkmcnt(8)
; #define LAS __attribute__((address_space(3)))
; __global__ void __launch_bounds__(NTHREADS, 2) hybrid_fwd(Args a) {
;     ...
; #pragma unroll
;                     for (int j = 0; j < 8; ++j) {
; #pragma unroll
;                         for (int e = 0; e < 16; ++e) { const f32x4 w = *(const LAS f32x4*)(rwT + e * 2052 + j * 256 + lane * 4);
;                             acc2[e] += y2[j][0] * (f32x2){w[0], w[0]}; acc2[e] += y2[j][1] * (f32x2){w[1], w[1]};
;                             acc2[e] += y2[j][2] * (f32x2){w[2], w[2]}; acc2[e] += y2[j][3] * (f32x2){w[3], w[3]}; }
;                         __builtin_amdgcn_sched_barrier(0);
;                     }
	v_pk_fma_f32 v[110:111], v[92:93], v[162:163], v[114:115] op_sel_hi:[1,0,1]
	s_nop 0
	v_pk_fma_f32 v[106:107], v[162:163], v[86:87], v[110:111] op_sel:[1,0,0]
	s_nop 0
	v_pk_fma_f32 v[106:107], v[164:165], v[94:95], v[106:107] op_sel_hi:[0,1,1]
	v_mov_b32_e32 v108, v165
	v_pk_fma_f32 v[106:107], v[108:109], v[84:85], v[106:107] op_sel_hi:[0,1,1]
	ds_read_b128 v[202:205], v25 offset:13328
	s_waitcnt lgkmcnt(8)
	v_pk_fma_f32 v[112:113], v[92:93], v[166:167], v[116:117] op_sel_hi:[1,0,1]
	s_nop 0
	v_pk_fma_f32 v[108:109], v[166:167], v[86:87], v[112:113] op_sel:[1,0,0]
	s_nop 0
	v_pk_fma_f32 v[108:109], v[168:169], v[94:95], v[108:109] op_sel_hi:[0,1,1]
	v_mov_b32_e32 v110, v169
	v_pk_fma_f32 v[108:109], v[110:111], v[84:85], v[108:109] op_sel_hi:[0,1,1]
	ds_read_b128 v[216:219], v25 offset:21536
	s_waitcnt lgkmcnt(8)
	v_pk_fma_f32 v[114:115], v[92:93], v[170:171], v[118:119] op_sel_hi:[1,0,1]
	s_nop 0
	v_pk_fma_f32 v[110:111], v[170:171], v[86:87], v[114:115] op_sel:[1,0,0]
	s_nop 0
	v_pk_fma_f32 v[110:111], v[172:173], v[94:95], v[110:111] op_sel_hi:[0,1,1]
	v_mov_b32_e32 v112, v173
	v_pk_fma_f32 v[110:111], v[112:113], v[84:85], v[110:111] op_sel_hi:[0,1,1]
	ds_read_b128 v[220:223], v25 offset:29744
	s_waitcnt lgkmcnt(8)
	v_pk_fma_f32 v[116:117], v[92:93], v[174:175], v[120:121] op_sel_hi:[1,0,1]
	s_nop 0
	v_pk_fma_f32 v[112:113], v[174:175], v[86:87], v[116:117] op_sel:[1,0,0]
	s_nop 0
	v_pk_fma_f32 v[112:113], v[176:177], v[94:95], v[112:113] op_sel_hi:[0,1,1]
	v_mov_b32_e32 v114, v177
	v_pk_fma_f32 v[112:113], v[114:115], v[84:85], v[112:113] op_sel_hi:[0,1,1]
	ds_read_b128 v[224:227], v25 offset:37952
	s_waitcnt lgkmcnt(8)
	v_pk_fma_f32 v[118:119], v[92:93], v[178:179], v[122:123] op_sel_hi:[1,0,1]
	s_nop 0
	v_pk_fma_f32 v[114:115], v[178:179], v[86:87], v[118:119] op_sel:[1,0,0]
	s_nop 0
	v_pk_fma_f32 v[114:115], v[180:181], v[94:95], v[114:115] op_sel_hi:[0,1,1]
	v_mov_b32_e32 v116, v181
	v_pk_fma_f32 v[114:115], v[116:117], v[84:85], v[114:115] op_sel_hi:[0,1,1]
	ds_read_b128 v[228:231], v25 offset:46160
	s_waitcnt lgkmcnt(8)
	v_pk_fma_f32 v[120:121], v[92:93], v[182:183], v[124:125] op_sel_hi:[1,0,1]
	s_nop 0
	v_pk_fma_f32 v[116:117], v[182:183], v[86:87], v[120:121] op_sel:[1,0,0]
	s_nop 0
	v_pk_fma_f32 v[116:117], v[184:185], v[94:95], v[116:117] op_sel_hi:[0,1,1]
	v_mov_b32_e32 v118, v185
	v_pk_fma_f32 v[116:117], v[118:119], v[84:85], v[116:117] op_sel_hi:[0,1,1]
	ds_read_b128 v[232:235], v25 offset:54368
	s_waitcnt lgkmcnt(8)
	v_pk_fma_f32 v[122:123], v[92:93], v[186:187], v[126:127] op_sel_hi:[1,0,1]
	s_nop 0
	v_pk_fma_f32 v[118:119], v[186:187], v[86:87], v[122:123] op_sel:[1,0,0]
	s_nop 0
	v_pk_fma_f32 v[118:119], v[188:189], v[94:95], v[118:119] op_sel_hi:[0,1,1]
	v_mov_b32_e32 v120, v189
	v_pk_fma_f32 v[118:119], v[120:121], v[84:85], v[118:119] op_sel_hi:[0,1,1]
	ds_read_b128 v[242:245], v25 offset:62576
	s_waitcnt lgkmcnt(8)
	v_pk_fma_f32 v[92:93], v[92:93], v[158:159], v[128:129] op_sel_hi:[1,0,1]
	s_nop 0
	v_pk_fma_f32 v[86:87], v[158:159], v[86:87], v[92:93] op_sel:[1,0,0]
	v_mov_b32_e32 v92, v161
	v_pk_fma_f32 v[86:87], v[160:161], v[94:95], v[86:87] op_sel_hi:[0,1,1]
	v_pk_fma_f32 v[120:121], v[92:93], v[84:85], v[86:87] op_sel_hi:[0,1,1]
	ds_read_b128 v[246:249], v238 offset:5248
	s_waitcnt lgkmcnt(8)
	v_pk_fma_f32 v[88:89], v[80:81], v[198:199], v[88:89] op_sel_hi:[1,0,1]
	s_nop 0
	v_pk_fma_f32 v[84:85], v[198:199], v[78:79], v[88:89] op_sel:[1,0,0]
	s_nop 0
	v_pk_fma_f32 v[84:85], v[200:201], v[82:83], v[84:85] op_sel_hi:[0,1,1]
	v_mov_b32_e32 v86, v201
	v_pk_fma_f32 v[84:85], v[86:87], v[76:77], v[84:85] op_sel_hi:[0,1,1]
	ds_read_b128 v[250:253], v238 offset:13456
	s_waitcnt lgkmcnt(8)
	v_pk_fma_f32 v[92:93], v[80:81], v[202:203], v[130:131] op_sel_hi:[1,0,1]
	s_nop 0
	v_pk_fma_f32 v[86:87], v[202:203], v[78:79], v[92:93] op_sel:[1,0,0]
	s_nop 0
	v_pk_fma_f32 v[86:87], v[204:205], v[82:83], v[86:87] op_sel_hi:[0,1,1]
	v_mov_b32_e32 v88, v205
	v_pk_fma_f32 v[122:123], v[88:89], v[76:77], v[86:87] op_sel_hi:[0,1,1]
	ds_read_b128 v[162:165], v238 offset:21664
	s_waitcnt lgkmcnt(8)
	v_pk_fma_f32 v[90:91], v[80:81], v[216:217], v[90:91] op_sel_hi:[1,0,1]
	s_nop 0
	v_pk_fma_f32 v[86:87], v[216:217], v[78:79], v[90:91] op_sel:[1,0,0]
	s_nop 0
	v_pk_fma_f32 v[86:87], v[218:219], v[82:83], v[86:87] op_sel_hi:[0,1,1]
	v_mov_b32_e32 v88, v219
	v_pk_fma_f32 v[86:87], v[88:89], v[76:77], v[86:87] op_sel_hi:[0,1,1]
	ds_read_b128 v[166:169], v238 offset:29872
	s_waitcnt lgkmcnt(8)
	v_pk_fma_f32 v[92:93], v[80:81], v[220:221], v[96:97] op_sel_hi:[1,0,1]
	s_nop 0
	v_pk_fma_f32 v[88:89], v[220:221], v[78:79], v[92:93] op_sel:[1,0,0]
	s_nop 0
	v_pk_fma_f32 v[88:89], v[222:223], v[82:83], v[88:89] op_sel_hi:[0,1,1]
	v_mov_b32_e32 v90, v223
	v_pk_fma_f32 v[88:89], v[90:91], v[76:77], v[88:89] op_sel_hi:[0,1,1]
	ds_read_b128 v[170:173], v238 offset:38080
	s_waitcnt lgkmcnt(8)
	v_pk_fma_f32 v[94:95], v[80:81], v[224:225], v[98:99] op_sel_hi:[1,0,1]
	s_nop 0
	v_pk_fma_f32 v[90:91], v[224:225], v[78:79], v[94:95] op_sel:[1,0,0]
	s_nop 0
	v_pk_fma_f32 v[90:91], v[226:227], v[82:83], v[90:91] op_sel_hi:[0,1,1]
	v_mov_b32_e32 v92, v227
	v_pk_fma_f32 v[90:91], v[92:93], v[76:77], v[90:91] op_sel_hi:[0,1,1]
	ds_read_b128 v[174:177], v238 offset:46288
	s_waitcnt lgkmcnt(8)
	v_pk_fma_f32 v[96:97], v[80:81], v[228:229], v[100:101] op_sel_hi:[1,0,1]
	s_nop 0
	v_pk_fma_f32 v[92:93], v[228:229], v[78:79], v[96:97] op_sel:[1,0,0]
	s_nop 0
	v_pk_fma_f32 v[92:93], v[230:231], v[82:83], v[92:93] op_sel_hi:[0,1,1]
	v_mov_b32_e32 v94, v231
	v_pk_fma_f32 v[92:93], v[94:95], v[76:77], v[92:93] op_sel_hi:[0,1,1]
	ds_read_b128 v[178:181], v238 offset:54496
	s_waitcnt lgkmcnt(8)
; #define LAS __attribute__((address_space(3)))
; __global__ void __launch_bounds__(NTHREADS, 2) hybrid_fwd(Args a) {
;     ...
; #pragma unroll
;                     for (int j = 0; j < 8; ++j) {
; #pragma unroll
;                         for (int e = 0; e < 16; ++e) { const f32x4 w = *(const LAS f32x4*)(rwT + e * 2052 + j * 256 + lane * 4);
;                             acc2[e] += y2[j][0] * (f32x2){w[0], w[0]}; acc2[e] += y2[j][1] * (f32x2){w[1], w[1]};
;                             acc2[e] += y2[j][2] * (f32x2){w[2], w[2]}; acc2[e] += y2[j][3] * (f32x2){w[3], w[3]}; }
;                         __builtin_amdgcn_sched_barrier(0);
;                     }
	v_pk_fma_f32 v[98:99], v[80:81], v[232:233], v[102:103] op_sel_hi:[1,0,1]
	s_nop 0
	v_pk_fma_f32 v[94:95], v[232:233], v[78:79], v[98:99] op_sel:[1,0,0]
	s_nop 0
	v_pk_fma_f32 v[94:95], v[234:235], v[82:83], v[94:95] op_sel_hi:[0,1,1]
	v_mov_b32_e32 v96, v235
	v_pk_fma_f32 v[94:95], v[96:97], v[76:77], v[94:95] op_sel_hi:[0,1,1]
	ds_read_b128 v[182:185], v238 offset:62704
	s_waitcnt lgkmcnt(8)
	v_pk_fma_f32 v[100:101], v[80:81], v[242:243], v[104:105] op_sel_hi:[1,0,1]
	s_nop 0
	v_pk_fma_f32 v[96:97], v[242:243], v[78:79], v[100:101] op_sel:[1,0,0]
	s_nop 0
	v_pk_fma_f32 v[96:97], v[244:245], v[82:83], v[96:97] op_sel_hi:[0,1,1]
	v_mov_b32_e32 v98, v245
	v_pk_fma_f32 v[96:97], v[98:99], v[76:77], v[96:97] op_sel_hi:[0,1,1]
	ds_read_b128 v[186:189], v25 offset:6144
	s_waitcnt lgkmcnt(8)
	v_pk_fma_f32 v[102:103], v[80:81], v[246:247], v[106:107] op_sel_hi:[1,0,1]
	s_nop 0
	v_pk_fma_f32 v[98:99], v[246:247], v[78:79], v[102:103] op_sel:[1,0,0]
	s_nop 0
	v_pk_fma_f32 v[98:99], v[248:249], v[82:83], v[98:99] op_sel_hi:[0,1,1]
	v_mov_b32_e32 v100, v249
	v_pk_fma_f32 v[98:99], v[100:101], v[76:77], v[98:99] op_sel_hi:[0,1,1]
	ds_read_b128 v[158:161], v25 offset:14352
	s_waitcnt lgkmcnt(8)
	v_pk_fma_f32 v[104:105], v[80:81], v[250:251], v[108:109] op_sel_hi:[1,0,1]
	s_nop 0
	v_pk_fma_f32 v[100:101], v[250:251], v[78:79], v[104:105] op_sel:[1,0,0]
	s_nop 0
	v_pk_fma_f32 v[100:101], v[252:253], v[82:83], v[100:101] op_sel_hi:[0,1,1]
	v_mov_b32_e32 v102, v253
	v_pk_fma_f32 v[100:101], v[102:103], v[76:77], v[100:101] op_sel_hi:[0,1,1]
	ds_read_b128 v[198:201], v25 offset:22560
	s_waitcnt lgkmcnt(8)
	v_pk_fma_f32 v[106:107], v[80:81], v[162:163], v[110:111] op_sel_hi:[1,0,1]
	s_nop 0
	v_pk_fma_f32 v[102:103], v[162:163], v[78:79], v[106:107] op_sel:[1,0,0]
	s_nop 0
	v_pk_fma_f32 v[102:103], v[164:165], v[82:83], v[102:103] op_sel_hi:[0,1,1]
	v_mov_b32_e32 v104, v165
	v_pk_fma_f32 v[102:103], v[104:105], v[76:77], v[102:103] op_sel_hi:[0,1,1]
	ds_read_b128 v[202:205], v25 offset:30768
	s_waitcnt lgkmcnt(8)
	v_pk_fma_f32 v[108:109], v[80:81], v[166:167], v[112:113] op_sel_hi:[1,0,1]
	s_nop 0
	v_pk_fma_f32 v[104:105], v[166:167], v[78:79], v[108:109] op_sel:[1,0,0]
	s_nop 0
	v_pk_fma_f32 v[104:105], v[168:169], v[82:83], v[104:105] op_sel_hi:[0,1,1]
	v_mov_b32_e32 v106, v169
	v_pk_fma_f32 v[104:105], v[106:107], v[76:77], v[104:105] op_sel_hi:[0,1,1]
	ds_read_b128 v[216:219], v25 offset:38976
	s_waitcnt lgkmcnt(8)
	v_pk_fma_f32 v[110:111], v[80:81], v[170:171], v[114:115] op_sel_hi:[1,0,1]
	s_nop 0
	v_pk_fma_f32 v[106:107], v[170:171], v[78:79], v[110:111] op_sel:[1,0,0]
	s_nop 0
	v_pk_fma_f32 v[106:107], v[172:173], v[82:83], v[106:107] op_sel_hi:[0,1,1]
	v_mov_b32_e32 v108, v173
	v_pk_fma_f32 v[106:107], v[108:109], v[76:77], v[106:107] op_sel_hi:[0,1,1]
	ds_read_b128 v[220:223], v25 offset:47184
	s_waitcnt lgkmcnt(8)
	v_pk_fma_f32 v[112:113], v[80:81], v[174:175], v[116:117] op_sel_hi:[1,0,1]
	s_nop 0
	v_pk_fma_f32 v[108:109], v[174:175], v[78:79], v[112:113] op_sel:[1,0,0]
	s_nop 0
	v_pk_fma_f32 v[108:109], v[176:177], v[82:83], v[108:109] op_sel_hi:[0,1,1]
	v_mov_b32_e32 v110, v177
	v_pk_fma_f32 v[108:109], v[110:111], v[76:77], v[108:109] op_sel_hi:[0,1,1]
	ds_read_b128 v[224:227], v25 offset:55392
	s_waitcnt lgkmcnt(8)
	v_pk_fma_f32 v[114:115], v[80:81], v[178:179], v[118:119] op_sel_hi:[1,0,1]
	s_nop 0
	v_pk_fma_f32 v[110:111], v[178:179], v[78:79], v[114:115] op_sel:[1,0,0]
	s_nop 0
	v_pk_fma_f32 v[110:111], v[180:181], v[82:83], v[110:111] op_sel_hi:[0,1,1]
	v_mov_b32_e32 v112, v181
	v_pk_fma_f32 v[110:111], v[112:113], v[76:77], v[110:111] op_sel_hi:[0,1,1]
	ds_read_b128 v[228:231], v25 offset:63600
	s_waitcnt lgkmcnt(8)
	v_pk_fma_f32 v[80:81], v[80:81], v[182:183], v[120:121] op_sel_hi:[1,0,1]
	s_nop 0
	v_pk_fma_f32 v[78:79], v[182:183], v[78:79], v[80:81] op_sel:[1,0,0]
	v_mov_b32_e32 v80, v185
	v_pk_fma_f32 v[78:79], v[184:185], v[82:83], v[78:79] op_sel_hi:[0,1,1]
	v_pk_fma_f32 v[112:113], v[80:81], v[76:77], v[78:79] op_sel_hi:[0,1,1]
	ds_read_b128 v[232:235], v238 offset:6272
	s_waitcnt lgkmcnt(8)
	v_pk_fma_f32 v[80:81], v[72:73], v[186:187], v[84:85] op_sel_hi:[1,0,1]
	s_nop 0
	v_pk_fma_f32 v[76:77], v[186:187], v[70:71], v[80:81] op_sel:[1,0,0]
	s_nop 0
	v_pk_fma_f32 v[76:77], v[188:189], v[74:75], v[76:77] op_sel_hi:[0,1,1]
	v_mov_b32_e32 v78, v189
	v_pk_fma_f32 v[76:77], v[78:79], v[68:69], v[76:77] op_sel_hi:[0,1,1]
	ds_read_b128 v[242:245], v238 offset:14480
	s_waitcnt lgkmcnt(8)
	v_pk_fma_f32 v[82:83], v[72:73], v[158:159], v[122:123] op_sel_hi:[1,0,1]
	s_nop 0
	v_pk_fma_f32 v[78:79], v[158:159], v[70:71], v[82:83] op_sel:[1,0,0]
	s_nop 0
	v_pk_fma_f32 v[78:79], v[160:161], v[74:75], v[78:79] op_sel_hi:[0,1,1]
	v_mov_b32_e32 v80, v161
	v_pk_fma_f32 v[114:115], v[80:81], v[68:69], v[78:79] op_sel_hi:[0,1,1]
	ds_read_b128 v[246:249], v238 offset:22688
	s_waitcnt lgkmcnt(8)
	v_pk_fma_f32 v[82:83], v[72:73], v[198:199], v[86:87] op_sel_hi:[1,0,1]
	s_nop 0
	v_pk_fma_f32 v[78:79], v[198:199], v[70:71], v[82:83] op_sel:[1,0,0]
	s_nop 0
	v_pk_fma_f32 v[78:79], v[200:201], v[74:75], v[78:79] op_sel_hi:[0,1,1]
	v_mov_b32_e32 v80, v201
	v_pk_fma_f32 v[78:79], v[80:81], v[68:69], v[78:79] op_sel_hi:[0,1,1]
	ds_read_b128 v[250:253], v238 offset:30896
	s_waitcnt lgkmcnt(8)
	v_pk_fma_f32 v[84:85], v[72:73], v[202:203], v[88:89] op_sel_hi:[1,0,1]
	s_nop 0
	v_pk_fma_f32 v[80:81], v[202:203], v[70:71], v[84:85] op_sel:[1,0,0]
	s_nop 0
	v_pk_fma_f32 v[80:81], v[204:205], v[74:75], v[80:81] op_sel_hi:[0,1,1]
	v_mov_b32_e32 v82, v205
	v_pk_fma_f32 v[80:81], v[82:83], v[68:69], v[80:81] op_sel_hi:[0,1,1]
	ds_read_b128 v[162:165], v238 offset:39104
	s_waitcnt lgkmcnt(8)
; #define LAS __attribute__((address_space(3)))
; __global__ void __launch_bounds__(NTHREADS, 2) hybrid_fwd(Args a) {
;     ...
; #pragma unroll
;                     for (int j = 0; j < 8; ++j) {
; #pragma unroll
;                         for (int e = 0; e < 16; ++e) { const f32x4 w = *(const LAS f32x4*)(rwT + e * 2052 + j * 256 + lane * 4);
;                             acc2[e] += y2[j][0] * (f32x2){w[0], w[0]}; acc2[e] += y2[j][1] * (f32x2){w[1], w[1]};
;                             acc2[e] += y2[j][2] * (f32x2){w[2], w[2]}; acc2[e] += y2[j][3] * (f32x2){w[3], w[3]}; }
;                         __builtin_amdgcn_sched_barrier(0);
;                     }
	v_pk_fma_f32 v[86:87], v[72:73], v[216:217], v[90:91] op_sel_hi:[1,0,1]
	s_nop 0
	v_pk_fma_f32 v[82:83], v[216:217], v[70:71], v[86:87] op_sel:[1,0,0]
	s_nop 0
	v_pk_fma_f32 v[82:83], v[218:219], v[74:75], v[82:83] op_sel_hi:[0,1,1]
	v_mov_b32_e32 v84, v219
	v_pk_fma_f32 v[82:83], v[84:85], v[68:69], v[82:83] op_sel_hi:[0,1,1]
	ds_read_b128 v[166:169], v238 offset:47312
	s_waitcnt lgkmcnt(8)
	v_pk_fma_f32 v[88:89], v[72:73], v[220:221], v[92:93] op_sel_hi:[1,0,1]
	s_nop 0
	v_pk_fma_f32 v[84:85], v[220:221], v[70:71], v[88:89] op_sel:[1,0,0]
	s_nop 0
	v_pk_fma_f32 v[84:85], v[222:223], v[74:75], v[84:85] op_sel_hi:[0,1,1]
	v_mov_b32_e32 v86, v223
	v_pk_fma_f32 v[84:85], v[86:87], v[68:69], v[84:85] op_sel_hi:[0,1,1]
	ds_read_b128 v[170:173], v238 offset:55520
	s_waitcnt lgkmcnt(8)
	v_pk_fma_f32 v[90:91], v[72:73], v[224:225], v[94:95] op_sel_hi:[1,0,1]
	s_nop 0
	v_pk_fma_f32 v[86:87], v[224:225], v[70:71], v[90:91] op_sel:[1,0,0]
	s_nop 0
	v_pk_fma_f32 v[86:87], v[226:227], v[74:75], v[86:87] op_sel_hi:[0,1,1]
	v_mov_b32_e32 v88, v227
	v_pk_fma_f32 v[86:87], v[88:89], v[68:69], v[86:87] op_sel_hi:[0,1,1]
	ds_read_b128 v[174:177], v238 offset:63728
	s_waitcnt lgkmcnt(8)
	v_pk_fma_f32 v[92:93], v[72:73], v[228:229], v[96:97] op_sel_hi:[1,0,1]
	s_nop 0
	v_pk_fma_f32 v[88:89], v[228:229], v[70:71], v[92:93] op_sel:[1,0,0]
	s_nop 0
	v_pk_fma_f32 v[88:89], v[230:231], v[74:75], v[88:89] op_sel_hi:[0,1,1]
	v_mov_b32_e32 v90, v231
	v_pk_fma_f32 v[88:89], v[90:91], v[68:69], v[88:89] op_sel_hi:[0,1,1]
	ds_read_b128 v[178:181], v25 offset:7168
	s_waitcnt lgkmcnt(8)
	v_pk_fma_f32 v[94:95], v[72:73], v[232:233], v[98:99] op_sel_hi:[1,0,1]
	s_nop 0
	v_pk_fma_f32 v[90:91], v[232:233], v[70:71], v[94:95] op_sel:[1,0,0]
	s_nop 0
	v_pk_fma_f32 v[90:91], v[234:235], v[74:75], v[90:91] op_sel_hi:[0,1,1]
	v_mov_b32_e32 v92, v235
	v_pk_fma_f32 v[90:91], v[92:93], v[68:69], v[90:91] op_sel_hi:[0,1,1]
	ds_read_b128 v[182:185], v25 offset:15376
	s_waitcnt lgkmcnt(8)
	v_pk_fma_f32 v[96:97], v[72:73], v[242:243], v[100:101] op_sel_hi:[1,0,1]
	s_nop 0
	v_pk_fma_f32 v[92:93], v[242:243], v[70:71], v[96:97] op_sel:[1,0,0]
	s_nop 0
	v_pk_fma_f32 v[92:93], v[244:245], v[74:75], v[92:93] op_sel_hi:[0,1,1]
	v_mov_b32_e32 v94, v245
	v_pk_fma_f32 v[92:93], v[94:95], v[68:69], v[92:93] op_sel_hi:[0,1,1]
	ds_read_b128 v[186:189], v25 offset:23584
	s_waitcnt lgkmcnt(8)
	v_pk_fma_f32 v[98:99], v[72:73], v[246:247], v[102:103] op_sel_hi:[1,0,1]
	s_nop 0
	v_pk_fma_f32 v[94:95], v[246:247], v[70:71], v[98:99] op_sel:[1,0,0]
	s_nop 0
	v_pk_fma_f32 v[94:95], v[248:249], v[74:75], v[94:95] op_sel_hi:[0,1,1]
	v_mov_b32_e32 v96, v249
	v_pk_fma_f32 v[94:95], v[96:97], v[68:69], v[94:95] op_sel_hi:[0,1,1]
	ds_read_b128 v[158:161], v25 offset:31792
	s_waitcnt lgkmcnt(8)
	v_pk_fma_f32 v[100:101], v[72:73], v[250:251], v[104:105] op_sel_hi:[1,0,1]
	s_nop 0
	v_pk_fma_f32 v[96:97], v[250:251], v[70:71], v[100:101] op_sel:[1,0,0]
	s_nop 0
	v_pk_fma_f32 v[96:97], v[252:253], v[74:75], v[96:97] op_sel_hi:[0,1,1]
	v_mov_b32_e32 v98, v253
	v_pk_fma_f32 v[96:97], v[98:99], v[68:69], v[96:97] op_sel_hi:[0,1,1]
	ds_read_b128 v[198:201], v25 offset:40000
	s_waitcnt lgkmcnt(8)
	v_pk_fma_f32 v[102:103], v[72:73], v[162:163], v[106:107] op_sel_hi:[1,0,1]
	s_nop 0
	v_pk_fma_f32 v[98:99], v[162:163], v[70:71], v[102:103] op_sel:[1,0,0]
	s_nop 0
	v_pk_fma_f32 v[98:99], v[164:165], v[74:75], v[98:99] op_sel_hi:[0,1,1]
	v_mov_b32_e32 v100, v165
	v_pk_fma_f32 v[98:99], v[100:101], v[68:69], v[98:99] op_sel_hi:[0,1,1]
	ds_read_b128 v[202:205], v25 offset:48208
	s_waitcnt lgkmcnt(8)
	v_pk_fma_f32 v[104:105], v[72:73], v[166:167], v[108:109] op_sel_hi:[1,0,1]
	s_nop 0
	v_pk_fma_f32 v[100:101], v[166:167], v[70:71], v[104:105] op_sel:[1,0,0]
	s_nop 0
	v_pk_fma_f32 v[100:101], v[168:169], v[74:75], v[100:101] op_sel_hi:[0,1,1]
	v_mov_b32_e32 v102, v169
	v_pk_fma_f32 v[100:101], v[102:103], v[68:69], v[100:101] op_sel_hi:[0,1,1]
	ds_read_b128 v[216:219], v25 offset:56416
	s_waitcnt lgkmcnt(8)
	v_pk_fma_f32 v[106:107], v[72:73], v[170:171], v[110:111] op_sel_hi:[1,0,1]
	s_nop 0
	v_pk_fma_f32 v[102:103], v[170:171], v[70:71], v[106:107] op_sel:[1,0,0]
	s_nop 0
	v_pk_fma_f32 v[102:103], v[172:173], v[74:75], v[102:103] op_sel_hi:[0,1,1]
	v_mov_b32_e32 v104, v173
	v_pk_fma_f32 v[102:103], v[104:105], v[68:69], v[102:103] op_sel_hi:[0,1,1]
	ds_read_b128 v[220:223], v25 offset:64624
	s_waitcnt lgkmcnt(8)
	v_pk_fma_f32 v[72:73], v[72:73], v[174:175], v[112:113] op_sel_hi:[1,0,1]
	s_nop 0
	v_pk_fma_f32 v[70:71], v[174:175], v[70:71], v[72:73] op_sel:[1,0,0]
	v_mov_b32_e32 v72, v177
	v_pk_fma_f32 v[70:71], v[176:177], v[74:75], v[70:71] op_sel_hi:[0,1,1]
	v_pk_fma_f32 v[104:105], v[72:73], v[68:69], v[70:71] op_sel_hi:[0,1,1]
	ds_read_b128 v[224:227], v238 offset:7296
	s_waitcnt lgkmcnt(8)
	v_pk_fma_f32 v[72:73], v[66:67], v[178:179], v[76:77] op_sel_hi:[1,0,1]
	s_nop 0
	v_pk_fma_f32 v[68:69], v[178:179], v[62:63], v[72:73] op_sel:[1,0,0]
	s_nop 0
	v_pk_fma_f32 v[68:69], v[180:181], v[64:65], v[68:69] op_sel_hi:[0,1,1]
	v_mov_b32_e32 v70, v181
	v_pk_fma_f32 v[68:69], v[70:71], v[60:61], v[68:69] op_sel_hi:[0,1,1]
	ds_read_b128 v[228:231], v238 offset:15504
	s_waitcnt lgkmcnt(8)
	v_pk_fma_f32 v[74:75], v[66:67], v[182:183], v[114:115] op_sel_hi:[1,0,1]
	s_nop 0
	v_pk_fma_f32 v[70:71], v[182:183], v[62:63], v[74:75] op_sel:[1,0,0]
	s_nop 0
	v_pk_fma_f32 v[70:71], v[184:185], v[64:65], v[70:71] op_sel_hi:[0,1,1]
	v_mov_b32_e32 v72, v185
	v_pk_fma_f32 v[70:71], v[72:73], v[60:61], v[70:71] op_sel_hi:[0,1,1]
	ds_read_b128 v[232:235], v238 offset:23712
	s_waitcnt lgkmcnt(8)
; #define LAS __attribute__((address_space(3)))
; __global__ void __launch_bounds__(NTHREADS, 2) hybrid_fwd(Args a) {
;     ...
; #pragma unroll
;                     for (int j = 0; j < 8; ++j) {
; #pragma unroll
;                         for (int e = 0; e < 16; ++e) { const f32x4 w = *(const LAS f32x4*)(rwT + e * 2052 + j * 256 + lane * 4);
;                             acc2[e] += y2[j][0] * (f32x2){w[0], w[0]}; acc2[e] += y2[j][1] * (f32x2){w[1], w[1]};
;                             acc2[e] += y2[j][2] * (f32x2){w[2], w[2]}; acc2[e] += y2[j][3] * (f32x2){w[3], w[3]}; }
;                         __builtin_amdgcn_sched_barrier(0);
;                     }
	v_pk_fma_f32 v[76:77], v[66:67], v[186:187], v[78:79] op_sel_hi:[1,0,1]
	s_nop 0
	v_pk_fma_f32 v[72:73], v[186:187], v[62:63], v[76:77] op_sel:[1,0,0]
	s_nop 0
	v_pk_fma_f32 v[72:73], v[188:189], v[64:65], v[72:73] op_sel_hi:[0,1,1]
	v_mov_b32_e32 v74, v189
	v_pk_fma_f32 v[72:73], v[74:75], v[60:61], v[72:73] op_sel_hi:[0,1,1]
	ds_read_b128 v[242:245], v238 offset:31920
	s_waitcnt lgkmcnt(8)
	v_pk_fma_f32 v[78:79], v[66:67], v[158:159], v[80:81] op_sel_hi:[1,0,1]
	s_nop 0
	v_pk_fma_f32 v[74:75], v[158:159], v[62:63], v[78:79] op_sel:[1,0,0]
	ds_read_b128 v[246:249], v238 offset:40128
	v_pk_fma_f32 v[74:75], v[160:161], v[64:65], v[74:75] op_sel_hi:[0,1,1]
	v_mov_b32_e32 v76, v161
	v_pk_fma_f32 v[76:77], v[76:77], v[60:61], v[74:75] op_sel_hi:[0,1,1]
	s_waitcnt lgkmcnt(8)
	v_pk_fma_f32 v[74:75], v[66:67], v[198:199], v[82:83] op_sel_hi:[1,0,1]
	s_nop 0
	v_pk_fma_f32 v[74:75], v[198:199], v[62:63], v[74:75] op_sel:[1,0,0]
	v_mov_b32_e32 v78, v201
	v_pk_fma_f32 v[74:75], v[200:201], v[64:65], v[74:75] op_sel_hi:[0,1,1]
	v_pk_fma_f32 v[74:75], v[78:79], v[60:61], v[74:75] op_sel_hi:[0,1,1]
	ds_read_b128 v[250:253], v238 offset:48336
	s_waitcnt lgkmcnt(8)
	v_pk_fma_f32 v[82:83], v[66:67], v[202:203], v[84:85] op_sel_hi:[1,0,1]
	s_nop 0
	v_pk_fma_f32 v[78:79], v[202:203], v[62:63], v[82:83] op_sel:[1,0,0]
	s_nop 0
	v_pk_fma_f32 v[78:79], v[204:205], v[64:65], v[78:79] op_sel_hi:[0,1,1]
	v_mov_b32_e32 v80, v205
	v_pk_fma_f32 v[78:79], v[80:81], v[60:61], v[78:79] op_sel_hi:[0,1,1]
	ds_read_b128 v[162:165], v238 offset:56544
	s_waitcnt lgkmcnt(8)
	v_pk_fma_f32 v[84:85], v[66:67], v[216:217], v[86:87] op_sel_hi:[1,0,1]
	s_nop 0
	v_pk_fma_f32 v[80:81], v[216:217], v[62:63], v[84:85] op_sel:[1,0,0]
	s_nop 0
	v_pk_fma_f32 v[80:81], v[218:219], v[64:65], v[80:81] op_sel_hi:[0,1,1]
	v_mov_b32_e32 v82, v219
	v_pk_fma_f32 v[80:81], v[82:83], v[60:61], v[80:81] op_sel_hi:[0,1,1]
	ds_read_b128 v[166:169], v238 offset:64752
	s_waitcnt lgkmcnt(8)
	v_pk_fma_f32 v[86:87], v[66:67], v[220:221], v[88:89] op_sel_hi:[1,0,1]
	s_nop 0
	v_pk_fma_f32 v[82:83], v[220:221], v[62:63], v[86:87] op_sel:[1,0,0]
	s_nop 0
	v_pk_fma_f32 v[82:83], v[222:223], v[64:65], v[82:83] op_sel_hi:[0,1,1]
	v_mov_b32_e32 v84, v223
	v_pk_fma_f32 v[82:83], v[84:85], v[60:61], v[82:83] op_sel_hi:[0,1,1]
	s_waitcnt lgkmcnt(7)
	v_pk_fma_f32 v[88:89], v[66:67], v[224:225], v[90:91] op_sel_hi:[1,0,1]
	s_nop 0
	v_pk_fma_f32 v[84:85], v[224:225], v[62:63], v[88:89] op_sel:[1,0,0]
	s_nop 0
	v_pk_fma_f32 v[84:85], v[226:227], v[64:65], v[84:85] op_sel_hi:[0,1,1]
	v_mov_b32_e32 v86, v227
	v_pk_fma_f32 v[84:85], v[86:87], v[60:61], v[84:85] op_sel_hi:[0,1,1]
	s_waitcnt lgkmcnt(6)
	v_pk_fma_f32 v[90:91], v[66:67], v[228:229], v[92:93] op_sel_hi:[1,0,1]
	s_nop 0
	v_pk_fma_f32 v[86:87], v[228:229], v[62:63], v[90:91] op_sel:[1,0,0]
	s_nop 0
	v_pk_fma_f32 v[86:87], v[230:231], v[64:65], v[86:87] op_sel_hi:[0,1,1]
	v_mov_b32_e32 v88, v231
	v_pk_fma_f32 v[86:87], v[88:89], v[60:61], v[86:87] op_sel_hi:[0,1,1]
	s_waitcnt lgkmcnt(5)
	v_pk_fma_f32 v[92:93], v[66:67], v[232:233], v[94:95] op_sel_hi:[1,0,1]
	s_nop 0
	v_pk_fma_f32 v[88:89], v[232:233], v[62:63], v[92:93] op_sel:[1,0,0]
	s_nop 0
	v_pk_fma_f32 v[88:89], v[234:235], v[64:65], v[88:89] op_sel_hi:[0,1,1]
	v_mov_b32_e32 v90, v235
	v_pk_fma_f32 v[88:89], v[90:91], v[60:61], v[88:89] op_sel_hi:[0,1,1]
	s_waitcnt lgkmcnt(4)
	v_pk_fma_f32 v[94:95], v[66:67], v[242:243], v[96:97] op_sel_hi:[1,0,1]
	s_nop 0
	v_pk_fma_f32 v[90:91], v[242:243], v[62:63], v[94:95] op_sel:[1,0,0]
	s_nop 0
	v_pk_fma_f32 v[90:91], v[244:245], v[64:65], v[90:91] op_sel_hi:[0,1,1]
	v_mov_b32_e32 v92, v245
	v_pk_fma_f32 v[90:91], v[92:93], v[60:61], v[90:91] op_sel_hi:[0,1,1]
	s_waitcnt lgkmcnt(3)
	v_pk_fma_f32 v[96:97], v[66:67], v[246:247], v[98:99] op_sel_hi:[1,0,1]
	s_nop 0
	v_pk_fma_f32 v[92:93], v[246:247], v[62:63], v[96:97] op_sel:[1,0,0]
	s_nop 0
	v_pk_fma_f32 v[92:93], v[248:249], v[64:65], v[92:93] op_sel_hi:[0,1,1]
	v_mov_b32_e32 v94, v249
	v_pk_fma_f32 v[92:93], v[94:95], v[60:61], v[92:93] op_sel_hi:[0,1,1]
	s_waitcnt lgkmcnt(2)
	v_pk_fma_f32 v[98:99], v[66:67], v[250:251], v[100:101] op_sel_hi:[1,0,1]
	s_nop 0
	v_pk_fma_f32 v[94:95], v[250:251], v[62:63], v[98:99] op_sel:[1,0,0]
	s_nop 0
	v_pk_fma_f32 v[94:95], v[252:253], v[64:65], v[94:95] op_sel_hi:[0,1,1]
	v_mov_b32_e32 v96, v253
	v_pk_fma_f32 v[94:95], v[96:97], v[60:61], v[94:95] op_sel_hi:[0,1,1]
	s_waitcnt lgkmcnt(1)
	v_pk_fma_f32 v[100:101], v[66:67], v[162:163], v[102:103] op_sel_hi:[1,0,1]
	s_nop 0
	v_pk_fma_f32 v[96:97], v[162:163], v[62:63], v[100:101] op_sel:[1,0,0]
	s_nop 0
	v_pk_fma_f32 v[96:97], v[164:165], v[64:65], v[96:97] op_sel_hi:[0,1,1]
	v_mov_b32_e32 v98, v165
	v_pk_fma_f32 v[96:97], v[98:99], v[60:61], v[96:97] op_sel_hi:[0,1,1]
	s_waitcnt lgkmcnt(0)
	v_pk_fma_f32 v[66:67], v[66:67], v[166:167], v[104:105] op_sel_hi:[1,0,1]
	s_nop 0
	v_pk_fma_f32 v[62:63], v[166:167], v[62:63], v[66:67] op_sel:[1,0,0]
	s_nop 0
	v_pk_fma_f32 v[62:63], v[168:169], v[64:65], v[62:63] op_sel_hi:[0,1,1]
	v_mov_b32_e32 v64, v169
	v_pk_fma_f32 v[60:61], v[64:65], v[60:61], v[62:63] op_sel_hi:[0,1,1]
	v_mbcnt_lo_u32_b32 v242, -1, 0
	v_mbcnt_hi_u32_b32 v242, -1, v242
	v_lshlrev_b32_e32 v242, 4, v242
	v_mov_b32_e32 v243, 0
	v_lshl_add_u64 v[244:245], s[34:35], 0, v[242:243]
	global_load_dwordx4 v[158:161], v[244:245], off
	global_load_dwordx4 v[162:165], v[244:245], off offset:1024
	global_load_dwordx4 v[166:169], v[244:245], off offset:2048
	global_load_dwordx4 v[170:173], v[244:245], off offset:3072
	v_add_co_u32_e32 v244, vcc, 0x1000, v244
	s_nop 1
	v_addc_co_u32_e32 v245, vcc, 0, v245, vcc
	global_load_dwordx4 v[174:177], v[244:245], off
	global_load_dwordx4 v[178:181], v[244:245], off offset:1024
	global_load_dwordx4 v[182:185], v[244:245], off offset:2048
	global_load_dwordx4 v[186:189], v[244:245], off offset:3072
	v_lshl_add_u64 v[244:245], s[36:37], 0, v[242:243]
	global_load_dwordx4 v[198:201], v[244:245], off
	global_load_dwordx4 v[202:205], v[244:245], off offset:1024
	global_load_dwordx4 v[216:219], v[244:245], off offset:2048
	global_load_dwordx4 v[220:223], v[244:245], off offset:3072
	v_add_co_u32_e32 v244, vcc, 0x1000, v244
	s_nop 1
	v_addc_co_u32_e32 v245, vcc, 0, v245, vcc
	global_load_dwordx4 v[224:227], v[244:245], off
	global_load_dwordx4 v[228:231], v[244:245], off offset:1024
	global_load_dwordx4 v[232:235], v[244:245], off offset:2048
	global_load_dwordx4 v[246:249], v[244:245], off offset:3072
	s_nop 1
	v_permlane32_swap_b32_e32 v60, v61
	v_permlane32_swap_b32_e32 v68, v69
	v_permlane32_swap_b32_e32 v70, v71
	v_permlane32_swap_b32_e32 v72, v73
	v_permlane32_swap_b32_e32 v74, v75
	v_permlane32_swap_b32_e32 v76, v77
	v_permlane32_swap_b32_e32 v78, v79
	v_permlane32_swap_b32_e32 v80, v81
	v_permlane32_swap_b32_e32 v82, v83
	v_permlane32_swap_b32_e32 v84, v85
	v_permlane32_swap_b32_e32 v86, v87
	v_permlane32_swap_b32_e32 v88, v89
	v_permlane32_swap_b32_e32 v90, v91
	v_permlane32_swap_b32_e32 v92, v93
	v_permlane32_swap_b32_e32 v94, v95
	v_permlane32_swap_b32_e32 v96, v97
	v_add_f32_e32 v60, v60, v61
	v_add_f32_e32 v68, v68, v69
	v_add_f32_e32 v70, v70, v71
	v_add_f32_e32 v72, v72, v73
	v_add_f32_e32 v74, v74, v75
	v_add_f32_e32 v76, v76, v77
	v_add_f32_e32 v78, v78, v79
	v_add_f32_e32 v80, v80, v81
	v_add_f32_e32 v82, v82, v83
	v_add_f32_e32 v84, v84, v85
	v_add_f32_e32 v86, v86, v87
	v_add_f32_e32 v88, v88, v89
	v_add_f32_e32 v90, v90, v91
	v_add_f32_e32 v92, v92, v93
	v_add_f32_e32 v94, v94, v95
	v_add_f32_e32 v96, v96, v97
	s_nop 1
	v_add_f32_dpp v62, v68, v68 quad_perm:[1,0,3,2] row_mask:0xf bank_mask:0xf bound_ctrl:1
	s_nop 0
	v_add_f32_dpp v60, v60, v60 quad_perm:[1,0,3,2] row_mask:0xf bank_mask:0xf bound_ctrl:1
	v_add_f32_dpp v68, v94, v94 quad_perm:[1,0,3,2] row_mask:0xf bank_mask:0xf bound_ctrl:1
	v_add_f32_dpp v62, v62, v62 quad_perm:[2,3,0,1] row_mask:0xf bank_mask:0xf bound_ctrl:1
	v_add_f32_dpp v60, v60, v60 quad_perm:[2,3,0,1] row_mask:0xf bank_mask:0xf bound_ctrl:1
	v_add_f32_dpp v68, v68, v68 quad_perm:[2,3,0,1] row_mask:0xf bank_mask:0xf bound_ctrl:1
	v_add_f32_dpp v62, v62, v62 row_ror:4 row_mask:0xf bank_mask:0xf bound_ctrl:1
	v_add_f32_dpp v60, v60, v60 row_ror:4 row_mask:0xf bank_mask:0xf bound_ctrl:1
	v_add_f32_dpp v68, v68, v68 row_ror:4 row_mask:0xf bank_mask:0xf bound_ctrl:1
	v_add_f32_dpp v62, v62, v62 row_ror:8 row_mask:0xf bank_mask:0xf bound_ctrl:1
	v_mov_b32_e32 v63, v62
	s_nop 1
	v_permlane16_swap_b32_e32 v62, v63
	v_add_f32_e32 v62, v62, v63
	v_mov_b32_e32 v63, v62
	s_nop 1
	s_nop 0
	v_mov_b32_e32 v62, v62
	s_nop 0
	v_add_f32_dpp v63, v70, v70 quad_perm:[1,0,3,2] row_mask:0xf bank_mask:0xf bound_ctrl:1
	v_mul_f32_e32 v62, 0xbfb8aa3b, v62
	v_exp_f32_e32 v62, v62
	v_add_f32_dpp v63, v63, v63 quad_perm:[2,3,0,1] row_mask:0xf bank_mask:0xf bound_ctrl:1
	v_add_f32_dpp v60, v60, v60 row_ror:8 row_mask:0xf bank_mask:0xf bound_ctrl:1
	v_add_f32_dpp v68, v68, v68 row_ror:8 row_mask:0xf bank_mask:0xf bound_ctrl:1
	v_add_f32_dpp v63, v63, v63 row_ror:4 row_mask:0xf bank_mask:0xf bound_ctrl:1
	v_add_f32_e32 v62, 1.0, v62
	v_rcp_f32_e32 v62, v62
	v_add_f32_dpp v63, v63, v63 row_ror:8 row_mask:0xf bank_mask:0xf bound_ctrl:1
	v_mov_b32_e32 v64, v63
	s_nop 1
	v_permlane16_swap_b32_e32 v63, v64
	v_add_f32_e32 v63, v63, v64
	v_mov_b32_e32 v64, v63
	s_nop 1
	s_nop 0
	v_mov_b32_e32 v63, v63
	s_nop 0
	v_add_f32_dpp v64, v72, v72 quad_perm:[1,0,3,2] row_mask:0xf bank_mask:0xf bound_ctrl:1
	v_mul_f32_e32 v63, 0xbfb8aa3b, v63
	v_exp_f32_e32 v63, v63
	v_add_f32_dpp v64, v64, v64 quad_perm:[2,3,0,1] row_mask:0xf bank_mask:0xf bound_ctrl:1
	v_add_f32_dpp v72, v96, v96 quad_perm:[1,0,3,2] row_mask:0xf bank_mask:0xf bound_ctrl:1
	v_mov_b32_e32 v70, v68
	v_add_f32_dpp v64, v64, v64 row_ror:4 row_mask:0xf bank_mask:0xf bound_ctrl:1
	v_add_f32_e32 v63, 1.0, v63
	v_rcp_f32_e32 v63, v63
	v_add_f32_dpp v64, v64, v64 row_ror:8 row_mask:0xf bank_mask:0xf bound_ctrl:1
	v_mov_b32_e32 v65, v64
	s_nop 1
	v_permlane16_swap_b32_e32 v64, v65
	v_add_f32_e32 v64, v64, v65
	v_mov_b32_e32 v65, v64
	s_nop 1
	s_nop 0
	v_mov_b32_e32 v64, v64
	s_nop 0
	v_add_f32_dpp v65, v76, v76 quad_perm:[1,0,3,2] row_mask:0xf bank_mask:0xf bound_ctrl:1
	v_mul_f32_e32 v64, 0xbfb8aa3b, v64
	v_exp_f32_e32 v64, v64
	v_add_f32_dpp v65, v65, v65 quad_perm:[2,3,0,1] row_mask:0xf bank_mask:0xf bound_ctrl:1
	v_mov_b32_e32 v76, v60
	s_nop 1
	v_permlane16_swap_b32_e32 v60, v76
	v_add_f32_dpp v65, v65, v65 row_ror:4 row_mask:0xf bank_mask:0xf bound_ctrl:1
	v_add_f32_e32 v64, 1.0, v64
	v_rcp_f32_e32 v102, v64
	v_add_f32_dpp v65, v65, v65 row_ror:8 row_mask:0xf bank_mask:0xf bound_ctrl:1
	v_mov_b32_e32 v66, v65
	s_nop 1
	v_permlane16_swap_b32_e32 v65, v66
	v_add_f32_e32 v65, v65, v66
	v_mov_b32_e32 v66, v65
	s_nop 1
	s_nop 0
	v_mov_b32_e32 v65, v65
	s_nop 0
	v_add_f32_dpp v66, v74, v74 quad_perm:[1,0,3,2] row_mask:0xf bank_mask:0xf bound_ctrl:1
	v_mul_f32_e32 v65, 0xbfb8aa3b, v65
	v_exp_f32_e32 v65, v65
	v_add_f32_dpp v66, v66, v66 quad_perm:[2,3,0,1] row_mask:0xf bank_mask:0xf bound_ctrl:1
	v_add_f32_e32 v111, v14, v102
	v_add_f32_e32 v76, v60, v76
	v_add_f32_dpp v66, v66, v66 row_ror:4 row_mask:0xf bank_mask:0xf bound_ctrl:1
	v_add_f32_e32 v64, 1.0, v65
	v_rcp_f32_e32 v104, v64
	v_add_f32_dpp v66, v66, v66 row_ror:8 row_mask:0xf bank_mask:0xf bound_ctrl:1
	v_mov_b32_e32 v67, v66
	s_nop 1
	v_permlane16_swap_b32_e32 v66, v67
	v_add_f32_e32 v101, v66, v67
	s_nop 0
	v_add_f32_dpp v66, v78, v78 quad_perm:[1,0,3,2] row_mask:0xf bank_mask:0xf bound_ctrl:1
	v_pk_add_f32 v[64:65], v[12:13], v[62:63]
	v_add_f32_e32 v112, v15, v104
	v_add_f32_dpp v66, v66, v66 quad_perm:[2,3,0,1] row_mask:0xf bank_mask:0xf bound_ctrl:1
	v_cmp_gt_f32_e32 vcc, v65, v64
	v_add_f32_dpp v72, v72, v72 quad_perm:[2,3,0,1] row_mask:0xf bank_mask:0xf bound_ctrl:1
	v_add_f32_dpp v66, v66, v66 row_ror:4 row_mask:0xf bank_mask:0xf bound_ctrl:1
	v_cndmask_b32_e32 v60, v64, v65, vcc
	v_cmp_gt_f32_e64 s[6:7], v111, v60
	v_add_f32_dpp v66, v66, v66 row_ror:8 row_mask:0xf bank_mask:0xf bound_ctrl:1
	v_mov_b32_e32 v67, v66
	s_nop 1
	v_permlane16_swap_b32_e32 v66, v67
	v_add_f32_e32 v105, v66, v67
	s_nop 0
	v_add_f32_dpp v66, v80, v80 quad_perm:[1,0,3,2] row_mask:0xf bank_mask:0xf bound_ctrl:1
	v_cndmask_b32_e64 v80, 0, 1, vcc
	v_cndmask_b32_e64 v60, v60, v111, s[6:7]
	v_add_f32_dpp v66, v66, v66 quad_perm:[2,3,0,1] row_mask:0xf bank_mask:0xf bound_ctrl:1
	v_cndmask_b32_e64 v80, v80, 2, s[6:7]
	v_cmp_ngt_f32_e64 s[8:9], v112, v60
	v_add_f32_dpp v66, v66, v66 row_ror:4 row_mask:0xf bank_mask:0xf bound_ctrl:1
	v_add_f32_dpp v72, v72, v72 row_ror:4 row_mask:0xf bank_mask:0xf bound_ctrl:1
	v_permlane16_swap_b32_e32 v68, v70
	v_add_f32_dpp v66, v66, v66 row_ror:8 row_mask:0xf bank_mask:0xf bound_ctrl:1
	v_mov_b32_e32 v67, v66
	s_nop 1
	v_permlane16_swap_b32_e32 v66, v67
	v_add_f32_e32 v107, v66, v67
	s_nop 0
	v_add_f32_dpp v66, v82, v82 quad_perm:[1,0,3,2] row_mask:0xf bank_mask:0xf bound_ctrl:1
	v_add_f32_dpp v72, v72, v72 row_ror:8 row_mask:0xf bank_mask:0xf bound_ctrl:1
	v_mov_b32_e32 v74, v72
	v_add_f32_dpp v66, v66, v66 quad_perm:[2,3,0,1] row_mask:0xf bank_mask:0xf bound_ctrl:1
	s_nop 0
	v_permlane16_swap_b32_e32 v72, v74
	v_add_f32_dpp v66, v66, v66 row_ror:4 row_mask:0xf bank_mask:0xf bound_ctrl:1
	v_add_f32_e32 v68, v68, v70
	v_add_f32_e32 v72, v72, v74
	v_add_f32_dpp v66, v66, v66 row_ror:8 row_mask:0xf bank_mask:0xf bound_ctrl:1
	v_mov_b32_e32 v67, v66
	s_nop 1
	v_permlane16_swap_b32_e32 v66, v67
	v_add_f32_e32 v109, v66, v67
	s_nop 0
	v_add_f32_dpp v66, v84, v84 quad_perm:[1,0,3,2] row_mask:0xf bank_mask:0xf bound_ctrl:1
	v_cndmask_b32_e64 v94, v112, v60, s[8:9]
	v_mov_b32_e32 v103, v101
	v_add_f32_dpp v66, v66, v66 quad_perm:[2,3,0,1] row_mask:0xf bank_mask:0xf bound_ctrl:1
	v_mov_b32_e32 v106, v105
	v_mov_b32_e32 v108, v107
	v_add_f32_dpp v66, v66, v66 row_ror:4 row_mask:0xf bank_mask:0xf bound_ctrl:1
	v_mov_b32_e32 v110, v109
	v_mov_b32_e32 v70, v68
	v_add_f32_dpp v66, v66, v66 row_ror:8 row_mask:0xf bank_mask:0xf bound_ctrl:1
	v_mov_b32_e32 v67, v66
	s_nop 1
	v_permlane16_swap_b32_e32 v66, v67
	v_add_f32_e32 v82, v66, v67
	s_nop 0
	v_add_f32_dpp v66, v86, v86 quad_perm:[1,0,3,2] row_mask:0xf bank_mask:0xf bound_ctrl:1
	v_mov_b32_e32 v84, v82
	v_mov_b32_e32 v74, v72
	v_add_f32_dpp v66, v66, v66 quad_perm:[2,3,0,1] row_mask:0xf bank_mask:0xf bound_ctrl:1
	v_mov_b32_e32 v78, v76
	s_nop 0
	v_add_f32_dpp v66, v66, v66 row_ror:4 row_mask:0xf bank_mask:0xf bound_ctrl:1
	s_nop 0
	s_nop 0
	v_add_f32_dpp v66, v66, v66 row_ror:8 row_mask:0xf bank_mask:0xf bound_ctrl:1
	v_mov_b32_e32 v67, v66
	s_nop 1
	v_permlane16_swap_b32_e32 v66, v67
	v_add_f32_e32 v86, v66, v67
	s_nop 0
	v_add_f32_dpp v66, v88, v88 quad_perm:[1,0,3,2] row_mask:0xf bank_mask:0xf bound_ctrl:1
	v_mov_b32_e32 v98, v86
	s_nop 0
	v_add_f32_dpp v66, v66, v66 quad_perm:[2,3,0,1] row_mask:0xf bank_mask:0xf bound_ctrl:1
	s_nop 0
	s_nop 0
	v_add_f32_dpp v66, v66, v66 row_ror:4 row_mask:0xf bank_mask:0xf bound_ctrl:1
	s_nop 0
	s_nop 0
	v_add_f32_dpp v66, v66, v66 row_ror:8 row_mask:0xf bank_mask:0xf bound_ctrl:1
	v_mov_b32_e32 v67, v66
	s_nop 1
	v_permlane16_swap_b32_e32 v66, v67
	v_add_f32_e32 v88, v66, v67
	s_nop 0
	v_add_f32_dpp v66, v90, v90 quad_perm:[1,0,3,2] row_mask:0xf bank_mask:0xf bound_ctrl:1
	v_mov_b32_e32 v99, v88
	s_nop 0
	v_add_f32_dpp v66, v66, v66 quad_perm:[2,3,0,1] row_mask:0xf bank_mask:0xf bound_ctrl:1
	s_nop 0
	s_nop 0
	v_add_f32_dpp v66, v66, v66 row_ror:4 row_mask:0xf bank_mask:0xf bound_ctrl:1
	s_nop 0
	s_nop 0
	v_add_f32_dpp v66, v66, v66 row_ror:8 row_mask:0xf bank_mask:0xf bound_ctrl:1
	v_mov_b32_e32 v67, v66
	s_nop 1
	v_permlane16_swap_b32_e32 v66, v67
	v_add_f32_e32 v90, v66, v67
	s_nop 0
	v_add_f32_dpp v66, v92, v92 quad_perm:[1,0,3,2] row_mask:0xf bank_mask:0xf bound_ctrl:1
	v_cndmask_b32_e64 v92, 3, v80, s[8:9]
	v_mov_b32_e32 v80, 0xff800000
	v_cmp_eq_u32_e64 s[10:11], 0, v92
	v_cmp_nlg_f32_e64 s[12:13], v64, v80
	s_or_b64 s[10:11], s[10:11], s[12:13]
	v_cndmask_b32_e64 v64, v64, v80, s[10:11]
	v_cmp_ne_u32_e64 s[12:13], 1, v92
	v_cmp_gt_f32_e64 s[14:15], v65, v64
	s_and_b64 s[12:13], s[12:13], s[14:15]
	v_cndmask_b32_e64 v64, v64, v65, s[12:13]
	v_add_f32_dpp v66, v66, v66 quad_perm:[2,3,0,1] row_mask:0xf bank_mask:0xf bound_ctrl:1
	v_cmp_ne_u32_e64 s[14:15], 2, v92
	v_cmp_gt_f32_e64 s[16:17], v111, v64
	v_add_f32_dpp v66, v66, v66 row_ror:4 row_mask:0xf bank_mask:0xf bound_ctrl:1
	s_and_b64 s[14:15], s[14:15], s[16:17]
	v_cndmask_b32_e64 v64, v64, v111, s[14:15]
	v_add_f32_dpp v66, v66, v66 row_ror:8 row_mask:0xf bank_mask:0xf bound_ctrl:1
	v_mov_b32_e32 v67, v66
	v_cmp_gt_f32_e64 s[16:17], v112, v64
	s_nop 0
	v_permlane16_swap_b32_e32 v66, v67
	s_and_b64 s[16:17], s[8:9], s[16:17]
	v_add_f32_e32 v66, v66, v67
	v_cndmask_b32_e64 v64, v64, v112, s[16:17]
	v_mov_b32_e32 v100, v90
	v_mov_b32_e32 v67, v66
	v_add_f32_e32 v94, v94, v64
	s_nop 0
	s_nop 0
	s_nop 0
	s_nop 0
	v_mov_b32_e32 v60, 1
	v_cmp_lg_f32_e64 s[18:19], v94, v80
	v_mov_b32_e32 v65, 0
	v_mov_b32_e32 v64, 0
	s_and_saveexec_b64 s[46:47], s[18:19]
	s_cbranch_execz .LBB0_891
	v_cndmask_b32_e64 v35, 0, 1, s[12:13]
	v_cndmask_b32_e64 v35, v35, 2, s[14:15]
	v_cndmask_b32_e64 v60, v35, 3, s[16:17]
	v_cndmask_b32_e64 v35, v62, 0, s[10:11]
	v_cndmask_b32_e64 v35, v35, v63, s[12:13]
	v_cndmask_b32_e32 v62, v62, v63, vcc
	v_cndmask_b32_e64 v35, v35, v102, s[14:15]
	v_cndmask_b32_e64 v62, v62, v102, s[6:7]
	v_cndmask_b32_e64 v35, v35, v104, s[16:17]
	v_cndmask_b32_e64 v65, v104, v62, s[8:9]
	v_mov_b32_e32 v64, v92
	v_mov_b32_e32 v80, v94

.LBB0_899:
	s_or_b64 exec, exec, s[6:7]
	s_waitcnt vmcnt(0)
	v_lshlrev_b32_e32 v80, 16, v58
	v_and_b32_e32 v81, 0xffff0000, v58
	v_lshlrev_b32_e32 v78, 16, v59
	v_and_b32_e32 v79, 0xffff0000, v59
	v_add_f32_e32 v35, v80, v81
	v_add_f32_e32 v58, v78, v79
	v_lshlrev_b32_e32 v62, 16, v56
	v_and_b32_e32 v63, 0xffff0000, v56
	v_lshlrev_b32_e32 v60, 16, v57
	v_and_b32_e32 v61, 0xffff0000, v57
	v_add_f32_e32 v35, v35, v58
	v_add_f32_e32 v56, v62, v63
	v_add_f32_e32 v57, v60, v61
	v_lshlrev_b32_e32 v68, 16, v54
	v_and_b32_e32 v69, 0xffff0000, v54
	v_lshlrev_b32_e32 v70, 16, v55
	v_and_b32_e32 v71, 0xffff0000, v55
	v_add_f32_e32 v35, 0, v35
	v_add_f32_e32 v56, v56, v57
	v_add_f32_e32 v54, v68, v69
	v_add_f32_e32 v55, v70, v71
	v_lshlrev_b32_e32 v72, 16, v52
	v_and_b32_e32 v73, 0xffff0000, v52
	v_lshlrev_b32_e32 v74, 16, v53
	v_and_b32_e32 v75, 0xffff0000, v53
	v_add_f32_e32 v35, v35, v56
	v_add_f32_e32 v54, v54, v55
	v_add_f32_e32 v52, v72, v73
	v_add_f32_e32 v53, v74, v75
	v_lshlrev_b32_e32 v64, 16, v50
	v_and_b32_e32 v65, 0xffff0000, v50
	v_lshlrev_b32_e32 v66, 16, v51
	v_and_b32_e32 v67, 0xffff0000, v51
	v_add_f32_e32 v35, v35, v54
	v_add_f32_e32 v52, v52, v53
	v_add_f32_e32 v50, v64, v65
	v_add_f32_e32 v51, v66, v67
	v_lshlrev_b32_e32 v56, 16, v48
	v_and_b32_e32 v57, 0xffff0000, v48
	v_lshlrev_b32_e32 v58, 16, v49
	v_and_b32_e32 v59, 0xffff0000, v49
	v_add_f32_e32 v35, v35, v52
	v_add_f32_e32 v50, v50, v51
	v_add_f32_e32 v48, v56, v57
	v_add_f32_e32 v49, v58, v59
	v_lshlrev_b32_e32 v52, 16, v46
	v_and_b32_e32 v53, 0xffff0000, v46
	v_lshlrev_b32_e32 v54, 16, v47
	v_and_b32_e32 v55, 0xffff0000, v47
	v_add_f32_e32 v35, v35, v50
	v_add_f32_e32 v48, v48, v49
	v_add_f32_e32 v46, v52, v53
	v_add_f32_e32 v47, v54, v55
	v_add_f32_e32 v35, v35, v48
	v_add_f32_e32 v46, v46, v47
	v_add_f32_e32 v35, v35, v46
	v_lshlrev_b32_e32 v46, 16, v44
	v_and_b32_e32 v47, 0xffff0000, v44
	v_lshlrev_b32_e32 v44, 16, v45
	v_and_b32_e32 v45, 0xffff0000, v45
	v_add_f32_e32 v48, v46, v47
	v_add_f32_e32 v49, v44, v45
	v_add_f32_e32 v48, v48, v49
	v_add_f32_e32 v35, v35, v48
	s_mov_b64 s[6:7], s[34:35]
	s_mov_b64 s[8:9], s[36:37]
	v_add_f32_dpp v35, v35, v35 quad_perm:[1,0,3,2] row_mask:0xf bank_mask:0xf bound_ctrl:1
	v_lshl_add_u64 v[92:93], s[6:7], 0, v[192:193]
	s_lshl_b64 s[6:7], s[38:39], 11
	v_add_f32_dpp v35, v35, v35 quad_perm:[2,3,0,1] row_mask:0xf bank_mask:0xf bound_ctrl:1
	v_lshl_add_u64 v[94:95], s[8:9], 0, v[192:193]
	v_add_co_u32_e32 v98, vcc, s33, v92
	v_add_f32_dpp v35, v35, v35 row_ror:4 row_mask:0xf bank_mask:0xf bound_ctrl:1
	s_nop 0
	v_addc_co_u32_e32 v99, vcc, 0, v93, vcc
	v_add_f32_dpp v35, v35, v35 row_ror:8 row_mask:0xf bank_mask:0xf bound_ctrl:1
	v_mov_b32_e32 v48, v35
	s_nop 1
	v_permlane16_swap_b32_e32 v35, v48
	v_add_f32_e32 v35, v35, v48
	v_mov_b32_e32 v48, v35
	s_nop 1
	v_permlane32_swap_b32_e32 v35, v48
	v_add_f32_e32 v35, v35, v48
	v_fmac_f32_e32 v79, 0xba000000, v35
	v_fmac_f32_e32 v81, 0xba000000, v35
	v_fmac_f32_e32 v78, 0xba000000, v35
	v_fmac_f32_e32 v80, 0xba000000, v35
	v_mul_f32_e32 v48, v81, v81
	v_mul_f32_e32 v49, v79, v79
	v_fmac_f32_e32 v48, v80, v80
	v_fmac_f32_e32 v49, v78, v78
	v_fmac_f32_e32 v61, 0xba000000, v35
	v_fmac_f32_e32 v63, 0xba000000, v35
	v_add_f32_e32 v48, v48, v49
	v_fmac_f32_e32 v60, 0xba000000, v35
	v_fmac_f32_e32 v62, 0xba000000, v35
	v_mul_f32_e32 v49, v63, v63
	v_mul_f32_e32 v50, v61, v61
	v_fmac_f32_e32 v49, v62, v62
	v_fmac_f32_e32 v50, v60, v60
	v_add_f32_e32 v49, v49, v50
	v_add_f32_e32 v76, v48, v49
	s_nop 0
	v_fmac_f32_e32 v71, 0xba000000, v35
	v_fmac_f32_e32 v69, 0xba000000, v35
	v_fmac_f32_e32 v70, 0xba000000, v35
	v_fmac_f32_e32 v68, 0xba000000, v35
	v_mul_f32_e32 v77, v69, v69
	v_mul_f32_e32 v82, v71, v71
	v_fmac_f32_e32 v77, v68, v68
	v_fmac_f32_e32 v82, v70, v70
	v_add_f32_e32 v77, v77, v82
	v_fmac_f32_e32 v75, 0xba000000, v35
	v_fmac_f32_e32 v73, 0xba000000, v35
	v_add_f32_e32 v76, v76, v77
	v_fmac_f32_e32 v74, 0xba000000, v35
	v_fmac_f32_e32 v72, 0xba000000, v35
	v_mul_f32_e32 v77, v73, v73
	v_mul_f32_e32 v82, v75, v75
	v_fmac_f32_e32 v77, v72, v72
	v_fmac_f32_e32 v82, v74, v74
	v_add_f32_e32 v77, v77, v82
	v_fmac_f32_e32 v67, 0xba000000, v35
	v_fmac_f32_e32 v65, 0xba000000, v35
	v_add_f32_e32 v76, v76, v77
	v_fmac_f32_e32 v66, 0xba000000, v35
	v_fmac_f32_e32 v64, 0xba000000, v35
	v_mul_f32_e32 v77, v65, v65
	v_mul_f32_e32 v82, v67, v67
	v_fmac_f32_e32 v77, v64, v64
	v_fmac_f32_e32 v82, v66, v66
	v_add_f32_e32 v77, v77, v82
	v_fmac_f32_e32 v59, 0xba000000, v35
	v_fmac_f32_e32 v57, 0xba000000, v35
	v_add_f32_e32 v76, v76, v77
	v_fmac_f32_e32 v58, 0xba000000, v35
	v_fmac_f32_e32 v56, 0xba000000, v35
	v_mul_f32_e32 v77, v57, v57
	v_mul_f32_e32 v82, v59, v59
	v_fmac_f32_e32 v77, v56, v56
	v_fmac_f32_e32 v82, v58, v58
	v_add_f32_e32 v77, v77, v82
	v_fmac_f32_e32 v55, 0xba000000, v35
	v_fmac_f32_e32 v53, 0xba000000, v35
	v_add_f32_e32 v76, v76, v77
	v_fmac_f32_e32 v54, 0xba000000, v35
	v_fmac_f32_e32 v52, 0xba000000, v35
	v_mul_f32_e32 v77, v53, v53
	v_mul_f32_e32 v82, v55, v55
	v_fmac_f32_e32 v77, v52, v52
	v_fmac_f32_e32 v82, v54, v54
	v_add_f32_e32 v77, v77, v82
	v_fmac_f32_e32 v45, 0xba000000, v35
	v_fmac_f32_e32 v47, 0xba000000, v35
	v_add_f32_e32 v76, v76, v77
	v_fmac_f32_e32 v44, 0xba000000, v35
	v_fmac_f32_e32 v46, 0xba000000, v35
	v_mul_f32_e32 v35, v47, v47
	v_mul_f32_e32 v77, v45, v45
	v_fmac_f32_e32 v35, v46, v46
	v_fmac_f32_e32 v77, v44, v44
	v_add_f32_e32 v35, v35, v77
	v_add_f32_e32 v35, v76, v35
	v_lshl_add_u64 v[82:83], v[30:31], 0, s[6:7]
	v_add_co_u32_e32 v100, vcc, s33, v94
	v_add_f32_dpp v35, v35, v35 quad_perm:[1,0,3,2] row_mask:0xf bank_mask:0xf bound_ctrl:1
	s_nop 0
	v_addc_co_u32_e32 v101, vcc, 0, v95, vcc
	v_add_f32_dpp v35, v35, v35 quad_perm:[2,3,0,1] row_mask:0xf bank_mask:0xf bound_ctrl:1
	s_nop 1
	v_add_f32_dpp v35, v35, v35 row_ror:4 row_mask:0xf bank_mask:0xf bound_ctrl:1
	s_nop 1
	v_add_f32_dpp v35, v35, v35 row_ror:8 row_mask:0xf bank_mask:0xf bound_ctrl:1
	v_mov_b32_e32 v76, v35
	s_nop 1
	v_permlane16_swap_b32_e32 v35, v76
	v_add_f32_e32 v35, v35, v76
	v_mov_b32_e32 v76, v35
	s_nop 1
	v_permlane32_swap_b32_e32 v35, v76
	v_add_f32_e32 v35, v35, v76
	v_fmamk_f32 v35, v35, 0x3a000000, v207
	v_rsq_f32_e32 v96, v35
	v_lshl_add_u64 v[76:77], v[28:29], 0, s[44:45]
	v_pk_mul_f32 v[80:81], v[96:97], v[80:81] op_sel_hi:[0,1]
	s_waitcnt vmcnt(0) lgkmcnt(0)
	v_pk_fma_f32 v[48:49], v[158:159], v[80:81], v[198:199]
	v_mov_b32_e32 v81, 0
	v_med3_f32 v35, v48, s69, v208
	v_med3_f32 v80, v49, s69, v208
	v_cvt_pk_fp8_f32 v81, v35, v80
	v_pk_mul_f32 v[78:79], v[96:97], v[78:79] op_sel_hi:[0,1]
	v_pk_fma_f32 v[50:51], v[160:161], v[78:79], v[200:201]
	v_pk_mul_f32 v[62:63], v[96:97], v[62:63] op_sel_hi:[0,1]
	v_med3_f32 v35, v50, s69, v208
	v_med3_f32 v78, v51, s69, v208
	v_cvt_pk_fp8_f32 v81, v35, v78 op_sel:[0,0,1]
	v_cvt_pk_bf16_f32 v78, v48, v49
	v_cvt_pk_bf16_f32 v79, v50, v51
	global_store_dwordx2 v[76:77], v[78:79], off nt
	global_store_dword v[82:83], v81, off nt
	s_nop 0
	s_nop 0
	v_pk_mul_f32 v[88:89], v[96:97], v[60:61] op_sel_hi:[0,1]
	v_pk_mul_f32 v[68:69], v[96:97], v[68:69] op_sel_hi:[0,1]
	v_pk_mul_f32 v[72:73], v[96:97], v[72:73] op_sel_hi:[0,1]
	v_pk_mul_f32 v[74:75], v[96:97], v[74:75] op_sel_hi:[0,1]
	v_pk_mul_f32 v[64:65], v[96:97], v[64:65] op_sel_hi:[0,1]
	v_pk_mul_f32 v[66:67], v[96:97], v[66:67] op_sel_hi:[0,1]
	v_pk_mul_f32 v[56:57], v[96:97], v[56:57] op_sel_hi:[0,1]
	v_pk_mul_f32 v[58:59], v[96:97], v[58:59] op_sel_hi:[0,1]
	v_pk_mul_f32 v[52:53], v[96:97], v[52:53] op_sel_hi:[0,1]
	v_pk_mul_f32 v[54:55], v[96:97], v[54:55] op_sel_hi:[0,1]
	v_pk_mul_f32 v[46:47], v[96:97], v[46:47] op_sel_hi:[0,1]
	v_pk_mul_f32 v[44:45], v[96:97], v[44:45] op_sel_hi:[0,1]
	s_nop 0
	v_pk_fma_f32 v[60:61], v[162:163], v[62:63], v[202:203]
	s_nop 0
	v_med3_f32 v35, v60, s69, v208
	v_med3_f32 v62, v61, s69, v208
	v_mov_b32_e32 v84, 0
	v_cvt_pk_fp8_f32 v84, v35, v62
	v_pk_fma_f32 v[62:63], v[164:165], v[88:89], v[204:205]
	v_pk_mul_f32 v[88:89], v[96:97], v[70:71] op_sel_hi:[0,1]
	v_med3_f32 v35, v62, s69, v208
	v_med3_f32 v78, v63, s69, v208
	v_cvt_pk_fp8_f32 v84, v35, v78 op_sel:[0,0,1]
	v_cvt_pk_bf16_f32 v78, v60, v61
	v_cvt_pk_bf16_f32 v79, v62, v63
	global_store_dwordx2 v[76:77], v[78:79], off offset:512 nt
	global_store_dword v[82:83], v84, off offset:256 nt
	s_nop 0
	s_nop 0
	v_mov_b32_e32 v35, 0
	s_nop 0
	v_pk_fma_f32 v[70:71], v[166:167], v[68:69], v[216:217]
	s_nop 0
	v_med3_f32 v68, v70, s69, v208
	v_med3_f32 v69, v71, s69, v208
	v_cvt_pk_fp8_f32 v35, v68, v69
	v_pk_fma_f32 v[68:69], v[168:169], v[88:89], v[218:219]
	s_nop 0
	v_med3_f32 v78, v68, s69, v208
	v_med3_f32 v79, v69, s69, v208
	v_cvt_pk_fp8_f32 v35, v78, v79 op_sel:[0,0,1]
	v_cvt_pk_bf16_f32 v78, v70, v71
	v_cvt_pk_bf16_f32 v79, v68, v69
	global_store_dwordx2 v[76:77], v[78:79], off offset:1024 nt
	global_store_dword v[82:83], v35, off offset:512 nt
	s_nop 0
	v_mov_b32_e32 v35, 0
	s_nop 0
	v_pk_fma_f32 v[80:81], v[170:171], v[72:73], v[220:221]
	s_nop 0
	v_med3_f32 v72, v80, s69, v208
	v_med3_f32 v73, v81, s69, v208
	v_cvt_pk_fp8_f32 v35, v72, v73
	v_pk_fma_f32 v[78:79], v[172:173], v[74:75], v[222:223]
	s_nop 0
	v_med3_f32 v72, v78, s69, v208
	v_med3_f32 v73, v79, s69, v208
	v_cvt_pk_fp8_f32 v35, v72, v73 op_sel:[0,0,1]
	v_cvt_pk_bf16_f32 v72, v80, v81
	v_cvt_pk_bf16_f32 v73, v78, v79
	global_store_dwordx2 v[76:77], v[72:73], off offset:1536 nt
	global_store_dword v[82:83], v35, off offset:768 nt
	s_nop 0
	s_nop 0
	v_mov_b32_e32 v35, 0
	s_nop 0
	v_pk_fma_f32 v[86:87], v[174:175], v[64:65], v[224:225]
	s_nop 0
	v_med3_f32 v64, v86, s69, v208
	v_med3_f32 v65, v87, s69, v208
	v_cvt_pk_fp8_f32 v35, v64, v65
	v_pk_fma_f32 v[84:85], v[176:177], v[66:67], v[226:227]
	s_nop 0
	v_med3_f32 v64, v84, s69, v208
	v_med3_f32 v65, v85, s69, v208
	v_cvt_pk_fp8_f32 v35, v64, v65 op_sel:[0,0,1]
	v_cvt_pk_bf16_f32 v64, v86, v87
	v_cvt_pk_bf16_f32 v65, v84, v85
	global_store_dwordx2 v[76:77], v[64:65], off offset:2048 nt
	global_store_dword v[82:83], v35, off offset:1024 nt
	s_nop 0
	s_nop 0
	v_mov_b32_e32 v35, 0
	s_nop 0
	v_pk_fma_f32 v[90:91], v[178:179], v[56:57], v[228:229]
	s_nop 0
	v_med3_f32 v56, v90, s69, v208
	v_med3_f32 v57, v91, s69, v208
	v_cvt_pk_fp8_f32 v35, v56, v57
	v_pk_fma_f32 v[88:89], v[180:181], v[58:59], v[230:231]
	s_nop 0
	v_med3_f32 v56, v88, s69, v208
	v_med3_f32 v57, v89, s69, v208
	v_cvt_pk_fp8_f32 v35, v56, v57 op_sel:[0,0,1]
	v_cvt_pk_bf16_f32 v56, v90, v91
	v_cvt_pk_bf16_f32 v57, v88, v89
	global_store_dwordx2 v[76:77], v[56:57], off offset:2560 nt
	global_store_dword v[82:83], v35, off offset:1280 nt
	s_nop 0
	s_nop 0
	v_mov_b32_e32 v35, 0
	s_nop 0
	v_pk_fma_f32 v[94:95], v[182:183], v[52:53], v[232:233]
	s_nop 0
	v_med3_f32 v52, v94, s69, v208
	v_med3_f32 v53, v95, s69, v208
	v_cvt_pk_fp8_f32 v35, v52, v53
	v_pk_fma_f32 v[92:93], v[184:185], v[54:55], v[234:235]
	s_nop 0
	v_med3_f32 v52, v92, s69, v208
	v_med3_f32 v53, v93, s69, v208
	v_cvt_pk_fp8_f32 v35, v52, v53 op_sel:[0,0,1]
	v_cvt_pk_bf16_f32 v52, v94, v95
	v_cvt_pk_bf16_f32 v53, v92, v93
	global_store_dwordx2 v[76:77], v[52:53], off offset:3072 nt
	global_store_dword v[82:83], v35, off offset:1536 nt
	s_nop 0
	s_nop 0
	v_mov_b32_e32 v35, 0
	s_nop 0
	v_pk_fma_f32 v[96:97], v[186:187], v[46:47], v[246:247]
	s_nop 0
	v_med3_f32 v46, v96, s69, v208
	v_med3_f32 v47, v97, s69, v208
	v_mov_b32_e32 v52, 0
	v_cvt_pk_fp8_f32 v52, v46, v47
	v_pk_fma_f32 v[98:99], v[188:189], v[44:45], v[248:249]
	s_nop 0
	v_med3_f32 v44, v98, s69, v208
	v_med3_f32 v45, v99, s69, v208
	v_cvt_pk_fp8_f32 v52, v44, v45 op_sel:[0,0,1]
	v_cvt_pk_bf16_f32 v44, v96, v97
	v_cvt_pk_bf16_f32 v45, v98, v99
	global_store_dwordx2 v[76:77], v[44:45], off offset:3584 nt
	global_store_dword v[82:83], v52, off offset:1792 nt
	v_lshlrev_b32_e32 v102, 16, v42
	v_and_b32_e32 v103, 0xffff0000, v42
	v_lshlrev_b32_e32 v100, 16, v43
	v_and_b32_e32 v101, 0xffff0000, v43
	v_add_f32_e32 v42, v102, v103
	v_add_f32_e32 v43, v100, v101
	v_lshlrev_b32_e32 v74, 16, v40
	v_and_b32_e32 v75, 0xffff0000, v40
	v_lshlrev_b32_e32 v72, 16, v41
	v_and_b32_e32 v73, 0xffff0000, v41
	v_add_f32_e32 v42, v42, v43
	v_add_f32_e32 v40, v74, v75
	v_add_f32_e32 v41, v72, v73
	v_lshlrev_b32_e32 v64, 16, v38
	v_and_b32_e32 v65, 0xffff0000, v38
	v_lshlrev_b32_e32 v66, 16, v39
	v_and_b32_e32 v67, 0xffff0000, v39
	v_add_f32_e32 v42, 0, v42
	v_add_f32_e32 v40, v40, v41
	v_add_f32_e32 v38, v64, v65
	v_add_f32_e32 v39, v66, v67
	v_lshlrev_b32_e32 v56, 16, v36
	v_and_b32_e32 v57, 0xffff0000, v36
	v_lshlrev_b32_e32 v58, 16, v37
	v_and_b32_e32 v59, 0xffff0000, v37
	v_add_f32_e32 v40, v42, v40
	v_add_f32_e32 v38, v38, v39
	v_add_f32_e32 v36, v56, v57
	v_add_f32_e32 v37, v58, v59
	v_lshlrev_b32_e32 v52, 16, v22
	v_and_b32_e32 v53, 0xffff0000, v22
	v_lshlrev_b32_e32 v54, 16, v23
	v_and_b32_e32 v55, 0xffff0000, v23
	v_add_f32_e32 v38, v40, v38
	v_add_f32_e32 v36, v36, v37
	v_add_f32_e32 v22, v52, v53
	v_add_f32_e32 v23, v54, v55
	v_add_f32_e32 v36, v38, v36
	v_add_f32_e32 v22, v22, v23
	v_lshlrev_b32_e32 v44, 16, v20
	v_and_b32_e32 v45, 0xffff0000, v20
	v_lshlrev_b32_e32 v46, 16, v21
	v_and_b32_e32 v47, 0xffff0000, v21
	v_add_f32_e32 v22, v36, v22
	v_add_f32_e32 v20, v44, v45
	v_add_f32_e32 v21, v46, v47
	v_lshlrev_b32_e32 v36, 16, v18
	v_and_b32_e32 v37, 0xffff0000, v18
	v_lshlrev_b32_e32 v38, 16, v19
	v_and_b32_e32 v39, 0xffff0000, v19
	v_add_f32_e32 v20, v20, v21
	v_add_f32_e32 v18, v36, v37
	v_add_f32_e32 v19, v38, v39
	v_lshlrev_b32_e32 v42, 16, v16
	v_and_b32_e32 v43, 0xffff0000, v16
	v_lshlrev_b32_e32 v40, 16, v17
	v_and_b32_e32 v41, 0xffff0000, v17
	v_add_f32_e32 v20, v22, v20
	v_add_f32_e32 v18, v18, v19
	v_add_f32_e32 v16, v42, v43
	v_add_f32_e32 v17, v40, v41
	v_add_f32_e32 v18, v20, v18
	v_add_f32_e32 v16, v16, v17
	v_add_f32_e32 v16, v18, v16
	s_mov_b64 s[6:7], s[34:35]
	s_mov_b64 s[8:9], s[36:37]
	v_add_f32_dpp v16, v16, v16 quad_perm:[1,0,3,2] row_mask:0xf bank_mask:0xf bound_ctrl:1
	v_lshl_add_u64 v[108:109], s[6:7], 0, v[192:193]
	v_lshl_add_u64 v[104:105], v[28:29], 0, s[42:43]
	v_add_f32_dpp v16, v16, v16 quad_perm:[2,3,0,1] row_mask:0xf bank_mask:0xf bound_ctrl:1
	v_lshl_add_u64 v[106:107], s[8:9], 0, v[192:193]
	s_lshl_b64 s[6:7], s[40:41], 11
	v_add_f32_dpp v16, v16, v16 row_ror:4 row_mask:0xf bank_mask:0xf bound_ctrl:1
	v_lshl_add_u64 v[82:83], v[30:31], 0, s[6:7]
	s_nop 0
	v_add_f32_dpp v16, v16, v16 row_ror:8 row_mask:0xf bank_mask:0xf bound_ctrl:1
	v_mov_b32_e32 v17, v16
	s_nop 1
	v_permlane16_swap_b32_e32 v16, v17
	v_add_f32_e32 v16, v16, v17
	v_mov_b32_e32 v17, v16
	s_nop 1
	v_permlane32_swap_b32_e32 v16, v17
	v_add_f32_e32 v16, v16, v17
	v_fmac_f32_e32 v101, 0xba000000, v16
	v_fmac_f32_e32 v103, 0xba000000, v16
	v_fmac_f32_e32 v100, 0xba000000, v16
	v_fmac_f32_e32 v102, 0xba000000, v16
	v_mul_f32_e32 v17, v103, v103
	v_mul_f32_e32 v18, v101, v101
	v_fmac_f32_e32 v17, v102, v102
	v_fmac_f32_e32 v18, v100, v100
	v_fmac_f32_e32 v73, 0xba000000, v16
	v_fmac_f32_e32 v75, 0xba000000, v16
	v_add_f32_e32 v17, v17, v18
	v_fmac_f32_e32 v72, 0xba000000, v16
	v_fmac_f32_e32 v74, 0xba000000, v16
	v_mul_f32_e32 v18, v75, v75
	v_mul_f32_e32 v19, v73, v73
	v_fmac_f32_e32 v18, v74, v74
	v_fmac_f32_e32 v19, v72, v72
	v_add_f32_e32 v18, v18, v19
	v_fmac_f32_e32 v67, 0xba000000, v16
	v_fmac_f32_e32 v65, 0xba000000, v16
	v_add_f32_e32 v17, v17, v18
	v_fmac_f32_e32 v66, 0xba000000, v16
	v_fmac_f32_e32 v64, 0xba000000, v16
	v_mul_f32_e32 v18, v65, v65
	v_mul_f32_e32 v19, v67, v67
	v_fmac_f32_e32 v18, v64, v64
	v_fmac_f32_e32 v19, v66, v66
	v_add_f32_e32 v18, v18, v19
	v_fmac_f32_e32 v59, 0xba000000, v16
	v_fmac_f32_e32 v57, 0xba000000, v16
	v_add_f32_e32 v17, v17, v18
	v_fmac_f32_e32 v58, 0xba000000, v16
	v_fmac_f32_e32 v56, 0xba000000, v16
	v_mul_f32_e32 v18, v57, v57
	v_mul_f32_e32 v19, v59, v59
	v_fmac_f32_e32 v18, v56, v56
	v_fmac_f32_e32 v19, v58, v58
	v_add_f32_e32 v18, v18, v19
	v_fmac_f32_e32 v55, 0xba000000, v16
	v_fmac_f32_e32 v53, 0xba000000, v16
	v_add_f32_e32 v17, v17, v18
	v_fmac_f32_e32 v54, 0xba000000, v16
	v_fmac_f32_e32 v52, 0xba000000, v16
	v_mul_f32_e32 v18, v53, v53
	v_mul_f32_e32 v19, v55, v55
	v_fmac_f32_e32 v18, v52, v52
	v_fmac_f32_e32 v19, v54, v54
	v_add_f32_e32 v18, v18, v19
	v_fmac_f32_e32 v47, 0xba000000, v16
	v_fmac_f32_e32 v45, 0xba000000, v16
	v_add_f32_e32 v17, v17, v18
	v_fmac_f32_e32 v46, 0xba000000, v16
	v_fmac_f32_e32 v44, 0xba000000, v16
	v_mul_f32_e32 v18, v45, v45
	v_mul_f32_e32 v19, v47, v47
	v_fmac_f32_e32 v18, v44, v44
	v_fmac_f32_e32 v19, v46, v46
	v_add_f32_e32 v18, v18, v19
	v_fmac_f32_e32 v39, 0xba000000, v16
	v_fmac_f32_e32 v37, 0xba000000, v16
	v_add_f32_e32 v17, v17, v18
	v_fmac_f32_e32 v38, 0xba000000, v16
	v_fmac_f32_e32 v36, 0xba000000, v16
	v_mul_f32_e32 v18, v37, v37
	v_mul_f32_e32 v19, v39, v39
	v_fmac_f32_e32 v18, v36, v36
	v_fmac_f32_e32 v19, v38, v38
	v_add_f32_e32 v18, v18, v19
	v_fmac_f32_e32 v41, 0xba000000, v16
	v_fmac_f32_e32 v43, 0xba000000, v16
	v_add_f32_e32 v17, v17, v18
	v_fmac_f32_e32 v40, 0xba000000, v16
	v_fmac_f32_e32 v42, 0xba000000, v16
	v_mul_f32_e32 v16, v43, v43
	v_mul_f32_e32 v18, v41, v41
	v_fmac_f32_e32 v16, v42, v42
	v_fmac_f32_e32 v18, v40, v40
	v_add_f32_e32 v16, v16, v18
	v_add_f32_e32 v16, v17, v16
	s_nop 1
	v_add_f32_dpp v16, v16, v16 quad_perm:[1,0,3,2] row_mask:0xf bank_mask:0xf bound_ctrl:1
	s_nop 1
	v_add_f32_dpp v16, v16, v16 quad_perm:[2,3,0,1] row_mask:0xf bank_mask:0xf bound_ctrl:1
	s_nop 1
	v_add_f32_dpp v16, v16, v16 row_ror:4 row_mask:0xf bank_mask:0xf bound_ctrl:1
	s_nop 1
	v_add_f32_dpp v16, v16, v16 row_ror:8 row_mask:0xf bank_mask:0xf bound_ctrl:1
	v_mov_b32_e32 v17, v16
	s_nop 1
	v_permlane16_swap_b32_e32 v16, v17
	v_add_f32_e32 v16, v16, v17
	v_mov_b32_e32 v17, v16
	s_nop 1
	v_permlane32_swap_b32_e32 v16, v17
	v_add_f32_e32 v16, v16, v17
	v_fmamk_f32 v16, v16, 0x3a000000, v207
	v_rsq_f32_e32 v76, v16
	s_nop 0
	v_pk_mul_f32 v[102:103], v[76:77], v[102:103] op_sel_hi:[0,1]
	v_pk_mul_f32 v[100:101], v[76:77], v[100:101] op_sel_hi:[0,1]
	v_pk_mul_f32 v[74:75], v[76:77], v[74:75] op_sel_hi:[0,1]
	v_pk_mul_f32 v[72:73], v[76:77], v[72:73] op_sel_hi:[0,1]
	v_pk_mul_f32 v[110:111], v[76:77], v[64:65] op_sel_hi:[0,1]
	v_pk_mul_f32 v[64:65], v[76:77], v[66:67] op_sel_hi:[0,1]
	s_waitcnt lgkmcnt(0)
; #define LAS __attribute__((address_space(3)))
; __global__ void __launch_bounds__(NTHREADS, 2) hybrid_fwd(Args a) {
;     ...
; #pragma unroll
;                     for (int j = 0; j < 8; ++j) {
; #pragma unroll
;                         for (int e = 0; e < 16; ++e) { const f32x4 w = *(const LAS f32x4*)(rwT + e * 2052 + j * 256 + lane * 4);
;                             acc2[e] += y2[j][0] * (f32x2){w[0], w[0]}; acc2[e] += y2[j][1] * (f32x2){w[1], w[1]};
;                             acc2[e] += y2[j][2] * (f32x2){w[2], w[2]}; acc2[e] += y2[j][3] * (f32x2){w[3], w[3]}; }
	v_pk_fma_f32 v[100:101], v[160:161], v[100:101], v[200:201]
	v_pk_fma_f32 v[102:103], v[158:159], v[102:103], v[198:199]
	v_mov_b32_e32 v20, 0
	v_cvt_pk_bf16_f32 v16, v102, v103
	v_cvt_pk_bf16_f32 v17, v100, v101
	global_store_dwordx2 v[104:105], v[16:17], off nt
	v_med3_f32 v16, v102, s69, v208
	v_med3_f32 v17, v103, s69, v208
	v_cvt_pk_fp8_f32 v20, v16, v17
	v_med3_f32 v18, v100, s69, v208
	v_med3_f32 v19, v101, s69, v208
	v_cvt_pk_fp8_f32 v20, v18, v19 op_sel:[0,0,1]
	global_store_dword v[82:83], v20, off nt
	s_nop 0
	s_nop 0
	s_nop 0
	v_pk_fma_f32 v[72:73], v[164:165], v[72:73], v[204:205]
	v_pk_fma_f32 v[74:75], v[162:163], v[74:75], v[202:203]
	v_mov_b32_e32 v20, 0
	v_cvt_pk_bf16_f32 v16, v74, v75
	v_cvt_pk_bf16_f32 v17, v72, v73
	global_store_dwordx2 v[104:105], v[16:17], off offset:512 nt
	v_med3_f32 v16, v74, s69, v208
	v_med3_f32 v17, v75, s69, v208
	v_cvt_pk_fp8_f32 v20, v16, v17
	v_med3_f32 v18, v72, s69, v208
	v_med3_f32 v19, v73, s69, v208
	v_cvt_pk_fp8_f32 v20, v18, v19 op_sel:[0,0,1]
	global_store_dword v[82:83], v20, off offset:256 nt
	s_nop 0
	s_nop 0
	s_nop 0
	v_pk_fma_f32 v[64:65], v[168:169], v[64:65], v[218:219]
	v_pk_fma_f32 v[66:67], v[166:167], v[110:111], v[216:217]
	v_mov_b32_e32 v20, 0
	v_cvt_pk_bf16_f32 v16, v66, v67
	v_cvt_pk_bf16_f32 v17, v64, v65
	global_store_dwordx2 v[104:105], v[16:17], off offset:1024 nt
	v_med3_f32 v16, v66, s69, v208
	v_med3_f32 v17, v67, s69, v208
	v_cvt_pk_fp8_f32 v20, v16, v17
	v_med3_f32 v18, v64, s69, v208
	v_med3_f32 v19, v65, s69, v208
	v_pk_mul_f32 v[110:111], v[76:77], v[56:57] op_sel_hi:[0,1]
	v_cvt_pk_fp8_f32 v20, v18, v19 op_sel:[0,0,1]
	v_pk_mul_f32 v[56:57], v[76:77], v[58:59] op_sel_hi:[0,1]
	global_store_dword v[82:83], v20, off offset:512 nt
	s_nop 0
	s_nop 0
	s_nop 0
	v_pk_fma_f32 v[56:57], v[172:173], v[56:57], v[222:223]
	v_pk_fma_f32 v[58:59], v[170:171], v[110:111], v[220:221]
	v_mov_b32_e32 v20, 0
	v_cvt_pk_bf16_f32 v16, v58, v59
	v_cvt_pk_bf16_f32 v17, v56, v57
	global_store_dwordx2 v[104:105], v[16:17], off offset:1536 nt
	v_med3_f32 v16, v58, s69, v208
	v_med3_f32 v17, v59, s69, v208
	v_cvt_pk_fp8_f32 v20, v16, v17
	v_med3_f32 v18, v56, s69, v208
	v_med3_f32 v19, v57, s69, v208
	v_add_co_u32_e32 v16, vcc, s33, v108
	v_cvt_pk_fp8_f32 v20, v18, v19 op_sel:[0,0,1]
	s_nop 0
	v_addc_co_u32_e32 v17, vcc, 0, v109, vcc
	v_add_co_u32_e32 v18, vcc, s33, v106
	global_store_dword v[82:83], v20, off offset:768 nt
	s_nop 0
	v_addc_co_u32_e32 v19, vcc, 0, v107, vcc
	s_nop 0
	v_pk_mul_f32 v[110:111], v[76:77], v[52:53] op_sel_hi:[0,1]
	v_pk_mul_f32 v[52:53], v[76:77], v[54:55] op_sel_hi:[0,1]
	v_mov_b32_e32 v77, 0
	s_nop 0
	v_pk_fma_f32 v[52:53], v[176:177], v[52:53], v[226:227]
	v_pk_fma_f32 v[54:55], v[174:175], v[110:111], v[224:225]
	v_med3_f32 v22, v52, s69, v208
	v_cvt_pk_bf16_f32 v20, v54, v55
	v_cvt_pk_bf16_f32 v21, v52, v53
	global_store_dwordx2 v[104:105], v[20:21], off offset:2048 nt
	v_med3_f32 v20, v54, s69, v208
	v_med3_f32 v21, v55, s69, v208
	v_cvt_pk_fp8_f32 v77, v20, v21
	v_med3_f32 v23, v53, s69, v208
	v_cvt_pk_fp8_f32 v77, v22, v23 op_sel:[0,0,1]
	global_store_dword v[82:83], v77, off offset:1024 nt
	s_nop 0
	v_pk_mul_f32 v[110:111], v[76:77], v[44:45] op_sel_hi:[0,1]
	v_pk_mul_f32 v[44:45], v[76:77], v[46:47] op_sel_hi:[0,1]
	v_mov_b32_e32 v77, 0
	s_nop 0
	v_pk_fma_f32 v[44:45], v[180:181], v[44:45], v[230:231]
	v_pk_fma_f32 v[46:47], v[178:179], v[110:111], v[228:229]
	v_med3_f32 v22, v44, s69, v208
	v_cvt_pk_bf16_f32 v20, v46, v47
	v_cvt_pk_bf16_f32 v21, v44, v45
	global_store_dwordx2 v[104:105], v[20:21], off offset:2560 nt
	v_med3_f32 v20, v46, s69, v208
	v_med3_f32 v21, v47, s69, v208
	v_cvt_pk_fp8_f32 v77, v20, v21
	v_med3_f32 v23, v45, s69, v208
	v_cvt_pk_fp8_f32 v77, v22, v23 op_sel:[0,0,1]
	global_store_dword v[82:83], v77, off offset:1280 nt
	s_nop 0
	v_pk_mul_f32 v[110:111], v[76:77], v[36:37] op_sel_hi:[0,1]
	v_pk_mul_f32 v[36:37], v[76:77], v[38:39] op_sel_hi:[0,1]
	v_mov_b32_e32 v77, 0
	s_nop 0
	v_pk_fma_f32 v[36:37], v[184:185], v[36:37], v[234:235]
	v_pk_fma_f32 v[38:39], v[182:183], v[110:111], v[232:233]
	v_med3_f32 v22, v36, s69, v208
	v_cvt_pk_bf16_f32 v20, v38, v39
	v_cvt_pk_bf16_f32 v21, v36, v37
	global_store_dwordx2 v[104:105], v[20:21], off offset:3072 nt
	v_med3_f32 v20, v38, s69, v208
	v_med3_f32 v21, v39, s69, v208
	v_cvt_pk_fp8_f32 v77, v20, v21
	v_med3_f32 v23, v37, s69, v208
	v_cvt_pk_fp8_f32 v77, v22, v23 op_sel:[0,0,1]
	global_store_dword v[82:83], v77, off offset:1536 nt
	s_nop 0
	v_pk_mul_f32 v[18:19], v[76:77], v[42:43] op_sel_hi:[0,1]
	v_pk_mul_f32 v[16:17], v[76:77], v[40:41] op_sel_hi:[0,1]
	v_mov_b32_e32 v40, 0
	s_nop 0
	v_pk_fma_f32 v[16:17], v[188:189], v[16:17], v[248:249]
	v_pk_fma_f32 v[18:19], v[186:187], v[18:19], v[246:247]
	v_med3_f32 v22, v16, s69, v208
	v_cvt_pk_bf16_f32 v20, v18, v19
	v_cvt_pk_bf16_f32 v21, v16, v17
	global_store_dwordx2 v[104:105], v[20:21], off offset:3584 nt
	v_med3_f32 v20, v18, s69, v208
	v_med3_f32 v21, v19, s69, v208
	v_cvt_pk_fp8_f32 v40, v20, v21
	v_med3_f32 v23, v17, s69, v208
	v_cvt_pk_fp8_f32 v40, v22, v23 op_sel:[0,0,1]
	global_store_dword v[82:83], v40, off offset:1792 nt
	v_add_u32_e32 v238, 0x10000, v25
	ds_read_b128 v[158:161], v25 offset:0
	ds_read_b128 v[162:165], v25 offset:8208
	ds_read_b128 v[166:169], v25 offset:16416
	ds_read_b128 v[170:173], v25 offset:24624
	ds_read_b128 v[174:177], v25 offset:32832
	ds_read_b128 v[178:181], v25 offset:41040
	ds_read_b128 v[182:185], v25 offset:49248
	ds_read_b128 v[186:189], v25 offset:57456
	v_mov_b32_e32 v76, v70
	v_mov_b32_e32 v77, v66
	v_mov_b32_e32 v66, v71
	v_mov_b32_e32 v82, v68
	v_mov_b32_e32 v83, v64
	v_mov_b32_e32 v64, v69
	v_mov_b32_e32 v68, v80
	v_mov_b32_e32 v69, v58
	v_mov_b32_e32 v58, v81
	v_mov_b32_e32 v70, v78
	v_mov_b32_e32 v71, v56
	v_mov_b32_e32 v56, v79
	ds_read_b128 v[198:201], v238 offset:128
	v_mov_b32_e32 v108, v48
	v_mov_b32_e32 v109, v102
	v_mov_b32_e32 v102, v49
	v_mov_b32_e32 v106, v62
	v_mov_b32_e32 v107, v72
	v_mov_b32_e32 v72, v63
	v_mov_b32_e32 v62, v84
	v_mov_b32_e32 v63, v52
	v_mov_b32_e32 v52, v85
	s_waitcnt lgkmcnt(8)
; #define LAS __attribute__((address_space(3)))
; __global__ void __launch_bounds__(NTHREADS, 2) hybrid_fwd(Args a) {
;     ...
; #pragma unroll
;                     for (int j = 0; j < 8; ++j) {
; #pragma unroll
;                         for (int e = 0; e < 16; ++e) { const f32x4 w = *(const LAS f32x4*)(rwT + e * 2052 + j * 256 + lane * 4);
;                             acc2[e] += y2[j][0] * (f32x2){w[0], w[0]}; acc2[e] += y2[j][1] * (f32x2){w[1], w[1]};
;                             acc2[e] += y2[j][2] * (f32x2){w[2], w[2]}; acc2[e] += y2[j][3] * (f32x2){w[3], w[3]}; }
;                         __builtin_amdgcn_sched_barrier(0);
;                     }
	v_pk_fma_f32 v[84:85], v[108:109], v[158:159], 0 op_sel_hi:[1,0,0]
	v_mov_b32_e32 v104, v60
	v_mov_b32_e32 v105, v74
	v_mov_b32_e32 v74, v61
	v_mov_b32_e32 v60, v86
	v_mov_b32_e32 v61, v54
	v_mov_b32_e32 v54, v87
	v_pk_fma_f32 v[78:79], v[158:159], v[102:103], v[84:85] op_sel:[1,0,0]
	ds_read_b128 v[202:205], v238 offset:8336
	v_mov_b32_e32 v110, v50
	v_mov_b32_e32 v111, v100
	v_mov_b32_e32 v100, v51
	v_pk_fma_f32 v[78:79], v[160:161], v[110:111], v[78:79] op_sel_hi:[0,1,1]
	v_mov_b32_e32 v80, v161
	v_pk_fma_f32 v[78:79], v[80:81], v[100:101], v[78:79] op_sel_hi:[0,1,1]
	s_waitcnt lgkmcnt(8)
	v_pk_fma_f32 v[80:81], v[108:109], v[162:163], 0 op_sel_hi:[1,0,0]
	v_mov_b32_e32 v50, v88
	v_pk_fma_f32 v[80:81], v[162:163], v[102:103], v[80:81] op_sel:[1,0,0]
	v_mov_b32_e32 v84, v165
	v_pk_fma_f32 v[80:81], v[164:165], v[110:111], v[80:81] op_sel_hi:[0,1,1]
	v_pk_fma_f32 v[120:121], v[84:85], v[100:101], v[80:81] op_sel_hi:[0,1,1]
	ds_read_b128 v[216:219], v238 offset:16544
	v_mov_b32_e32 v51, v44
	v_mov_b32_e32 v44, v89
	v_mov_b32_e32 v48, v90
	v_mov_b32_e32 v49, v46
	s_waitcnt lgkmcnt(8)
	v_pk_fma_f32 v[80:81], v[108:109], v[166:167], 0 op_sel_hi:[1,0,0]
	v_mov_b32_e32 v46, v91
	v_pk_fma_f32 v[80:81], v[166:167], v[102:103], v[80:81] op_sel:[1,0,0]
	v_mov_b32_e32 v84, v169
	v_pk_fma_f32 v[80:81], v[168:169], v[110:111], v[80:81] op_sel_hi:[0,1,1]
	v_pk_fma_f32 v[122:123], v[84:85], v[100:101], v[80:81] op_sel_hi:[0,1,1]
	ds_read_b128 v[220:223], v238 offset:24752
	v_mov_b32_e32 v42, v92
	v_mov_b32_e32 v43, v36
	v_mov_b32_e32 v36, v93
	v_mov_b32_e32 v40, v94
	s_waitcnt lgkmcnt(8)
	v_pk_fma_f32 v[80:81], v[108:109], v[170:171], 0 op_sel_hi:[1,0,0]
	v_mov_b32_e32 v41, v38
	v_pk_fma_f32 v[80:81], v[170:171], v[102:103], v[80:81] op_sel:[1,0,0]
	v_mov_b32_e32 v84, v173
	v_pk_fma_f32 v[80:81], v[172:173], v[110:111], v[80:81] op_sel_hi:[0,1,1]
	v_pk_fma_f32 v[80:81], v[84:85], v[100:101], v[80:81] op_sel_hi:[0,1,1]
	ds_read_b128 v[224:227], v238 offset:32960
	v_mov_b32_e32 v38, v95
	v_mov_b32_e32 v22, v96
	v_mov_b32_e32 v23, v18
	v_mov_b32_e32 v18, v97
	s_waitcnt lgkmcnt(8)
	v_pk_fma_f32 v[88:89], v[108:109], v[174:175], 0 op_sel_hi:[1,0,0]
	v_mov_b32_e32 v20, v98
	v_pk_fma_f32 v[84:85], v[174:175], v[102:103], v[88:89] op_sel:[1,0,0]
	v_mov_b32_e32 v21, v16
	v_pk_fma_f32 v[84:85], v[176:177], v[110:111], v[84:85] op_sel_hi:[0,1,1]
	v_mov_b32_e32 v86, v177
	v_pk_fma_f32 v[84:85], v[86:87], v[100:101], v[84:85] op_sel_hi:[0,1,1]
	ds_read_b128 v[228:231], v238 offset:41168
	v_mov_b32_e32 v16, v99
	s_waitcnt lgkmcnt(8)
	v_pk_fma_f32 v[90:91], v[108:109], v[178:179], 0 op_sel_hi:[1,0,0]
	s_nop 0
	v_pk_fma_f32 v[86:87], v[178:179], v[102:103], v[90:91] op_sel:[1,0,0]
	s_nop 0
	v_pk_fma_f32 v[86:87], v[180:181], v[110:111], v[86:87] op_sel_hi:[0,1,1]
	v_mov_b32_e32 v88, v181
	v_pk_fma_f32 v[86:87], v[88:89], v[100:101], v[86:87] op_sel_hi:[0,1,1]
	ds_read_b128 v[232:235], v238 offset:49376
	s_waitcnt lgkmcnt(8)
	v_pk_fma_f32 v[92:93], v[108:109], v[182:183], 0 op_sel_hi:[1,0,0]
	s_nop 0
	v_pk_fma_f32 v[88:89], v[182:183], v[102:103], v[92:93] op_sel:[1,0,0]
	s_nop 0
	v_pk_fma_f32 v[88:89], v[184:185], v[110:111], v[88:89] op_sel_hi:[0,1,1]
	v_mov_b32_e32 v90, v185
	v_pk_fma_f32 v[88:89], v[90:91], v[100:101], v[88:89] op_sel_hi:[0,1,1]
	ds_read_b128 v[242:245], v238 offset:57584
	s_waitcnt lgkmcnt(8)
	v_pk_fma_f32 v[94:95], v[108:109], v[186:187], 0 op_sel_hi:[1,0,0]
	s_nop 0
	v_pk_fma_f32 v[90:91], v[186:187], v[102:103], v[94:95] op_sel:[1,0,0]
	s_nop 0
	v_pk_fma_f32 v[90:91], v[188:189], v[110:111], v[90:91] op_sel_hi:[0,1,1]
	v_mov_b32_e32 v92, v189
	v_pk_fma_f32 v[90:91], v[92:93], v[100:101], v[90:91] op_sel_hi:[0,1,1]
	ds_read_b128 v[246:249], v25 offset:1024
	s_waitcnt lgkmcnt(8)
	v_pk_fma_f32 v[96:97], v[108:109], v[198:199], 0 op_sel_hi:[1,0,0]
	s_nop 0
	v_pk_fma_f32 v[92:93], v[198:199], v[102:103], v[96:97] op_sel:[1,0,0]
	s_nop 0
	v_pk_fma_f32 v[92:93], v[200:201], v[110:111], v[92:93] op_sel_hi:[0,1,1]
	v_mov_b32_e32 v94, v201
	v_pk_fma_f32 v[92:93], v[94:95], v[100:101], v[92:93] op_sel_hi:[0,1,1]
	ds_read_b128 v[250:253], v25 offset:9232
	s_waitcnt lgkmcnt(8)
	v_pk_fma_f32 v[98:99], v[108:109], v[202:203], 0 op_sel_hi:[1,0,0]
	s_nop 0
	v_pk_fma_f32 v[94:95], v[202:203], v[102:103], v[98:99] op_sel:[1,0,0]
	s_nop 0
	v_pk_fma_f32 v[94:95], v[204:205], v[110:111], v[94:95] op_sel_hi:[0,1,1]
	v_mov_b32_e32 v96, v205
	v_pk_fma_f32 v[94:95], v[96:97], v[100:101], v[94:95] op_sel_hi:[0,1,1]
	ds_read_b128 v[158:161], v25 offset:17440
	s_waitcnt lgkmcnt(8)
	v_pk_fma_f32 v[112:113], v[108:109], v[216:217], 0 op_sel_hi:[1,0,0]
	s_nop 0
	v_pk_fma_f32 v[96:97], v[216:217], v[102:103], v[112:113] op_sel:[1,0,0]
	ds_read_b128 v[162:165], v25 offset:25648
	v_pk_fma_f32 v[96:97], v[218:219], v[110:111], v[96:97] op_sel_hi:[0,1,1]
	v_mov_b32_e32 v98, v219
	v_pk_fma_f32 v[96:97], v[98:99], v[100:101], v[96:97] op_sel_hi:[0,1,1]
	s_waitcnt lgkmcnt(8)
	v_pk_fma_f32 v[98:99], v[108:109], v[220:221], 0 op_sel_hi:[1,0,0]
	s_nop 0
	v_pk_fma_f32 v[98:99], v[220:221], v[102:103], v[98:99] op_sel:[1,0,0]
	v_mov_b32_e32 v112, v223
	v_pk_fma_f32 v[98:99], v[222:223], v[110:111], v[98:99] op_sel_hi:[0,1,1]
	v_pk_fma_f32 v[98:99], v[112:113], v[100:101], v[98:99] op_sel_hi:[0,1,1]
	ds_read_b128 v[166:169], v25 offset:33856
	s_waitcnt lgkmcnt(8)
	v_pk_fma_f32 v[116:117], v[108:109], v[224:225], 0 op_sel_hi:[1,0,0]
	s_nop 0
	v_pk_fma_f32 v[112:113], v[224:225], v[102:103], v[116:117] op_sel:[1,0,0]
	s_nop 0
	v_pk_fma_f32 v[112:113], v[226:227], v[110:111], v[112:113] op_sel_hi:[0,1,1]
	v_mov_b32_e32 v114, v227
	v_pk_fma_f32 v[112:113], v[114:115], v[100:101], v[112:113] op_sel_hi:[0,1,1]
	ds_read_b128 v[170:173], v25 offset:42064
	s_waitcnt lgkmcnt(8)
; #define LAS __attribute__((address_space(3)))
; __global__ void __launch_bounds__(NTHREADS, 2) hybrid_fwd(Args a) {
;     ...
; #pragma unroll
;                     for (int j = 0; j < 8; ++j) {
; #pragma unroll
;                         for (int e = 0; e < 16; ++e) { const f32x4 w = *(const LAS f32x4*)(rwT + e * 2052 + j * 256 + lane * 4);
;                             acc2[e] += y2[j][0] * (f32x2){w[0], w[0]}; acc2[e] += y2[j][1] * (f32x2){w[1], w[1]};
;                             acc2[e] += y2[j][2] * (f32x2){w[2], w[2]}; acc2[e] += y2[j][3] * (f32x2){w[3], w[3]}; }
;                         __builtin_amdgcn_sched_barrier(0);
;                     }
	v_pk_fma_f32 v[118:119], v[108:109], v[228:229], 0 op_sel_hi:[1,0,0]
	s_nop 0
	v_pk_fma_f32 v[114:115], v[228:229], v[102:103], v[118:119] op_sel:[1,0,0]
	s_nop 0
	v_pk_fma_f32 v[114:115], v[230:231], v[110:111], v[114:115] op_sel_hi:[0,1,1]
	v_mov_b32_e32 v116, v231
	v_pk_fma_f32 v[114:115], v[116:117], v[100:101], v[114:115] op_sel_hi:[0,1,1]
	ds_read_b128 v[174:177], v25 offset:50272
	s_waitcnt lgkmcnt(8)
	v_pk_fma_f32 v[124:125], v[108:109], v[232:233], 0 op_sel_hi:[1,0,0]
	s_nop 0
	v_pk_fma_f32 v[116:117], v[232:233], v[102:103], v[124:125] op_sel:[1,0,0]
	ds_read_b128 v[178:181], v25 offset:58480
	v_pk_fma_f32 v[116:117], v[234:235], v[110:111], v[116:117] op_sel_hi:[0,1,1]
	v_mov_b32_e32 v118, v235
	v_pk_fma_f32 v[116:117], v[118:119], v[100:101], v[116:117] op_sel_hi:[0,1,1]
	s_waitcnt lgkmcnt(8)
	v_pk_fma_f32 v[108:109], v[108:109], v[242:243], 0 op_sel_hi:[1,0,0]
	s_nop 0
	v_pk_fma_f32 v[102:103], v[242:243], v[102:103], v[108:109] op_sel:[1,0,0]
	v_mov_b32_e32 v108, v245
	v_pk_fma_f32 v[102:103], v[244:245], v[110:111], v[102:103] op_sel_hi:[0,1,1]
	v_pk_fma_f32 v[118:119], v[108:109], v[100:101], v[102:103] op_sel_hi:[0,1,1]
	ds_read_b128 v[182:185], v238 offset:1152
	s_waitcnt lgkmcnt(8)
	v_pk_fma_f32 v[78:79], v[104:105], v[246:247], v[78:79] op_sel_hi:[1,0,1]
	s_nop 0
	v_pk_fma_f32 v[78:79], v[246:247], v[74:75], v[78:79] op_sel:[1,0,0]
	v_mov_b32_e32 v100, v249
	v_pk_fma_f32 v[78:79], v[248:249], v[106:107], v[78:79] op_sel_hi:[0,1,1]
	v_pk_fma_f32 v[78:79], v[100:101], v[72:73], v[78:79] op_sel_hi:[0,1,1]
	ds_read_b128 v[186:189], v238 offset:9360
	s_waitcnt lgkmcnt(8)
	v_pk_fma_f32 v[108:109], v[104:105], v[250:251], v[120:121] op_sel_hi:[1,0,1]
	s_nop 0
	v_pk_fma_f32 v[100:101], v[250:251], v[74:75], v[108:109] op_sel:[1,0,0]
	s_nop 0
	v_pk_fma_f32 v[100:101], v[252:253], v[106:107], v[100:101] op_sel_hi:[0,1,1]
	v_mov_b32_e32 v102, v253
	v_pk_fma_f32 v[120:121], v[102:103], v[72:73], v[100:101] op_sel_hi:[0,1,1]
	ds_read_b128 v[198:201], v238 offset:17568
	s_waitcnt lgkmcnt(8)
	v_pk_fma_f32 v[108:109], v[104:105], v[158:159], v[122:123] op_sel_hi:[1,0,1]
	s_nop 0
	v_pk_fma_f32 v[100:101], v[158:159], v[74:75], v[108:109] op_sel:[1,0,0]
	ds_read_b128 v[202:205], v238 offset:25776
	v_pk_fma_f32 v[100:101], v[160:161], v[106:107], v[100:101] op_sel_hi:[0,1,1]
	v_mov_b32_e32 v102, v161
	v_pk_fma_f32 v[100:101], v[102:103], v[72:73], v[100:101] op_sel_hi:[0,1,1]
	s_waitcnt lgkmcnt(8)
	v_pk_fma_f32 v[80:81], v[104:105], v[162:163], v[80:81] op_sel_hi:[1,0,1]
	s_nop 0
	v_pk_fma_f32 v[80:81], v[162:163], v[74:75], v[80:81] op_sel:[1,0,0]
	v_mov_b32_e32 v102, v165
	v_pk_fma_f32 v[80:81], v[164:165], v[106:107], v[80:81] op_sel_hi:[0,1,1]
	ds_read_b128 v[216:219], v238 offset:33984
	v_pk_fma_f32 v[80:81], v[102:103], v[72:73], v[80:81] op_sel_hi:[0,1,1]
	s_waitcnt lgkmcnt(8)
	v_pk_fma_f32 v[84:85], v[104:105], v[166:167], v[84:85] op_sel_hi:[1,0,1]
	s_nop 0
	v_pk_fma_f32 v[84:85], v[166:167], v[74:75], v[84:85] op_sel:[1,0,0]
	v_mov_b32_e32 v102, v169
	v_pk_fma_f32 v[84:85], v[168:169], v[106:107], v[84:85] op_sel_hi:[0,1,1]
	ds_read_b128 v[220:223], v238 offset:42192
	v_pk_fma_f32 v[84:85], v[102:103], v[72:73], v[84:85] op_sel_hi:[0,1,1]
	s_waitcnt lgkmcnt(8)
	v_pk_fma_f32 v[86:87], v[104:105], v[170:171], v[86:87] op_sel_hi:[1,0,1]
	s_nop 0
	v_pk_fma_f32 v[86:87], v[170:171], v[74:75], v[86:87] op_sel:[1,0,0]
	v_mov_b32_e32 v102, v173
	v_pk_fma_f32 v[86:87], v[172:173], v[106:107], v[86:87] op_sel_hi:[0,1,1]
	ds_read_b128 v[224:227], v238 offset:50400
	v_pk_fma_f32 v[86:87], v[102:103], v[72:73], v[86:87] op_sel_hi:[0,1,1]
	s_waitcnt lgkmcnt(8)
	v_pk_fma_f32 v[88:89], v[104:105], v[174:175], v[88:89] op_sel_hi:[1,0,1]
	s_nop 0
	v_pk_fma_f32 v[88:89], v[174:175], v[74:75], v[88:89] op_sel:[1,0,0]
	v_mov_b32_e32 v102, v177
	v_pk_fma_f32 v[88:89], v[176:177], v[106:107], v[88:89] op_sel_hi:[0,1,1]
	ds_read_b128 v[228:231], v238 offset:58608
	v_pk_fma_f32 v[88:89], v[102:103], v[72:73], v[88:89] op_sel_hi:[0,1,1]
	s_waitcnt lgkmcnt(8)
	v_pk_fma_f32 v[90:91], v[104:105], v[178:179], v[90:91] op_sel_hi:[1,0,1]
	s_nop 0
	v_pk_fma_f32 v[90:91], v[178:179], v[74:75], v[90:91] op_sel:[1,0,0]
	v_mov_b32_e32 v102, v181
	v_pk_fma_f32 v[90:91], v[180:181], v[106:107], v[90:91] op_sel_hi:[0,1,1]
	ds_read_b128 v[232:235], v25 offset:2048
	v_pk_fma_f32 v[90:91], v[102:103], v[72:73], v[90:91] op_sel_hi:[0,1,1]
	s_waitcnt lgkmcnt(8)
	v_pk_fma_f32 v[92:93], v[104:105], v[182:183], v[92:93] op_sel_hi:[1,0,1]
	s_nop 0
	v_pk_fma_f32 v[92:93], v[182:183], v[74:75], v[92:93] op_sel:[1,0,0]
	v_mov_b32_e32 v102, v185
	v_pk_fma_f32 v[92:93], v[184:185], v[106:107], v[92:93] op_sel_hi:[0,1,1]
	ds_read_b128 v[242:245], v25 offset:10256
	v_pk_fma_f32 v[92:93], v[102:103], v[72:73], v[92:93] op_sel_hi:[0,1,1]
	s_waitcnt lgkmcnt(8)
	v_pk_fma_f32 v[94:95], v[104:105], v[186:187], v[94:95] op_sel_hi:[1,0,1]
	s_nop 0
	v_pk_fma_f32 v[94:95], v[186:187], v[74:75], v[94:95] op_sel:[1,0,0]
	v_mov_b32_e32 v102, v189
	v_pk_fma_f32 v[94:95], v[188:189], v[106:107], v[94:95] op_sel_hi:[0,1,1]
	ds_read_b128 v[246:249], v25 offset:18464
	v_pk_fma_f32 v[94:95], v[102:103], v[72:73], v[94:95] op_sel_hi:[0,1,1]
	s_waitcnt lgkmcnt(8)
	v_pk_fma_f32 v[96:97], v[104:105], v[198:199], v[96:97] op_sel_hi:[1,0,1]
	s_nop 0
	v_pk_fma_f32 v[96:97], v[198:199], v[74:75], v[96:97] op_sel:[1,0,0]
	v_mov_b32_e32 v102, v201
	v_pk_fma_f32 v[96:97], v[200:201], v[106:107], v[96:97] op_sel_hi:[0,1,1]
	ds_read_b128 v[250:253], v25 offset:26672
	v_pk_fma_f32 v[96:97], v[102:103], v[72:73], v[96:97] op_sel_hi:[0,1,1]
	s_waitcnt lgkmcnt(8)
; #define LAS __attribute__((address_space(3)))
; __global__ void __launch_bounds__(NTHREADS, 2) hybrid_fwd(Args a) {
;     ...
; #pragma unroll
;                     for (int j = 0; j < 8; ++j) {
; #pragma unroll
;                         for (int e = 0; e < 16; ++e) { const f32x4 w = *(const LAS f32x4*)(rwT + e * 2052 + j * 256 + lane * 4);
;                             acc2[e] += y2[j][0] * (f32x2){w[0], w[0]}; acc2[e] += y2[j][1] * (f32x2){w[1], w[1]};
;                             acc2[e] += y2[j][2] * (f32x2){w[2], w[2]}; acc2[e] += y2[j][3] * (f32x2){w[3], w[3]}; }
;                         __builtin_amdgcn_sched_barrier(0);
;                     }
	v_pk_fma_f32 v[98:99], v[104:105], v[202:203], v[98:99] op_sel_hi:[1,0,1]
	s_nop 0
	v_pk_fma_f32 v[98:99], v[202:203], v[74:75], v[98:99] op_sel:[1,0,0]
	v_mov_b32_e32 v102, v205
	v_pk_fma_f32 v[98:99], v[204:205], v[106:107], v[98:99] op_sel_hi:[0,1,1]
	ds_read_b128 v[162:165], v25 offset:34880
	v_pk_fma_f32 v[98:99], v[102:103], v[72:73], v[98:99] op_sel_hi:[0,1,1]
	s_waitcnt lgkmcnt(8)
	v_pk_fma_f32 v[102:103], v[104:105], v[216:217], v[112:113] op_sel_hi:[1,0,1]
	s_nop 0
	v_pk_fma_f32 v[102:103], v[216:217], v[74:75], v[102:103] op_sel:[1,0,0]
	v_mov_b32_e32 v108, v219
	v_pk_fma_f32 v[102:103], v[218:219], v[106:107], v[102:103] op_sel_hi:[0,1,1]
	v_pk_fma_f32 v[102:103], v[108:109], v[72:73], v[102:103] op_sel_hi:[0,1,1]
	ds_read_b128 v[166:169], v25 offset:43088
	s_waitcnt lgkmcnt(8)
	v_pk_fma_f32 v[112:113], v[104:105], v[220:221], v[114:115] op_sel_hi:[1,0,1]
	s_nop 0
	v_pk_fma_f32 v[108:109], v[220:221], v[74:75], v[112:113] op_sel:[1,0,0]
	s_nop 0
	v_pk_fma_f32 v[108:109], v[222:223], v[106:107], v[108:109] op_sel_hi:[0,1,1]
	v_mov_b32_e32 v110, v223
	v_pk_fma_f32 v[108:109], v[110:111], v[72:73], v[108:109] op_sel_hi:[0,1,1]
	ds_read_b128 v[170:173], v25 offset:51296
	s_waitcnt lgkmcnt(8)
	v_pk_fma_f32 v[114:115], v[104:105], v[224:225], v[116:117] op_sel_hi:[1,0,1]
	s_nop 0
	v_pk_fma_f32 v[110:111], v[224:225], v[74:75], v[114:115] op_sel:[1,0,0]
	s_nop 0
	v_pk_fma_f32 v[110:111], v[226:227], v[106:107], v[110:111] op_sel_hi:[0,1,1]
	v_mov_b32_e32 v112, v227
	v_pk_fma_f32 v[110:111], v[112:113], v[72:73], v[110:111] op_sel_hi:[0,1,1]
	ds_read_b128 v[174:177], v25 offset:59504
	s_waitcnt lgkmcnt(8)
	v_pk_fma_f32 v[104:105], v[104:105], v[228:229], v[118:119] op_sel_hi:[1,0,1]
	s_nop 0
	v_pk_fma_f32 v[74:75], v[228:229], v[74:75], v[104:105] op_sel:[1,0,0]
	v_mov_b32_e32 v104, v231
	v_pk_fma_f32 v[74:75], v[230:231], v[106:107], v[74:75] op_sel_hi:[0,1,1]
	v_pk_fma_f32 v[104:105], v[104:105], v[72:73], v[74:75] op_sel_hi:[0,1,1]
	ds_read_b128 v[178:181], v238 offset:2176
	ds_read_b128 v[182:185], v238 offset:10384
	s_waitcnt lgkmcnt(8)
	v_pk_fma_f32 v[78:79], v[76:77], v[232:233], v[78:79] op_sel_hi:[1,0,1]
	s_nop 0
	v_pk_fma_f32 v[72:73], v[232:233], v[66:67], v[78:79] op_sel:[1,0,0]
	v_mov_b32_e32 v78, v245
	v_pk_fma_f32 v[72:73], v[234:235], v[82:83], v[72:73] op_sel_hi:[0,1,1]
	v_mov_b32_e32 v74, v235
	v_pk_fma_f32 v[72:73], v[74:75], v[64:65], v[72:73] op_sel_hi:[0,1,1]
	v_pk_fma_f32 v[74:75], v[76:77], v[242:243], v[120:121] op_sel_hi:[1,0,1]
	s_nop 0
	v_pk_fma_f32 v[74:75], v[242:243], v[66:67], v[74:75] op_sel:[1,0,0]
	s_nop 0
	v_pk_fma_f32 v[74:75], v[244:245], v[82:83], v[74:75] op_sel_hi:[0,1,1]
	ds_read_b128 v[186:189], v238 offset:18592
	v_pk_fma_f32 v[106:107], v[78:79], v[64:65], v[74:75] op_sel_hi:[0,1,1]
	s_waitcnt lgkmcnt(8)
	v_pk_fma_f32 v[74:75], v[76:77], v[246:247], v[100:101] op_sel_hi:[1,0,1]
	s_nop 0
	v_pk_fma_f32 v[74:75], v[246:247], v[66:67], v[74:75] op_sel:[1,0,0]
	v_mov_b32_e32 v78, v249
	v_pk_fma_f32 v[74:75], v[248:249], v[82:83], v[74:75] op_sel_hi:[0,1,1]
	ds_read_b128 v[198:201], v238 offset:26800
	v_pk_fma_f32 v[74:75], v[78:79], v[64:65], v[74:75] op_sel_hi:[0,1,1]
	s_waitcnt lgkmcnt(8)
	v_pk_fma_f32 v[78:79], v[76:77], v[250:251], v[80:81] op_sel_hi:[1,0,1]
	s_nop 0
	v_pk_fma_f32 v[78:79], v[250:251], v[66:67], v[78:79] op_sel:[1,0,0]
	v_mov_b32_e32 v80, v253
	v_pk_fma_f32 v[78:79], v[252:253], v[82:83], v[78:79] op_sel_hi:[0,1,1]
	ds_read_b128 v[202:205], v238 offset:35008
	v_pk_fma_f32 v[78:79], v[80:81], v[64:65], v[78:79] op_sel_hi:[0,1,1]
	s_waitcnt lgkmcnt(8)
	v_pk_fma_f32 v[80:81], v[76:77], v[162:163], v[84:85] op_sel_hi:[1,0,1]
	s_nop 0
	v_pk_fma_f32 v[80:81], v[162:163], v[66:67], v[80:81] op_sel:[1,0,0]
	v_mov_b32_e32 v84, v165
	v_pk_fma_f32 v[80:81], v[164:165], v[82:83], v[80:81] op_sel_hi:[0,1,1]
	ds_read_b128 v[158:161], v238 offset:51424
	v_pk_fma_f32 v[80:81], v[84:85], v[64:65], v[80:81] op_sel_hi:[0,1,1]
	s_waitcnt lgkmcnt(8)
	v_pk_fma_f32 v[84:85], v[76:77], v[166:167], v[86:87] op_sel_hi:[1,0,1]
	s_nop 0
	v_pk_fma_f32 v[84:85], v[166:167], v[66:67], v[84:85] op_sel:[1,0,0]
	v_mov_b32_e32 v86, v169
	v_pk_fma_f32 v[84:85], v[168:169], v[82:83], v[84:85] op_sel_hi:[0,1,1]
	ds_read_b128 v[216:219], v238 offset:43216
	v_pk_fma_f32 v[84:85], v[86:87], v[64:65], v[84:85] op_sel_hi:[0,1,1]
	s_waitcnt lgkmcnt(8)
	v_pk_fma_f32 v[86:87], v[76:77], v[170:171], v[88:89] op_sel_hi:[1,0,1]
	s_nop 0
	v_pk_fma_f32 v[86:87], v[170:171], v[66:67], v[86:87] op_sel:[1,0,0]
	v_mov_b32_e32 v88, v173
	v_pk_fma_f32 v[86:87], v[172:173], v[82:83], v[86:87] op_sel_hi:[0,1,1]
	ds_read_b128 v[220:223], v238 offset:59632
	v_pk_fma_f32 v[86:87], v[88:89], v[64:65], v[86:87] op_sel_hi:[0,1,1]
	s_waitcnt lgkmcnt(8)
	v_pk_fma_f32 v[88:89], v[76:77], v[174:175], v[90:91] op_sel_hi:[1,0,1]
	s_nop 0
	v_pk_fma_f32 v[88:89], v[174:175], v[66:67], v[88:89] op_sel:[1,0,0]
	v_mov_b32_e32 v90, v177
	v_pk_fma_f32 v[88:89], v[176:177], v[82:83], v[88:89] op_sel_hi:[0,1,1]
	ds_read_b128 v[224:227], v25 offset:3072
	v_pk_fma_f32 v[88:89], v[90:91], v[64:65], v[88:89] op_sel_hi:[0,1,1]
	s_waitcnt lgkmcnt(8)
	v_pk_fma_f32 v[90:91], v[76:77], v[178:179], v[92:93] op_sel_hi:[1,0,1]
	s_nop 0
	v_pk_fma_f32 v[90:91], v[178:179], v[66:67], v[90:91] op_sel:[1,0,0]
	v_mov_b32_e32 v92, v181
	v_pk_fma_f32 v[90:91], v[180:181], v[82:83], v[90:91] op_sel_hi:[0,1,1]
	ds_read_b128 v[228:231], v25 offset:11280
	v_pk_fma_f32 v[90:91], v[92:93], v[64:65], v[90:91] op_sel_hi:[0,1,1]
	s_waitcnt lgkmcnt(8)
; #define LAS __attribute__((address_space(3)))
; __global__ void __launch_bounds__(NTHREADS, 2) hybrid_fwd(Args a) {
;     ...
; #pragma unroll
;                     for (int j = 0; j < 8; ++j) {
; #pragma unroll
;                         for (int e = 0; e < 16; ++e) { const f32x4 w = *(const LAS f32x4*)(rwT + e * 2052 + j * 256 + lane * 4);
;                             acc2[e] += y2[j][0] * (f32x2){w[0], w[0]}; acc2[e] += y2[j][1] * (f32x2){w[1], w[1]};
;                             acc2[e] += y2[j][2] * (f32x2){w[2], w[2]}; acc2[e] += y2[j][3] * (f32x2){w[3], w[3]}; }
;                         __builtin_amdgcn_sched_barrier(0);
;                     }
	v_pk_fma_f32 v[92:93], v[76:77], v[182:183], v[94:95] op_sel_hi:[1,0,1]
	s_nop 0
	v_pk_fma_f32 v[92:93], v[182:183], v[66:67], v[92:93] op_sel:[1,0,0]
	v_mov_b32_e32 v94, v185
	v_pk_fma_f32 v[92:93], v[184:185], v[82:83], v[92:93] op_sel_hi:[0,1,1]
	ds_read_b128 v[232:235], v25 offset:19488
	v_pk_fma_f32 v[92:93], v[94:95], v[64:65], v[92:93] op_sel_hi:[0,1,1]
	s_waitcnt lgkmcnt(8)
	v_pk_fma_f32 v[94:95], v[76:77], v[186:187], v[96:97] op_sel_hi:[1,0,1]
	s_nop 0
	v_pk_fma_f32 v[94:95], v[186:187], v[66:67], v[94:95] op_sel:[1,0,0]
	v_mov_b32_e32 v96, v189
	v_pk_fma_f32 v[94:95], v[188:189], v[82:83], v[94:95] op_sel_hi:[0,1,1]
	ds_read_b128 v[242:245], v25 offset:27696
	v_pk_fma_f32 v[94:95], v[96:97], v[64:65], v[94:95] op_sel_hi:[0,1,1]
	s_waitcnt lgkmcnt(8)
	v_pk_fma_f32 v[96:97], v[76:77], v[198:199], v[98:99] op_sel_hi:[1,0,1]
	s_nop 0
	v_pk_fma_f32 v[96:97], v[198:199], v[66:67], v[96:97] op_sel:[1,0,0]
	v_mov_b32_e32 v98, v201
	v_pk_fma_f32 v[96:97], v[200:201], v[82:83], v[96:97] op_sel_hi:[0,1,1]
	v_pk_fma_f32 v[96:97], v[98:99], v[64:65], v[96:97] op_sel_hi:[0,1,1]
	ds_read_b128 v[246:249], v25 offset:35904
	ds_read_b128 v[250:253], v25 offset:44112
	s_waitcnt lgkmcnt(8)
	v_pk_fma_f32 v[102:103], v[76:77], v[202:203], v[102:103] op_sel_hi:[1,0,1]
	s_nop 0
	v_pk_fma_f32 v[98:99], v[202:203], v[66:67], v[102:103] op_sel:[1,0,0]
	s_nop 0
	v_pk_fma_f32 v[98:99], v[204:205], v[82:83], v[98:99] op_sel_hi:[0,1,1]
	v_mov_b32_e32 v100, v205
	v_pk_fma_f32 v[98:99], v[100:101], v[64:65], v[98:99] op_sel_hi:[0,1,1]
	ds_read_b128 v[162:165], v25 offset:52320
	s_waitcnt lgkmcnt(8)
	v_pk_fma_f32 v[108:109], v[76:77], v[216:217], v[108:109] op_sel_hi:[1,0,1]
	s_nop 0
	v_pk_fma_f32 v[100:101], v[216:217], v[66:67], v[108:109] op_sel:[1,0,0]
	v_mov_b32_e32 v108, v161
	v_pk_fma_f32 v[100:101], v[218:219], v[82:83], v[100:101] op_sel_hi:[0,1,1]
	v_mov_b32_e32 v102, v219
	v_pk_fma_f32 v[100:101], v[102:103], v[64:65], v[100:101] op_sel_hi:[0,1,1]
	v_pk_fma_f32 v[102:103], v[76:77], v[158:159], v[110:111] op_sel_hi:[1,0,1]
	s_nop 0
	v_pk_fma_f32 v[102:103], v[158:159], v[66:67], v[102:103] op_sel:[1,0,0]
	s_nop 0
	v_pk_fma_f32 v[102:103], v[160:161], v[82:83], v[102:103] op_sel_hi:[0,1,1]
	v_pk_fma_f32 v[102:103], v[108:109], v[64:65], v[102:103] op_sel_hi:[0,1,1]
	ds_read_b128 v[166:169], v25 offset:60528
	s_waitcnt lgkmcnt(8)
	v_pk_fma_f32 v[76:77], v[76:77], v[220:221], v[104:105] op_sel_hi:[1,0,1]
	s_nop 0
	v_pk_fma_f32 v[66:67], v[220:221], v[66:67], v[76:77] op_sel:[1,0,0]
	v_mov_b32_e32 v76, v223
	v_pk_fma_f32 v[66:67], v[222:223], v[82:83], v[66:67] op_sel_hi:[0,1,1]
	v_pk_fma_f32 v[104:105], v[76:77], v[64:65], v[66:67] op_sel_hi:[0,1,1]
	ds_read_b128 v[170:173], v238 offset:3200
	ds_read_b128 v[174:177], v238 offset:11408
	s_waitcnt lgkmcnt(8)
	v_pk_fma_f32 v[72:73], v[68:69], v[224:225], v[72:73] op_sel_hi:[1,0,1]
	s_nop 0
	v_pk_fma_f32 v[64:65], v[224:225], v[58:59], v[72:73] op_sel:[1,0,0]
	v_mov_b32_e32 v72, v231
	v_pk_fma_f32 v[64:65], v[226:227], v[70:71], v[64:65] op_sel_hi:[0,1,1]
	v_mov_b32_e32 v66, v227
	v_pk_fma_f32 v[64:65], v[66:67], v[56:57], v[64:65] op_sel_hi:[0,1,1]
	v_pk_fma_f32 v[66:67], v[68:69], v[228:229], v[106:107] op_sel_hi:[1,0,1]
	s_nop 0
	v_pk_fma_f32 v[66:67], v[228:229], v[58:59], v[66:67] op_sel:[1,0,0]
	s_nop 0
	v_pk_fma_f32 v[66:67], v[230:231], v[70:71], v[66:67] op_sel_hi:[0,1,1]
	ds_read_b128 v[178:181], v238 offset:19616
	v_pk_fma_f32 v[106:107], v[72:73], v[56:57], v[66:67] op_sel_hi:[0,1,1]
	s_waitcnt lgkmcnt(8)
	v_pk_fma_f32 v[66:67], v[68:69], v[232:233], v[74:75] op_sel_hi:[1,0,1]
	s_nop 0
	v_pk_fma_f32 v[66:67], v[232:233], v[58:59], v[66:67] op_sel:[1,0,0]
	v_mov_b32_e32 v72, v235
	v_pk_fma_f32 v[66:67], v[234:235], v[70:71], v[66:67] op_sel_hi:[0,1,1]
	v_pk_fma_f32 v[66:67], v[72:73], v[56:57], v[66:67] op_sel_hi:[0,1,1]
	ds_read_b128 v[182:185], v238 offset:27824
	s_waitcnt lgkmcnt(8)
	v_pk_fma_f32 v[76:77], v[68:69], v[242:243], v[78:79] op_sel_hi:[1,0,1]
	s_nop 0
	v_pk_fma_f32 v[72:73], v[242:243], v[58:59], v[76:77] op_sel:[1,0,0]
	s_nop 0
	v_pk_fma_f32 v[72:73], v[244:245], v[70:71], v[72:73] op_sel_hi:[0,1,1]
	v_mov_b32_e32 v74, v245
	v_pk_fma_f32 v[72:73], v[74:75], v[56:57], v[72:73] op_sel_hi:[0,1,1]
	ds_read_b128 v[186:189], v238 offset:36032
	s_waitcnt lgkmcnt(8)
	v_pk_fma_f32 v[78:79], v[68:69], v[246:247], v[80:81] op_sel_hi:[1,0,1]
	s_nop 0
	v_pk_fma_f32 v[74:75], v[246:247], v[58:59], v[78:79] op_sel:[1,0,0]
	s_nop 0
	v_pk_fma_f32 v[74:75], v[248:249], v[70:71], v[74:75] op_sel_hi:[0,1,1]
	v_mov_b32_e32 v76, v249
	v_pk_fma_f32 v[74:75], v[76:77], v[56:57], v[74:75] op_sel_hi:[0,1,1]
	ds_read_b128 v[198:201], v238 offset:44240
	s_waitcnt lgkmcnt(8)
	v_pk_fma_f32 v[80:81], v[68:69], v[250:251], v[84:85] op_sel_hi:[1,0,1]
	s_nop 0
	v_pk_fma_f32 v[76:77], v[250:251], v[58:59], v[80:81] op_sel:[1,0,0]
	s_nop 0
	v_pk_fma_f32 v[76:77], v[252:253], v[70:71], v[76:77] op_sel_hi:[0,1,1]
	v_mov_b32_e32 v78, v253
	v_pk_fma_f32 v[76:77], v[78:79], v[56:57], v[76:77] op_sel_hi:[0,1,1]
	ds_read_b128 v[202:205], v238 offset:52448
	s_waitcnt lgkmcnt(8)
	v_pk_fma_f32 v[82:83], v[68:69], v[162:163], v[86:87] op_sel_hi:[1,0,1]
	s_nop 0
	v_pk_fma_f32 v[78:79], v[162:163], v[58:59], v[82:83] op_sel:[1,0,0]
	s_nop 0
	v_pk_fma_f32 v[78:79], v[164:165], v[70:71], v[78:79] op_sel_hi:[0,1,1]
	v_mov_b32_e32 v80, v165
	v_pk_fma_f32 v[78:79], v[80:81], v[56:57], v[78:79] op_sel_hi:[0,1,1]
	ds_read_b128 v[216:219], v238 offset:60656
	s_waitcnt lgkmcnt(8)
; #define LAS __attribute__((address_space(3)))
; __global__ void __launch_bounds__(NTHREADS, 2) hybrid_fwd(Args a) {
;     ...
; #pragma unroll
;                     for (int j = 0; j < 8; ++j) {
; #pragma unroll
;                         for (int e = 0; e < 16; ++e) { const f32x4 w = *(const LAS f32x4*)(rwT + e * 2052 + j * 256 + lane * 4);
;                             acc2[e] += y2[j][0] * (f32x2){w[0], w[0]}; acc2[e] += y2[j][1] * (f32x2){w[1], w[1]};
;                             acc2[e] += y2[j][2] * (f32x2){w[2], w[2]}; acc2[e] += y2[j][3] * (f32x2){w[3], w[3]}; }
;                         __builtin_amdgcn_sched_barrier(0);
;                     }
	v_pk_fma_f32 v[84:85], v[68:69], v[166:167], v[88:89] op_sel_hi:[1,0,1]
	s_nop 0
	v_pk_fma_f32 v[80:81], v[166:167], v[58:59], v[84:85] op_sel:[1,0,0]
	s_nop 0
	v_pk_fma_f32 v[80:81], v[168:169], v[70:71], v[80:81] op_sel_hi:[0,1,1]
	v_mov_b32_e32 v82, v169
	v_pk_fma_f32 v[80:81], v[82:83], v[56:57], v[80:81] op_sel_hi:[0,1,1]
	ds_read_b128 v[158:161], v25 offset:4096
	s_waitcnt lgkmcnt(8)
	v_pk_fma_f32 v[86:87], v[68:69], v[170:171], v[90:91] op_sel_hi:[1,0,1]
	s_nop 0
	v_pk_fma_f32 v[82:83], v[170:171], v[58:59], v[86:87] op_sel:[1,0,0]
	s_nop 0
	v_pk_fma_f32 v[82:83], v[172:173], v[70:71], v[82:83] op_sel_hi:[0,1,1]
	v_mov_b32_e32 v84, v173
	v_pk_fma_f32 v[82:83], v[84:85], v[56:57], v[82:83] op_sel_hi:[0,1,1]
	ds_read_b128 v[220:223], v25 offset:12304
	s_waitcnt lgkmcnt(8)
	v_pk_fma_f32 v[88:89], v[68:69], v[174:175], v[92:93] op_sel_hi:[1,0,1]
	s_nop 0
	v_pk_fma_f32 v[84:85], v[174:175], v[58:59], v[88:89] op_sel:[1,0,0]
	s_nop 0
	v_pk_fma_f32 v[84:85], v[176:177], v[70:71], v[84:85] op_sel_hi:[0,1,1]
	v_mov_b32_e32 v86, v177
	v_pk_fma_f32 v[84:85], v[86:87], v[56:57], v[84:85] op_sel_hi:[0,1,1]
	ds_read_b128 v[224:227], v25 offset:20512
	s_waitcnt lgkmcnt(8)
	v_pk_fma_f32 v[90:91], v[68:69], v[178:179], v[94:95] op_sel_hi:[1,0,1]
	s_nop 0
	v_pk_fma_f32 v[86:87], v[178:179], v[58:59], v[90:91] op_sel:[1,0,0]
	s_nop 0
	v_pk_fma_f32 v[86:87], v[180:181], v[70:71], v[86:87] op_sel_hi:[0,1,1]
	v_mov_b32_e32 v88, v181
	v_pk_fma_f32 v[86:87], v[88:89], v[56:57], v[86:87] op_sel_hi:[0,1,1]
	ds_read_b128 v[228:231], v25 offset:28720
	s_waitcnt lgkmcnt(8)
	v_pk_fma_f32 v[92:93], v[68:69], v[182:183], v[96:97] op_sel_hi:[1,0,1]
	s_nop 0
	v_pk_fma_f32 v[88:89], v[182:183], v[58:59], v[92:93] op_sel:[1,0,0]
	s_nop 0
	v_pk_fma_f32 v[88:89], v[184:185], v[70:71], v[88:89] op_sel_hi:[0,1,1]
	v_mov_b32_e32 v90, v185
	v_pk_fma_f32 v[88:89], v[90:91], v[56:57], v[88:89] op_sel_hi:[0,1,1]
	ds_read_b128 v[232:235], v25 offset:36928
	s_waitcnt lgkmcnt(8)
	v_pk_fma_f32 v[94:95], v[68:69], v[186:187], v[98:99] op_sel_hi:[1,0,1]
	s_nop 0
	v_pk_fma_f32 v[90:91], v[186:187], v[58:59], v[94:95] op_sel:[1,0,0]
	s_nop 0
	v_pk_fma_f32 v[90:91], v[188:189], v[70:71], v[90:91] op_sel_hi:[0,1,1]
	v_mov_b32_e32 v92, v189
	v_pk_fma_f32 v[90:91], v[92:93], v[56:57], v[90:91] op_sel_hi:[0,1,1]
	ds_read_b128 v[242:245], v25 offset:45136
	s_waitcnt lgkmcnt(8)
	v_pk_fma_f32 v[96:97], v[68:69], v[198:199], v[100:101] op_sel_hi:[1,0,1]
	s_nop 0
	v_pk_fma_f32 v[92:93], v[198:199], v[58:59], v[96:97] op_sel:[1,0,0]
	s_nop 0
	v_pk_fma_f32 v[92:93], v[200:201], v[70:71], v[92:93] op_sel_hi:[0,1,1]
	v_mov_b32_e32 v94, v201
	v_pk_fma_f32 v[92:93], v[94:95], v[56:57], v[92:93] op_sel_hi:[0,1,1]
	ds_read_b128 v[246:249], v25 offset:53344
	s_waitcnt lgkmcnt(8)
	v_pk_fma_f32 v[98:99], v[68:69], v[202:203], v[102:103] op_sel_hi:[1,0,1]
	s_nop 0
	v_pk_fma_f32 v[94:95], v[202:203], v[58:59], v[98:99] op_sel:[1,0,0]
	s_nop 0
	v_pk_fma_f32 v[94:95], v[204:205], v[70:71], v[94:95] op_sel_hi:[0,1,1]
	v_mov_b32_e32 v96, v205
	v_pk_fma_f32 v[94:95], v[96:97], v[56:57], v[94:95] op_sel_hi:[0,1,1]
	ds_read_b128 v[250:253], v25 offset:61552
	s_waitcnt lgkmcnt(8)
	v_pk_fma_f32 v[68:69], v[68:69], v[216:217], v[104:105] op_sel_hi:[1,0,1]
	s_nop 0
	v_pk_fma_f32 v[58:59], v[216:217], v[58:59], v[68:69] op_sel:[1,0,0]
	v_mov_b32_e32 v68, v219
	v_pk_fma_f32 v[58:59], v[218:219], v[70:71], v[58:59] op_sel_hi:[0,1,1]
	v_pk_fma_f32 v[96:97], v[68:69], v[56:57], v[58:59] op_sel_hi:[0,1,1]
	ds_read_b128 v[162:165], v238 offset:4224
	ds_read_b128 v[166:169], v238 offset:12432
	s_waitcnt lgkmcnt(8)
	v_pk_fma_f32 v[64:65], v[60:61], v[158:159], v[64:65] op_sel_hi:[1,0,1]
	s_nop 0
	v_pk_fma_f32 v[56:57], v[158:159], v[54:55], v[64:65] op_sel:[1,0,0]
	v_mov_b32_e32 v64, v223
	v_pk_fma_f32 v[56:57], v[160:161], v[62:63], v[56:57] op_sel_hi:[0,1,1]
	v_mov_b32_e32 v58, v161
	v_pk_fma_f32 v[56:57], v[58:59], v[52:53], v[56:57] op_sel_hi:[0,1,1]
	v_pk_fma_f32 v[58:59], v[60:61], v[220:221], v[106:107] op_sel_hi:[1,0,1]
	s_nop 0
	v_pk_fma_f32 v[58:59], v[220:221], v[54:55], v[58:59] op_sel:[1,0,0]
	s_nop 0
	v_pk_fma_f32 v[58:59], v[222:223], v[62:63], v[58:59] op_sel_hi:[0,1,1]
	ds_read_b128 v[170:173], v238 offset:20640
	v_pk_fma_f32 v[98:99], v[64:65], v[52:53], v[58:59] op_sel_hi:[0,1,1]
	s_waitcnt lgkmcnt(8)
	v_pk_fma_f32 v[58:59], v[60:61], v[224:225], v[66:67] op_sel_hi:[1,0,1]
	s_nop 0
	v_pk_fma_f32 v[58:59], v[224:225], v[54:55], v[58:59] op_sel:[1,0,0]
	v_mov_b32_e32 v64, v227
	v_pk_fma_f32 v[58:59], v[226:227], v[62:63], v[58:59] op_sel_hi:[0,1,1]
	v_pk_fma_f32 v[58:59], v[64:65], v[52:53], v[58:59] op_sel_hi:[0,1,1]
	ds_read_b128 v[174:177], v238 offset:28848
	s_waitcnt lgkmcnt(8)
	v_pk_fma_f32 v[68:69], v[60:61], v[228:229], v[72:73] op_sel_hi:[1,0,1]
	s_nop 0
	v_pk_fma_f32 v[64:65], v[228:229], v[54:55], v[68:69] op_sel:[1,0,0]
	s_nop 0
	v_pk_fma_f32 v[64:65], v[230:231], v[62:63], v[64:65] op_sel_hi:[0,1,1]
	v_mov_b32_e32 v66, v231
	v_pk_fma_f32 v[64:65], v[66:67], v[52:53], v[64:65] op_sel_hi:[0,1,1]
	ds_read_b128 v[178:181], v238 offset:37056
	s_waitcnt lgkmcnt(8)
	v_pk_fma_f32 v[70:71], v[60:61], v[232:233], v[74:75] op_sel_hi:[1,0,1]
	s_nop 0
	v_pk_fma_f32 v[66:67], v[232:233], v[54:55], v[70:71] op_sel:[1,0,0]
	s_nop 0
	v_pk_fma_f32 v[66:67], v[234:235], v[62:63], v[66:67] op_sel_hi:[0,1,1]
	v_mov_b32_e32 v68, v235
	v_pk_fma_f32 v[66:67], v[68:69], v[52:53], v[66:67] op_sel_hi:[0,1,1]
	ds_read_b128 v[182:185], v238 offset:45264
	s_waitcnt lgkmcnt(8)
; #define LAS __attribute__((address_space(3)))
; __global__ void __launch_bounds__(NTHREADS, 2) hybrid_fwd(Args a) {
;     ...
; #pragma unroll
;                     for (int j = 0; j < 8; ++j) {
; #pragma unroll
;                         for (int e = 0; e < 16; ++e) { const f32x4 w = *(const LAS f32x4*)(rwT + e * 2052 + j * 256 + lane * 4);
;                             acc2[e] += y2[j][0] * (f32x2){w[0], w[0]}; acc2[e] += y2[j][1] * (f32x2){w[1], w[1]};
;                             acc2[e] += y2[j][2] * (f32x2){w[2], w[2]}; acc2[e] += y2[j][3] * (f32x2){w[3], w[3]}; }
;                         __builtin_amdgcn_sched_barrier(0);
;                     }
	v_pk_fma_f32 v[72:73], v[60:61], v[242:243], v[76:77] op_sel_hi:[1,0,1]
	s_nop 0
	v_pk_fma_f32 v[68:69], v[242:243], v[54:55], v[72:73] op_sel:[1,0,0]
	s_nop 0
	v_pk_fma_f32 v[68:69], v[244:245], v[62:63], v[68:69] op_sel_hi:[0,1,1]
	v_mov_b32_e32 v70, v245
	v_pk_fma_f32 v[68:69], v[70:71], v[52:53], v[68:69] op_sel_hi:[0,1,1]
	ds_read_b128 v[186:189], v238 offset:53472
	s_waitcnt lgkmcnt(8)
	v_pk_fma_f32 v[74:75], v[60:61], v[246:247], v[78:79] op_sel_hi:[1,0,1]
	s_nop 0
	v_pk_fma_f32 v[70:71], v[246:247], v[54:55], v[74:75] op_sel:[1,0,0]
	s_nop 0
	v_pk_fma_f32 v[70:71], v[248:249], v[62:63], v[70:71] op_sel_hi:[0,1,1]
	v_mov_b32_e32 v72, v249
	v_pk_fma_f32 v[70:71], v[72:73], v[52:53], v[70:71] op_sel_hi:[0,1,1]
	ds_read_b128 v[198:201], v238 offset:61680
	s_waitcnt lgkmcnt(8)
	v_pk_fma_f32 v[76:77], v[60:61], v[250:251], v[80:81] op_sel_hi:[1,0,1]
	s_nop 0
	v_pk_fma_f32 v[72:73], v[250:251], v[54:55], v[76:77] op_sel:[1,0,0]
	s_nop 0
	v_pk_fma_f32 v[72:73], v[252:253], v[62:63], v[72:73] op_sel_hi:[0,1,1]
	v_mov_b32_e32 v74, v253
	v_pk_fma_f32 v[72:73], v[74:75], v[52:53], v[72:73] op_sel_hi:[0,1,1]
	ds_read_b128 v[202:205], v25 offset:5120
	s_waitcnt lgkmcnt(8)
	v_pk_fma_f32 v[78:79], v[60:61], v[162:163], v[82:83] op_sel_hi:[1,0,1]
	s_nop 0
	v_pk_fma_f32 v[74:75], v[162:163], v[54:55], v[78:79] op_sel:[1,0,0]
	s_nop 0
	v_pk_fma_f32 v[74:75], v[164:165], v[62:63], v[74:75] op_sel_hi:[0,1,1]
	v_mov_b32_e32 v76, v165
	v_pk_fma_f32 v[74:75], v[76:77], v[52:53], v[74:75] op_sel_hi:[0,1,1]
	ds_read_b128 v[216:219], v25 offset:13328
	s_waitcnt lgkmcnt(8)
	v_pk_fma_f32 v[80:81], v[60:61], v[166:167], v[84:85] op_sel_hi:[1,0,1]
	s_nop 0
	v_pk_fma_f32 v[76:77], v[166:167], v[54:55], v[80:81] op_sel:[1,0,0]
	s_nop 0
	v_pk_fma_f32 v[76:77], v[168:169], v[62:63], v[76:77] op_sel_hi:[0,1,1]
	v_mov_b32_e32 v78, v169
	v_pk_fma_f32 v[76:77], v[78:79], v[52:53], v[76:77] op_sel_hi:[0,1,1]
	ds_read_b128 v[158:161], v25 offset:21536
	s_waitcnt lgkmcnt(8)
	v_pk_fma_f32 v[82:83], v[60:61], v[170:171], v[86:87] op_sel_hi:[1,0,1]
	s_nop 0
	v_pk_fma_f32 v[78:79], v[170:171], v[54:55], v[82:83] op_sel:[1,0,0]
	s_nop 0
	v_pk_fma_f32 v[78:79], v[172:173], v[62:63], v[78:79] op_sel_hi:[0,1,1]
	v_mov_b32_e32 v80, v173
	v_pk_fma_f32 v[78:79], v[80:81], v[52:53], v[78:79] op_sel_hi:[0,1,1]
	ds_read_b128 v[220:223], v25 offset:29744
	s_waitcnt lgkmcnt(8)
	v_pk_fma_f32 v[84:85], v[60:61], v[174:175], v[88:89] op_sel_hi:[1,0,1]
	s_nop 0
	v_pk_fma_f32 v[80:81], v[174:175], v[54:55], v[84:85] op_sel:[1,0,0]
	s_nop 0
	v_pk_fma_f32 v[80:81], v[176:177], v[62:63], v[80:81] op_sel_hi:[0,1,1]
	v_mov_b32_e32 v82, v177
	v_pk_fma_f32 v[80:81], v[82:83], v[52:53], v[80:81] op_sel_hi:[0,1,1]
	ds_read_b128 v[224:227], v25 offset:37952
	s_waitcnt lgkmcnt(8)
	v_pk_fma_f32 v[86:87], v[60:61], v[178:179], v[90:91] op_sel_hi:[1,0,1]
	s_nop 0
	v_pk_fma_f32 v[82:83], v[178:179], v[54:55], v[86:87] op_sel:[1,0,0]
	s_nop 0
	v_pk_fma_f32 v[82:83], v[180:181], v[62:63], v[82:83] op_sel_hi:[0,1,1]
	v_mov_b32_e32 v84, v181
	v_pk_fma_f32 v[82:83], v[84:85], v[52:53], v[82:83] op_sel_hi:[0,1,1]
	ds_read_b128 v[228:231], v25 offset:46160
	s_waitcnt lgkmcnt(8)
	v_pk_fma_f32 v[88:89], v[60:61], v[182:183], v[92:93] op_sel_hi:[1,0,1]
	s_nop 0
	v_pk_fma_f32 v[84:85], v[182:183], v[54:55], v[88:89] op_sel:[1,0,0]
	s_nop 0
	v_pk_fma_f32 v[84:85], v[184:185], v[62:63], v[84:85] op_sel_hi:[0,1,1]
	v_mov_b32_e32 v86, v185
	v_pk_fma_f32 v[84:85], v[86:87], v[52:53], v[84:85] op_sel_hi:[0,1,1]
	ds_read_b128 v[232:235], v25 offset:54368
	s_waitcnt lgkmcnt(8)
	v_pk_fma_f32 v[90:91], v[60:61], v[186:187], v[94:95] op_sel_hi:[1,0,1]
	s_nop 0
	v_pk_fma_f32 v[86:87], v[186:187], v[54:55], v[90:91] op_sel:[1,0,0]
	s_nop 0
	v_pk_fma_f32 v[86:87], v[188:189], v[62:63], v[86:87] op_sel_hi:[0,1,1]
	v_mov_b32_e32 v88, v189
	v_pk_fma_f32 v[86:87], v[88:89], v[52:53], v[86:87] op_sel_hi:[0,1,1]
	ds_read_b128 v[242:245], v25 offset:62576
	s_waitcnt lgkmcnt(8)
	v_pk_fma_f32 v[60:61], v[60:61], v[198:199], v[96:97] op_sel_hi:[1,0,1]
	s_nop 0
	v_pk_fma_f32 v[54:55], v[198:199], v[54:55], v[60:61] op_sel:[1,0,0]
	v_mov_b32_e32 v60, v201
	v_pk_fma_f32 v[54:55], v[200:201], v[62:63], v[54:55] op_sel_hi:[0,1,1]
	v_pk_fma_f32 v[88:89], v[60:61], v[52:53], v[54:55] op_sel_hi:[0,1,1]
	ds_read_b128 v[246:249], v238 offset:5248
	s_waitcnt lgkmcnt(8)
	v_pk_fma_f32 v[56:57], v[48:49], v[202:203], v[56:57] op_sel_hi:[1,0,1]
	s_nop 0
	v_pk_fma_f32 v[52:53], v[202:203], v[46:47], v[56:57] op_sel:[1,0,0]
	s_nop 0
	v_pk_fma_f32 v[52:53], v[204:205], v[50:51], v[52:53] op_sel_hi:[0,1,1]
	v_mov_b32_e32 v54, v205
	v_pk_fma_f32 v[52:53], v[54:55], v[44:45], v[52:53] op_sel_hi:[0,1,1]
	ds_read_b128 v[250:253], v238 offset:13456
	s_waitcnt lgkmcnt(8)
	v_pk_fma_f32 v[60:61], v[48:49], v[216:217], v[98:99] op_sel_hi:[1,0,1]
	s_nop 0
	v_pk_fma_f32 v[54:55], v[216:217], v[46:47], v[60:61] op_sel:[1,0,0]
	s_nop 0
	v_pk_fma_f32 v[54:55], v[218:219], v[50:51], v[54:55] op_sel_hi:[0,1,1]
	v_mov_b32_e32 v56, v219
	v_pk_fma_f32 v[90:91], v[56:57], v[44:45], v[54:55] op_sel_hi:[0,1,1]
	ds_read_b128 v[162:165], v238 offset:21664
	s_waitcnt lgkmcnt(8)
	v_pk_fma_f32 v[58:59], v[48:49], v[158:159], v[58:59] op_sel_hi:[1,0,1]
	s_nop 0
	v_pk_fma_f32 v[54:55], v[158:159], v[46:47], v[58:59] op_sel:[1,0,0]
	s_nop 0
	v_pk_fma_f32 v[54:55], v[160:161], v[50:51], v[54:55] op_sel_hi:[0,1,1]
	v_mov_b32_e32 v56, v161
	v_pk_fma_f32 v[54:55], v[56:57], v[44:45], v[54:55] op_sel_hi:[0,1,1]
	ds_read_b128 v[166:169], v238 offset:29872
	s_waitcnt lgkmcnt(8)
; #define LAS __attribute__((address_space(3)))
; __global__ void __launch_bounds__(NTHREADS, 2) hybrid_fwd(Args a) {
;     ...
; #pragma unroll
;                     for (int j = 0; j < 8; ++j) {
; #pragma unroll
;                         for (int e = 0; e < 16; ++e) { const f32x4 w = *(const LAS f32x4*)(rwT + e * 2052 + j * 256 + lane * 4);
;                             acc2[e] += y2[j][0] * (f32x2){w[0], w[0]}; acc2[e] += y2[j][1] * (f32x2){w[1], w[1]};
;                             acc2[e] += y2[j][2] * (f32x2){w[2], w[2]}; acc2[e] += y2[j][3] * (f32x2){w[3], w[3]}; }
;                         __builtin_amdgcn_sched_barrier(0);
;                     }
	v_pk_fma_f32 v[60:61], v[48:49], v[220:221], v[64:65] op_sel_hi:[1,0,1]
	s_nop 0
	v_pk_fma_f32 v[56:57], v[220:221], v[46:47], v[60:61] op_sel:[1,0,0]
	s_nop 0
	v_pk_fma_f32 v[56:57], v[222:223], v[50:51], v[56:57] op_sel_hi:[0,1,1]
	v_mov_b32_e32 v58, v223
	v_pk_fma_f32 v[56:57], v[58:59], v[44:45], v[56:57] op_sel_hi:[0,1,1]
	ds_read_b128 v[170:173], v238 offset:38080
	s_waitcnt lgkmcnt(8)
	v_pk_fma_f32 v[62:63], v[48:49], v[224:225], v[66:67] op_sel_hi:[1,0,1]
	s_nop 0
	v_pk_fma_f32 v[58:59], v[224:225], v[46:47], v[62:63] op_sel:[1,0,0]
	s_nop 0
	v_pk_fma_f32 v[58:59], v[226:227], v[50:51], v[58:59] op_sel_hi:[0,1,1]
	v_mov_b32_e32 v60, v227
	v_pk_fma_f32 v[58:59], v[60:61], v[44:45], v[58:59] op_sel_hi:[0,1,1]
	ds_read_b128 v[174:177], v238 offset:46288
	s_waitcnt lgkmcnt(8)
	v_pk_fma_f32 v[64:65], v[48:49], v[228:229], v[68:69] op_sel_hi:[1,0,1]
	s_nop 0
	v_pk_fma_f32 v[60:61], v[228:229], v[46:47], v[64:65] op_sel:[1,0,0]
	s_nop 0
	v_pk_fma_f32 v[60:61], v[230:231], v[50:51], v[60:61] op_sel_hi:[0,1,1]
	v_mov_b32_e32 v62, v231
	v_pk_fma_f32 v[60:61], v[62:63], v[44:45], v[60:61] op_sel_hi:[0,1,1]
	ds_read_b128 v[178:181], v238 offset:54496
	s_waitcnt lgkmcnt(8)
	v_pk_fma_f32 v[66:67], v[48:49], v[232:233], v[70:71] op_sel_hi:[1,0,1]
	s_nop 0
	v_pk_fma_f32 v[62:63], v[232:233], v[46:47], v[66:67] op_sel:[1,0,0]
	s_nop 0
	v_pk_fma_f32 v[62:63], v[234:235], v[50:51], v[62:63] op_sel_hi:[0,1,1]
	v_mov_b32_e32 v64, v235
	v_pk_fma_f32 v[62:63], v[64:65], v[44:45], v[62:63] op_sel_hi:[0,1,1]
	ds_read_b128 v[182:185], v238 offset:62704
	s_waitcnt lgkmcnt(8)
	v_pk_fma_f32 v[68:69], v[48:49], v[242:243], v[72:73] op_sel_hi:[1,0,1]
	s_nop 0
	v_pk_fma_f32 v[64:65], v[242:243], v[46:47], v[68:69] op_sel:[1,0,0]
	s_nop 0
	v_pk_fma_f32 v[64:65], v[244:245], v[50:51], v[64:65] op_sel_hi:[0,1,1]
	v_mov_b32_e32 v66, v245
	v_pk_fma_f32 v[64:65], v[66:67], v[44:45], v[64:65] op_sel_hi:[0,1,1]
	ds_read_b128 v[186:189], v25 offset:6144
	s_waitcnt lgkmcnt(8)
	v_pk_fma_f32 v[70:71], v[48:49], v[246:247], v[74:75] op_sel_hi:[1,0,1]
	s_nop 0
	v_pk_fma_f32 v[66:67], v[246:247], v[46:47], v[70:71] op_sel:[1,0,0]
	s_nop 0
	v_pk_fma_f32 v[66:67], v[248:249], v[50:51], v[66:67] op_sel_hi:[0,1,1]
	v_mov_b32_e32 v68, v249
	v_pk_fma_f32 v[66:67], v[68:69], v[44:45], v[66:67] op_sel_hi:[0,1,1]
	ds_read_b128 v[198:201], v25 offset:14352
	s_waitcnt lgkmcnt(8)
	v_pk_fma_f32 v[72:73], v[48:49], v[250:251], v[76:77] op_sel_hi:[1,0,1]
	s_nop 0
	v_pk_fma_f32 v[68:69], v[250:251], v[46:47], v[72:73] op_sel:[1,0,0]
	s_nop 0
	v_pk_fma_f32 v[68:69], v[252:253], v[50:51], v[68:69] op_sel_hi:[0,1,1]
	v_mov_b32_e32 v70, v253
	v_pk_fma_f32 v[68:69], v[70:71], v[44:45], v[68:69] op_sel_hi:[0,1,1]
	ds_read_b128 v[202:205], v25 offset:22560
	s_waitcnt lgkmcnt(8)
	v_pk_fma_f32 v[74:75], v[48:49], v[162:163], v[78:79] op_sel_hi:[1,0,1]
	s_nop 0
	v_pk_fma_f32 v[70:71], v[162:163], v[46:47], v[74:75] op_sel:[1,0,0]
	s_nop 0
	v_pk_fma_f32 v[70:71], v[164:165], v[50:51], v[70:71] op_sel_hi:[0,1,1]
	v_mov_b32_e32 v72, v165
	v_pk_fma_f32 v[70:71], v[72:73], v[44:45], v[70:71] op_sel_hi:[0,1,1]
	ds_read_b128 v[216:219], v25 offset:30768
	s_waitcnt lgkmcnt(8)
	v_pk_fma_f32 v[76:77], v[48:49], v[166:167], v[80:81] op_sel_hi:[1,0,1]
	s_nop 0
	v_pk_fma_f32 v[72:73], v[166:167], v[46:47], v[76:77] op_sel:[1,0,0]
	s_nop 0
	v_pk_fma_f32 v[72:73], v[168:169], v[50:51], v[72:73] op_sel_hi:[0,1,1]
	v_mov_b32_e32 v74, v169
	v_pk_fma_f32 v[72:73], v[74:75], v[44:45], v[72:73] op_sel_hi:[0,1,1]
	ds_read_b128 v[158:161], v25 offset:38976
	s_waitcnt lgkmcnt(8)
	v_pk_fma_f32 v[78:79], v[48:49], v[170:171], v[82:83] op_sel_hi:[1,0,1]
	s_nop 0
	v_pk_fma_f32 v[74:75], v[170:171], v[46:47], v[78:79] op_sel:[1,0,0]
	s_nop 0
	v_pk_fma_f32 v[74:75], v[172:173], v[50:51], v[74:75] op_sel_hi:[0,1,1]
	v_mov_b32_e32 v76, v173
	v_pk_fma_f32 v[74:75], v[76:77], v[44:45], v[74:75] op_sel_hi:[0,1,1]
	ds_read_b128 v[220:223], v25 offset:47184
	s_waitcnt lgkmcnt(8)
	v_pk_fma_f32 v[80:81], v[48:49], v[174:175], v[84:85] op_sel_hi:[1,0,1]
	s_nop 0
	v_pk_fma_f32 v[76:77], v[174:175], v[46:47], v[80:81] op_sel:[1,0,0]
	s_nop 0
	v_pk_fma_f32 v[76:77], v[176:177], v[50:51], v[76:77] op_sel_hi:[0,1,1]
	v_mov_b32_e32 v78, v177
	v_pk_fma_f32 v[76:77], v[78:79], v[44:45], v[76:77] op_sel_hi:[0,1,1]
	ds_read_b128 v[224:227], v25 offset:55392
	s_waitcnt lgkmcnt(8)
	v_pk_fma_f32 v[82:83], v[48:49], v[178:179], v[86:87] op_sel_hi:[1,0,1]
	s_nop 0
	v_pk_fma_f32 v[78:79], v[178:179], v[46:47], v[82:83] op_sel:[1,0,0]
	s_nop 0
	v_pk_fma_f32 v[78:79], v[180:181], v[50:51], v[78:79] op_sel_hi:[0,1,1]
	v_mov_b32_e32 v80, v181
	v_pk_fma_f32 v[78:79], v[80:81], v[44:45], v[78:79] op_sel_hi:[0,1,1]
	ds_read_b128 v[228:231], v25 offset:63600
	s_waitcnt lgkmcnt(8)
	v_pk_fma_f32 v[48:49], v[48:49], v[182:183], v[88:89] op_sel_hi:[1,0,1]
	s_nop 0
	v_pk_fma_f32 v[46:47], v[182:183], v[46:47], v[48:49] op_sel:[1,0,0]
	v_mov_b32_e32 v48, v185
	v_pk_fma_f32 v[46:47], v[184:185], v[50:51], v[46:47] op_sel_hi:[0,1,1]
	v_pk_fma_f32 v[80:81], v[48:49], v[44:45], v[46:47] op_sel_hi:[0,1,1]
	ds_read_b128 v[232:235], v238 offset:6272
	s_waitcnt lgkmcnt(8)
	v_pk_fma_f32 v[48:49], v[40:41], v[186:187], v[52:53] op_sel_hi:[1,0,1]
	s_nop 0
	v_pk_fma_f32 v[44:45], v[186:187], v[38:39], v[48:49] op_sel:[1,0,0]
	s_nop 0
	v_pk_fma_f32 v[44:45], v[188:189], v[42:43], v[44:45] op_sel_hi:[0,1,1]
	v_mov_b32_e32 v46, v189
	v_pk_fma_f32 v[44:45], v[46:47], v[36:37], v[44:45] op_sel_hi:[0,1,1]
	ds_read_b128 v[242:245], v238 offset:14480
	s_waitcnt lgkmcnt(8)
; #define LAS __attribute__((address_space(3)))
; __global__ void __launch_bounds__(NTHREADS, 2) hybrid_fwd(Args a) {
;     ...
; #pragma unroll
;                     for (int j = 0; j < 8; ++j) {
; #pragma unroll
;                         for (int e = 0; e < 16; ++e) { const f32x4 w = *(const LAS f32x4*)(rwT + e * 2052 + j * 256 + lane * 4);
;                             acc2[e] += y2[j][0] * (f32x2){w[0], w[0]}; acc2[e] += y2[j][1] * (f32x2){w[1], w[1]};
;                             acc2[e] += y2[j][2] * (f32x2){w[2], w[2]}; acc2[e] += y2[j][3] * (f32x2){w[3], w[3]}; }
;                         __builtin_amdgcn_sched_barrier(0);
;                     }
	v_pk_fma_f32 v[50:51], v[40:41], v[198:199], v[90:91] op_sel_hi:[1,0,1]
	s_nop 0
	v_pk_fma_f32 v[46:47], v[198:199], v[38:39], v[50:51] op_sel:[1,0,0]
	s_nop 0
	v_pk_fma_f32 v[46:47], v[200:201], v[42:43], v[46:47] op_sel_hi:[0,1,1]
	v_mov_b32_e32 v48, v201
	v_pk_fma_f32 v[82:83], v[48:49], v[36:37], v[46:47] op_sel_hi:[0,1,1]
	ds_read_b128 v[246:249], v238 offset:22688
	s_waitcnt lgkmcnt(8)
	v_pk_fma_f32 v[50:51], v[40:41], v[202:203], v[54:55] op_sel_hi:[1,0,1]
	s_nop 0
	v_pk_fma_f32 v[46:47], v[202:203], v[38:39], v[50:51] op_sel:[1,0,0]
	s_nop 0
	v_pk_fma_f32 v[46:47], v[204:205], v[42:43], v[46:47] op_sel_hi:[0,1,1]
	v_mov_b32_e32 v48, v205
	v_pk_fma_f32 v[46:47], v[48:49], v[36:37], v[46:47] op_sel_hi:[0,1,1]
	ds_read_b128 v[250:253], v238 offset:30896
	s_waitcnt lgkmcnt(8)
	v_pk_fma_f32 v[52:53], v[40:41], v[216:217], v[56:57] op_sel_hi:[1,0,1]
	s_nop 0
	v_pk_fma_f32 v[48:49], v[216:217], v[38:39], v[52:53] op_sel:[1,0,0]
	s_nop 0
	v_pk_fma_f32 v[48:49], v[218:219], v[42:43], v[48:49] op_sel_hi:[0,1,1]
	v_mov_b32_e32 v50, v219
	v_pk_fma_f32 v[48:49], v[50:51], v[36:37], v[48:49] op_sel_hi:[0,1,1]
	ds_read_b128 v[162:165], v238 offset:39104
	s_waitcnt lgkmcnt(8)
	v_pk_fma_f32 v[54:55], v[40:41], v[158:159], v[58:59] op_sel_hi:[1,0,1]
	s_nop 0
	v_pk_fma_f32 v[50:51], v[158:159], v[38:39], v[54:55] op_sel:[1,0,0]
	s_nop 0
	v_pk_fma_f32 v[50:51], v[160:161], v[42:43], v[50:51] op_sel_hi:[0,1,1]
	v_mov_b32_e32 v52, v161
	v_pk_fma_f32 v[50:51], v[52:53], v[36:37], v[50:51] op_sel_hi:[0,1,1]
	ds_read_b128 v[166:169], v238 offset:47312
	s_waitcnt lgkmcnt(8)
	v_pk_fma_f32 v[56:57], v[40:41], v[220:221], v[60:61] op_sel_hi:[1,0,1]
	s_nop 0
	v_pk_fma_f32 v[52:53], v[220:221], v[38:39], v[56:57] op_sel:[1,0,0]
	s_nop 0
	v_pk_fma_f32 v[52:53], v[222:223], v[42:43], v[52:53] op_sel_hi:[0,1,1]
	v_mov_b32_e32 v54, v223
	v_pk_fma_f32 v[52:53], v[54:55], v[36:37], v[52:53] op_sel_hi:[0,1,1]
	ds_read_b128 v[170:173], v238 offset:55520
	s_waitcnt lgkmcnt(8)
	v_pk_fma_f32 v[58:59], v[40:41], v[224:225], v[62:63] op_sel_hi:[1,0,1]
	s_nop 0
	v_pk_fma_f32 v[54:55], v[224:225], v[38:39], v[58:59] op_sel:[1,0,0]
	s_nop 0
	v_pk_fma_f32 v[54:55], v[226:227], v[42:43], v[54:55] op_sel_hi:[0,1,1]
	v_mov_b32_e32 v56, v227
	v_pk_fma_f32 v[54:55], v[56:57], v[36:37], v[54:55] op_sel_hi:[0,1,1]
	ds_read_b128 v[174:177], v238 offset:63728
	s_waitcnt lgkmcnt(8)
	v_pk_fma_f32 v[60:61], v[40:41], v[228:229], v[64:65] op_sel_hi:[1,0,1]
	s_nop 0
	v_pk_fma_f32 v[56:57], v[228:229], v[38:39], v[60:61] op_sel:[1,0,0]
	s_nop 0
	v_pk_fma_f32 v[56:57], v[230:231], v[42:43], v[56:57] op_sel_hi:[0,1,1]
	v_mov_b32_e32 v58, v231
	v_pk_fma_f32 v[56:57], v[58:59], v[36:37], v[56:57] op_sel_hi:[0,1,1]
	ds_read_b128 v[178:181], v25 offset:7168
	s_waitcnt lgkmcnt(8)
	v_pk_fma_f32 v[62:63], v[40:41], v[232:233], v[66:67] op_sel_hi:[1,0,1]
	s_nop 0
	v_pk_fma_f32 v[58:59], v[232:233], v[38:39], v[62:63] op_sel:[1,0,0]
	s_nop 0
	v_pk_fma_f32 v[58:59], v[234:235], v[42:43], v[58:59] op_sel_hi:[0,1,1]
	v_mov_b32_e32 v60, v235
	v_pk_fma_f32 v[58:59], v[60:61], v[36:37], v[58:59] op_sel_hi:[0,1,1]
	ds_read_b128 v[182:185], v25 offset:15376
	s_waitcnt lgkmcnt(8)
	v_pk_fma_f32 v[64:65], v[40:41], v[242:243], v[68:69] op_sel_hi:[1,0,1]
	s_nop 0
	v_pk_fma_f32 v[60:61], v[242:243], v[38:39], v[64:65] op_sel:[1,0,0]
	s_nop 0
	v_pk_fma_f32 v[60:61], v[244:245], v[42:43], v[60:61] op_sel_hi:[0,1,1]
	v_mov_b32_e32 v62, v245
	v_pk_fma_f32 v[60:61], v[62:63], v[36:37], v[60:61] op_sel_hi:[0,1,1]
	ds_read_b128 v[186:189], v25 offset:23584
	s_waitcnt lgkmcnt(8)
	v_pk_fma_f32 v[66:67], v[40:41], v[246:247], v[70:71] op_sel_hi:[1,0,1]
	s_nop 0
	v_pk_fma_f32 v[62:63], v[246:247], v[38:39], v[66:67] op_sel:[1,0,0]
	s_nop 0
	v_pk_fma_f32 v[62:63], v[248:249], v[42:43], v[62:63] op_sel_hi:[0,1,1]
	v_mov_b32_e32 v64, v249
	v_pk_fma_f32 v[62:63], v[64:65], v[36:37], v[62:63] op_sel_hi:[0,1,1]
	ds_read_b128 v[198:201], v25 offset:31792
	s_waitcnt lgkmcnt(8)
	v_pk_fma_f32 v[68:69], v[40:41], v[250:251], v[72:73] op_sel_hi:[1,0,1]
	s_nop 0
	v_pk_fma_f32 v[64:65], v[250:251], v[38:39], v[68:69] op_sel:[1,0,0]
	s_nop 0
	v_pk_fma_f32 v[64:65], v[252:253], v[42:43], v[64:65] op_sel_hi:[0,1,1]
	v_mov_b32_e32 v66, v253
	v_pk_fma_f32 v[64:65], v[66:67], v[36:37], v[64:65] op_sel_hi:[0,1,1]
	ds_read_b128 v[202:205], v25 offset:40000
	s_waitcnt lgkmcnt(8)
	v_pk_fma_f32 v[70:71], v[40:41], v[162:163], v[74:75] op_sel_hi:[1,0,1]
	s_nop 0
	v_pk_fma_f32 v[66:67], v[162:163], v[38:39], v[70:71] op_sel:[1,0,0]
	s_nop 0
	v_pk_fma_f32 v[66:67], v[164:165], v[42:43], v[66:67] op_sel_hi:[0,1,1]
	v_mov_b32_e32 v68, v165
	v_pk_fma_f32 v[66:67], v[68:69], v[36:37], v[66:67] op_sel_hi:[0,1,1]
	ds_read_b128 v[216:219], v25 offset:48208
	s_waitcnt lgkmcnt(8)
	v_pk_fma_f32 v[72:73], v[40:41], v[166:167], v[76:77] op_sel_hi:[1,0,1]
	s_nop 0
	v_pk_fma_f32 v[68:69], v[166:167], v[38:39], v[72:73] op_sel:[1,0,0]
	s_nop 0
	v_pk_fma_f32 v[68:69], v[168:169], v[42:43], v[68:69] op_sel_hi:[0,1,1]
	v_mov_b32_e32 v70, v169
	v_pk_fma_f32 v[68:69], v[70:71], v[36:37], v[68:69] op_sel_hi:[0,1,1]
	ds_read_b128 v[158:161], v25 offset:56416
	s_waitcnt lgkmcnt(8)
	v_pk_fma_f32 v[74:75], v[40:41], v[170:171], v[78:79] op_sel_hi:[1,0,1]
	s_nop 0
	v_pk_fma_f32 v[70:71], v[170:171], v[38:39], v[74:75] op_sel:[1,0,0]
	s_nop 0
	v_pk_fma_f32 v[70:71], v[172:173], v[42:43], v[70:71] op_sel_hi:[0,1,1]
	v_mov_b32_e32 v72, v173
	v_pk_fma_f32 v[70:71], v[72:73], v[36:37], v[70:71] op_sel_hi:[0,1,1]
	ds_read_b128 v[220:223], v25 offset:64624
	s_waitcnt lgkmcnt(8)
; #define LAS __attribute__((address_space(3)))
; __global__ void __launch_bounds__(NTHREADS, 2) hybrid_fwd(Args a) {
;     ...
; #pragma unroll
;                     for (int j = 0; j < 8; ++j) {
; #pragma unroll
;                         for (int e = 0; e < 16; ++e) { const f32x4 w = *(const LAS f32x4*)(rwT + e * 2052 + j * 256 + lane * 4);
;                             acc2[e] += y2[j][0] * (f32x2){w[0], w[0]}; acc2[e] += y2[j][1] * (f32x2){w[1], w[1]};
;                             acc2[e] += y2[j][2] * (f32x2){w[2], w[2]}; acc2[e] += y2[j][3] * (f32x2){w[3], w[3]}; }
;                         __builtin_amdgcn_sched_barrier(0);
;                     }
	v_pk_fma_f32 v[40:41], v[40:41], v[174:175], v[80:81] op_sel_hi:[1,0,1]
	s_nop 0
	v_pk_fma_f32 v[38:39], v[174:175], v[38:39], v[40:41] op_sel:[1,0,0]
	v_mov_b32_e32 v40, v177
	v_pk_fma_f32 v[38:39], v[176:177], v[42:43], v[38:39] op_sel_hi:[0,1,1]
	v_pk_fma_f32 v[72:73], v[40:41], v[36:37], v[38:39] op_sel_hi:[0,1,1]
	ds_read_b128 v[224:227], v238 offset:7296
	s_waitcnt lgkmcnt(8)
	v_pk_fma_f32 v[40:41], v[22:23], v[178:179], v[44:45] op_sel_hi:[1,0,1]
	s_nop 0
	v_pk_fma_f32 v[36:37], v[178:179], v[18:19], v[40:41] op_sel:[1,0,0]
	s_nop 0
	v_pk_fma_f32 v[36:37], v[180:181], v[20:21], v[36:37] op_sel_hi:[0,1,1]
	v_mov_b32_e32 v38, v181
	v_pk_fma_f32 v[36:37], v[38:39], v[16:17], v[36:37] op_sel_hi:[0,1,1]
	ds_read_b128 v[228:231], v238 offset:15504
	s_waitcnt lgkmcnt(8)
	v_pk_fma_f32 v[42:43], v[22:23], v[182:183], v[82:83] op_sel_hi:[1,0,1]
	s_nop 0
	v_pk_fma_f32 v[38:39], v[182:183], v[18:19], v[42:43] op_sel:[1,0,0]
	s_nop 0
	v_pk_fma_f32 v[38:39], v[184:185], v[20:21], v[38:39] op_sel_hi:[0,1,1]
	v_mov_b32_e32 v40, v185
	v_pk_fma_f32 v[38:39], v[40:41], v[16:17], v[38:39] op_sel_hi:[0,1,1]
	ds_read_b128 v[232:235], v238 offset:23712
	s_waitcnt lgkmcnt(8)
	v_pk_fma_f32 v[44:45], v[22:23], v[186:187], v[46:47] op_sel_hi:[1,0,1]
	s_nop 0
	v_pk_fma_f32 v[40:41], v[186:187], v[18:19], v[44:45] op_sel:[1,0,0]
	s_nop 0
	v_pk_fma_f32 v[40:41], v[188:189], v[20:21], v[40:41] op_sel_hi:[0,1,1]
	v_mov_b32_e32 v42, v189
	v_pk_fma_f32 v[40:41], v[42:43], v[16:17], v[40:41] op_sel_hi:[0,1,1]
	ds_read_b128 v[242:245], v238 offset:31920
	s_waitcnt lgkmcnt(8)
	v_pk_fma_f32 v[46:47], v[22:23], v[198:199], v[48:49] op_sel_hi:[1,0,1]
	s_nop 0
	v_pk_fma_f32 v[42:43], v[198:199], v[18:19], v[46:47] op_sel:[1,0,0]
	ds_read_b128 v[246:249], v238 offset:40128
	v_pk_fma_f32 v[42:43], v[200:201], v[20:21], v[42:43] op_sel_hi:[0,1,1]
	v_mov_b32_e32 v44, v201
	v_pk_fma_f32 v[44:45], v[44:45], v[16:17], v[42:43] op_sel_hi:[0,1,1]
	s_waitcnt lgkmcnt(8)
	v_pk_fma_f32 v[42:43], v[22:23], v[202:203], v[50:51] op_sel_hi:[1,0,1]
	s_nop 0
	v_pk_fma_f32 v[42:43], v[202:203], v[18:19], v[42:43] op_sel:[1,0,0]
	v_mov_b32_e32 v46, v205
	v_pk_fma_f32 v[42:43], v[204:205], v[20:21], v[42:43] op_sel_hi:[0,1,1]
	v_pk_fma_f32 v[42:43], v[46:47], v[16:17], v[42:43] op_sel_hi:[0,1,1]
	ds_read_b128 v[250:253], v238 offset:48336
	s_waitcnt lgkmcnt(8)
	v_pk_fma_f32 v[50:51], v[22:23], v[216:217], v[52:53] op_sel_hi:[1,0,1]
	s_nop 0
	v_pk_fma_f32 v[46:47], v[216:217], v[18:19], v[50:51] op_sel:[1,0,0]
	s_nop 0
	v_pk_fma_f32 v[46:47], v[218:219], v[20:21], v[46:47] op_sel_hi:[0,1,1]
	v_mov_b32_e32 v48, v219
	v_pk_fma_f32 v[46:47], v[48:49], v[16:17], v[46:47] op_sel_hi:[0,1,1]
	ds_read_b128 v[162:165], v238 offset:56544
	s_waitcnt lgkmcnt(8)
	v_pk_fma_f32 v[52:53], v[22:23], v[158:159], v[54:55] op_sel_hi:[1,0,1]
	s_nop 0
	v_pk_fma_f32 v[48:49], v[158:159], v[18:19], v[52:53] op_sel:[1,0,0]
	s_nop 0
	v_pk_fma_f32 v[48:49], v[160:161], v[20:21], v[48:49] op_sel_hi:[0,1,1]
	v_mov_b32_e32 v50, v161
	v_pk_fma_f32 v[48:49], v[50:51], v[16:17], v[48:49] op_sel_hi:[0,1,1]
	ds_read_b128 v[166:169], v238 offset:64752
	s_waitcnt lgkmcnt(8)
	v_pk_fma_f32 v[54:55], v[22:23], v[220:221], v[56:57] op_sel_hi:[1,0,1]
	s_nop 0
	v_pk_fma_f32 v[50:51], v[220:221], v[18:19], v[54:55] op_sel:[1,0,0]
	s_nop 0
	v_pk_fma_f32 v[50:51], v[222:223], v[20:21], v[50:51] op_sel_hi:[0,1,1]
	v_mov_b32_e32 v52, v223
	v_pk_fma_f32 v[50:51], v[52:53], v[16:17], v[50:51] op_sel_hi:[0,1,1]
	s_waitcnt lgkmcnt(7)
	v_pk_fma_f32 v[56:57], v[22:23], v[224:225], v[58:59] op_sel_hi:[1,0,1]
	s_nop 0
	v_pk_fma_f32 v[52:53], v[224:225], v[18:19], v[56:57] op_sel:[1,0,0]
	s_nop 0
	v_pk_fma_f32 v[52:53], v[226:227], v[20:21], v[52:53] op_sel_hi:[0,1,1]
	v_mov_b32_e32 v54, v227
	v_pk_fma_f32 v[52:53], v[54:55], v[16:17], v[52:53] op_sel_hi:[0,1,1]
	s_waitcnt lgkmcnt(6)
	v_pk_fma_f32 v[58:59], v[22:23], v[228:229], v[60:61] op_sel_hi:[1,0,1]
	s_nop 0
	v_pk_fma_f32 v[54:55], v[228:229], v[18:19], v[58:59] op_sel:[1,0,0]
	s_nop 0
	v_pk_fma_f32 v[54:55], v[230:231], v[20:21], v[54:55] op_sel_hi:[0,1,1]
	v_mov_b32_e32 v56, v231
	v_pk_fma_f32 v[54:55], v[56:57], v[16:17], v[54:55] op_sel_hi:[0,1,1]
	s_waitcnt lgkmcnt(5)
	v_pk_fma_f32 v[60:61], v[22:23], v[232:233], v[62:63] op_sel_hi:[1,0,1]
	s_nop 0
	v_pk_fma_f32 v[56:57], v[232:233], v[18:19], v[60:61] op_sel:[1,0,0]
	s_nop 0
	v_pk_fma_f32 v[56:57], v[234:235], v[20:21], v[56:57] op_sel_hi:[0,1,1]
	v_mov_b32_e32 v58, v235
	v_pk_fma_f32 v[56:57], v[58:59], v[16:17], v[56:57] op_sel_hi:[0,1,1]
	s_waitcnt lgkmcnt(4)
	v_pk_fma_f32 v[62:63], v[22:23], v[242:243], v[64:65] op_sel_hi:[1,0,1]
	s_nop 0
	v_pk_fma_f32 v[58:59], v[242:243], v[18:19], v[62:63] op_sel:[1,0,0]
	s_nop 0
	v_pk_fma_f32 v[58:59], v[244:245], v[20:21], v[58:59] op_sel_hi:[0,1,1]
	v_mov_b32_e32 v60, v245
	v_pk_fma_f32 v[58:59], v[60:61], v[16:17], v[58:59] op_sel_hi:[0,1,1]
	s_waitcnt lgkmcnt(3)
	v_pk_fma_f32 v[64:65], v[22:23], v[246:247], v[66:67] op_sel_hi:[1,0,1]
	s_nop 0
	v_pk_fma_f32 v[60:61], v[246:247], v[18:19], v[64:65] op_sel:[1,0,0]
	s_nop 0
	v_pk_fma_f32 v[60:61], v[248:249], v[20:21], v[60:61] op_sel_hi:[0,1,1]
	v_mov_b32_e32 v62, v249
	v_pk_fma_f32 v[60:61], v[62:63], v[16:17], v[60:61] op_sel_hi:[0,1,1]
	s_waitcnt lgkmcnt(2)
	v_pk_fma_f32 v[66:67], v[22:23], v[250:251], v[68:69] op_sel_hi:[1,0,1]
	s_nop 0
	v_pk_fma_f32 v[62:63], v[250:251], v[18:19], v[66:67] op_sel:[1,0,0]
	s_nop 0
	v_pk_fma_f32 v[62:63], v[252:253], v[20:21], v[62:63] op_sel_hi:[0,1,1]
	v_mov_b32_e32 v64, v253
	v_pk_fma_f32 v[62:63], v[64:65], v[16:17], v[62:63] op_sel_hi:[0,1,1]
	s_waitcnt lgkmcnt(1)
; #define WS_STEP(ctrl) v += __int_as_float(__builtin_amdgcn_update_dpp(0, __float_as_int(v), (ctrl), 0xf, 0xf, true))
; __device__ __forceinline__ float wave_sum(float v) {
;     ...
;     WS_STEP(0xB1); WS_STEP(0x4E); WS_STEP(0x124); WS_STEP(0x128);
;     ...
;     const auto r16 = __builtin_amdgcn_permlane16_swap(__float_as_uint(v), __float_as_uint(v), false, false);
;     v = __uint_as_float(r16[0]) + __uint_as_float(r16[1]);
;     const auto rr = __builtin_amdgcn_permlane32_swap(__float_as_uint(v), __float_as_uint(v), false, false);
;     return __uint_as_float(rr[0]) + __uint_as_float(rr[1]);
; }
; __device__ __forceinline__ float sigmoidf_(float x) { return __builtin_amdgcn_rcpf(1.f + __expf(-x)); }
	v_pk_fma_f32 v[68:69], v[22:23], v[162:163], v[70:71] op_sel_hi:[1,0,1]
	s_nop 0
	v_pk_fma_f32 v[64:65], v[162:163], v[18:19], v[68:69] op_sel:[1,0,0]
	s_nop 0
	v_pk_fma_f32 v[64:65], v[164:165], v[20:21], v[64:65] op_sel_hi:[0,1,1]
	v_mov_b32_e32 v66, v165
	v_pk_fma_f32 v[64:65], v[66:67], v[16:17], v[64:65] op_sel_hi:[0,1,1]
	s_waitcnt lgkmcnt(0)
	v_pk_fma_f32 v[22:23], v[22:23], v[166:167], v[72:73] op_sel_hi:[1,0,1]
	s_nop 0
	v_pk_fma_f32 v[18:19], v[166:167], v[18:19], v[22:23] op_sel:[1,0,0]
	s_nop 0
	v_pk_fma_f32 v[18:19], v[168:169], v[20:21], v[18:19] op_sel_hi:[0,1,1]
	v_mov_b32_e32 v20, v169
	v_pk_fma_f32 v[16:17], v[20:21], v[16:17], v[18:19] op_sel_hi:[0,1,1]
	s_nop 1
	v_permlane32_swap_b32_e32 v16, v17
	v_permlane32_swap_b32_e32 v36, v37
	v_permlane32_swap_b32_e32 v38, v39
	v_permlane32_swap_b32_e32 v40, v41
	v_permlane32_swap_b32_e32 v42, v43
	v_permlane32_swap_b32_e32 v44, v45
	v_permlane32_swap_b32_e32 v46, v47
	v_permlane32_swap_b32_e32 v48, v49
	v_permlane32_swap_b32_e32 v50, v51
	v_permlane32_swap_b32_e32 v52, v53
	v_permlane32_swap_b32_e32 v54, v55
	v_permlane32_swap_b32_e32 v56, v57
	v_permlane32_swap_b32_e32 v58, v59
	v_permlane32_swap_b32_e32 v60, v61
	v_permlane32_swap_b32_e32 v62, v63
	v_permlane32_swap_b32_e32 v64, v65
	v_add_f32_e32 v16, v16, v17
	v_add_f32_e32 v36, v36, v37
	v_add_f32_e32 v38, v38, v39
	v_add_f32_e32 v40, v40, v41
	v_add_f32_e32 v42, v42, v43
	v_add_f32_e32 v44, v44, v45
	v_add_f32_e32 v46, v46, v47
	v_add_f32_e32 v48, v48, v49
	v_add_f32_e32 v50, v50, v51
	v_add_f32_e32 v52, v52, v53
	v_add_f32_e32 v54, v54, v55
	v_add_f32_e32 v56, v56, v57
	v_add_f32_e32 v58, v58, v59
	v_add_f32_e32 v60, v60, v61
	v_add_f32_e32 v62, v62, v63
	v_add_f32_e32 v64, v64, v65
	s_nop 1
	v_add_f32_dpp v18, v36, v36 quad_perm:[1,0,3,2] row_mask:0xf bank_mask:0xf bound_ctrl:1
	s_nop 0
	v_add_f32_dpp v16, v16, v16 quad_perm:[1,0,3,2] row_mask:0xf bank_mask:0xf bound_ctrl:1
	v_add_f32_dpp v36, v62, v62 quad_perm:[1,0,3,2] row_mask:0xf bank_mask:0xf bound_ctrl:1
	v_add_f32_dpp v18, v18, v18 quad_perm:[2,3,0,1] row_mask:0xf bank_mask:0xf bound_ctrl:1
	v_add_f32_dpp v16, v16, v16 quad_perm:[2,3,0,1] row_mask:0xf bank_mask:0xf bound_ctrl:1
	v_add_f32_dpp v36, v36, v36 quad_perm:[2,3,0,1] row_mask:0xf bank_mask:0xf bound_ctrl:1
	v_add_f32_dpp v18, v18, v18 row_ror:4 row_mask:0xf bank_mask:0xf bound_ctrl:1
	v_add_f32_dpp v16, v16, v16 row_ror:4 row_mask:0xf bank_mask:0xf bound_ctrl:1
	v_add_f32_dpp v36, v36, v36 row_ror:4 row_mask:0xf bank_mask:0xf bound_ctrl:1
	v_add_f32_dpp v18, v18, v18 row_ror:8 row_mask:0xf bank_mask:0xf bound_ctrl:1
	v_mov_b32_e32 v19, v18
	s_nop 1
	v_permlane16_swap_b32_e32 v18, v19
	v_add_f32_e32 v18, v18, v19
	v_mov_b32_e32 v19, v18
	s_nop 1
	s_nop 0
	v_mov_b32_e32 v18, v18
	s_nop 0
	v_add_f32_dpp v19, v38, v38 quad_perm:[1,0,3,2] row_mask:0xf bank_mask:0xf bound_ctrl:1
	v_mul_f32_e32 v18, 0xbfb8aa3b, v18
	v_exp_f32_e32 v18, v18
	v_add_f32_dpp v19, v19, v19 quad_perm:[2,3,0,1] row_mask:0xf bank_mask:0xf bound_ctrl:1
	v_add_f32_dpp v16, v16, v16 row_ror:8 row_mask:0xf bank_mask:0xf bound_ctrl:1
	v_add_f32_dpp v36, v36, v36 row_ror:8 row_mask:0xf bank_mask:0xf bound_ctrl:1
	v_add_f32_dpp v19, v19, v19 row_ror:4 row_mask:0xf bank_mask:0xf bound_ctrl:1
	v_add_f32_e32 v18, 1.0, v18
	v_rcp_f32_e32 v18, v18
	v_add_f32_dpp v19, v19, v19 row_ror:8 row_mask:0xf bank_mask:0xf bound_ctrl:1
	v_mov_b32_e32 v20, v19
	s_nop 1
	v_permlane16_swap_b32_e32 v19, v20
	v_add_f32_e32 v19, v19, v20
	v_mov_b32_e32 v20, v19
	s_nop 1
	s_nop 0
	v_mov_b32_e32 v19, v19
	s_nop 0
	v_add_f32_dpp v20, v40, v40 quad_perm:[1,0,3,2] row_mask:0xf bank_mask:0xf bound_ctrl:1
	v_mul_f32_e32 v19, 0xbfb8aa3b, v19
	v_exp_f32_e32 v19, v19
	v_add_f32_dpp v20, v20, v20 quad_perm:[2,3,0,1] row_mask:0xf bank_mask:0xf bound_ctrl:1
	v_add_f32_dpp v40, v64, v64 quad_perm:[1,0,3,2] row_mask:0xf bank_mask:0xf bound_ctrl:1
	v_mov_b32_e32 v38, v36
	v_add_f32_dpp v20, v20, v20 row_ror:4 row_mask:0xf bank_mask:0xf bound_ctrl:1
	v_add_f32_e32 v19, 1.0, v19
	v_rcp_f32_e32 v19, v19
	v_add_f32_dpp v20, v20, v20 row_ror:8 row_mask:0xf bank_mask:0xf bound_ctrl:1
	v_mov_b32_e32 v21, v20
	s_nop 1
	v_permlane16_swap_b32_e32 v20, v21
	v_add_f32_e32 v20, v20, v21
	v_mov_b32_e32 v21, v20
	s_nop 1
	s_nop 0
	v_mov_b32_e32 v20, v20
	s_nop 0
	v_add_f32_dpp v21, v44, v44 quad_perm:[1,0,3,2] row_mask:0xf bank_mask:0xf bound_ctrl:1
	v_mul_f32_e32 v20, 0xbfb8aa3b, v20
	v_exp_f32_e32 v20, v20
	v_add_f32_dpp v21, v21, v21 quad_perm:[2,3,0,1] row_mask:0xf bank_mask:0xf bound_ctrl:1
	v_mov_b32_e32 v44, v16
	s_nop 1
	v_permlane16_swap_b32_e32 v16, v44
	v_add_f32_dpp v21, v21, v21 row_ror:4 row_mask:0xf bank_mask:0xf bound_ctrl:1
	v_add_f32_e32 v20, 1.0, v20
	v_rcp_f32_e32 v70, v20
	v_add_f32_dpp v21, v21, v21 row_ror:8 row_mask:0xf bank_mask:0xf bound_ctrl:1
	v_mov_b32_e32 v22, v21
	s_nop 1
	v_permlane16_swap_b32_e32 v21, v22
	v_add_f32_e32 v21, v21, v22
	v_mov_b32_e32 v22, v21
	s_nop 1
	s_nop 0
	v_mov_b32_e32 v21, v21
	s_nop 0
	v_add_f32_dpp v22, v42, v42 quad_perm:[1,0,3,2] row_mask:0xf bank_mask:0xf bound_ctrl:1
	v_mul_f32_e32 v21, 0xbfb8aa3b, v21
	v_exp_f32_e32 v21, v21
	v_add_f32_dpp v22, v22, v22 quad_perm:[2,3,0,1] row_mask:0xf bank_mask:0xf bound_ctrl:1
	v_add_f32_e32 v79, v14, v70
	v_add_f32_e32 v44, v16, v44
	v_add_f32_dpp v22, v22, v22 row_ror:4 row_mask:0xf bank_mask:0xf bound_ctrl:1
	v_add_f32_e32 v20, 1.0, v21
	v_rcp_f32_e32 v72, v20
	v_add_f32_dpp v22, v22, v22 row_ror:8 row_mask:0xf bank_mask:0xf bound_ctrl:1
	v_mov_b32_e32 v23, v22
	s_nop 1
	v_permlane16_swap_b32_e32 v22, v23
	v_add_f32_e32 v69, v22, v23
	s_nop 0
	v_add_f32_dpp v22, v46, v46 quad_perm:[1,0,3,2] row_mask:0xf bank_mask:0xf bound_ctrl:1
	v_pk_add_f32 v[20:21], v[12:13], v[18:19]
	v_add_f32_e32 v80, v15, v72
	v_add_f32_dpp v22, v22, v22 quad_perm:[2,3,0,1] row_mask:0xf bank_mask:0xf bound_ctrl:1
	v_cmp_gt_f32_e32 vcc, v21, v20
	v_add_f32_dpp v40, v40, v40 quad_perm:[2,3,0,1] row_mask:0xf bank_mask:0xf bound_ctrl:1
	v_add_f32_dpp v22, v22, v22 row_ror:4 row_mask:0xf bank_mask:0xf bound_ctrl:1
	v_cndmask_b32_e32 v16, v20, v21, vcc
	v_cmp_gt_f32_e64 s[6:7], v79, v16
	v_add_f32_dpp v22, v22, v22 row_ror:8 row_mask:0xf bank_mask:0xf bound_ctrl:1
	v_mov_b32_e32 v23, v22
	s_nop 1
	v_permlane16_swap_b32_e32 v22, v23
	v_add_f32_e32 v73, v22, v23
	s_nop 0
	v_add_f32_dpp v22, v48, v48 quad_perm:[1,0,3,2] row_mask:0xf bank_mask:0xf bound_ctrl:1
	v_cndmask_b32_e64 v48, 0, 1, vcc
	v_cndmask_b32_e64 v16, v16, v79, s[6:7]
	v_add_f32_dpp v22, v22, v22 quad_perm:[2,3,0,1] row_mask:0xf bank_mask:0xf bound_ctrl:1
	v_cndmask_b32_e64 v48, v48, 2, s[6:7]
	v_cmp_ngt_f32_e64 s[8:9], v80, v16
	v_add_f32_dpp v22, v22, v22 row_ror:4 row_mask:0xf bank_mask:0xf bound_ctrl:1
	v_add_f32_dpp v40, v40, v40 row_ror:4 row_mask:0xf bank_mask:0xf bound_ctrl:1
	v_permlane16_swap_b32_e32 v36, v38
	v_add_f32_dpp v22, v22, v22 row_ror:8 row_mask:0xf bank_mask:0xf bound_ctrl:1
	v_mov_b32_e32 v23, v22
	s_nop 1
	v_permlane16_swap_b32_e32 v22, v23
	v_add_f32_e32 v75, v22, v23
	s_nop 0
	v_add_f32_dpp v22, v50, v50 quad_perm:[1,0,3,2] row_mask:0xf bank_mask:0xf bound_ctrl:1
	v_add_f32_dpp v40, v40, v40 row_ror:8 row_mask:0xf bank_mask:0xf bound_ctrl:1
	v_mov_b32_e32 v42, v40
	v_add_f32_dpp v22, v22, v22 quad_perm:[2,3,0,1] row_mask:0xf bank_mask:0xf bound_ctrl:1
	s_nop 0
	v_permlane16_swap_b32_e32 v40, v42
	v_add_f32_dpp v22, v22, v22 row_ror:4 row_mask:0xf bank_mask:0xf bound_ctrl:1
	v_add_f32_e32 v36, v36, v38
	v_add_f32_e32 v40, v40, v42
	v_add_f32_dpp v22, v22, v22 row_ror:8 row_mask:0xf bank_mask:0xf bound_ctrl:1
	v_mov_b32_e32 v23, v22
	s_nop 1
	v_permlane16_swap_b32_e32 v22, v23
	v_add_f32_e32 v77, v22, v23
	s_nop 0
	v_add_f32_dpp v22, v52, v52 quad_perm:[1,0,3,2] row_mask:0xf bank_mask:0xf bound_ctrl:1
	v_cndmask_b32_e64 v62, v80, v16, s[8:9]
	v_mov_b32_e32 v71, v69
	v_add_f32_dpp v22, v22, v22 quad_perm:[2,3,0,1] row_mask:0xf bank_mask:0xf bound_ctrl:1
	v_mov_b32_e32 v74, v73
	v_mov_b32_e32 v76, v75
	v_add_f32_dpp v22, v22, v22 row_ror:4 row_mask:0xf bank_mask:0xf bound_ctrl:1
	v_mov_b32_e32 v78, v77
	v_mov_b32_e32 v38, v36
	v_add_f32_dpp v22, v22, v22 row_ror:8 row_mask:0xf bank_mask:0xf bound_ctrl:1
	v_mov_b32_e32 v23, v22
	s_nop 1
	v_permlane16_swap_b32_e32 v22, v23
	v_add_f32_e32 v50, v22, v23
	s_nop 0
	v_add_f32_dpp v22, v54, v54 quad_perm:[1,0,3,2] row_mask:0xf bank_mask:0xf bound_ctrl:1
	v_mov_b32_e32 v52, v50
	v_mov_b32_e32 v42, v40
	v_add_f32_dpp v22, v22, v22 quad_perm:[2,3,0,1] row_mask:0xf bank_mask:0xf bound_ctrl:1
	v_mov_b32_e32 v46, v44
	s_nop 0
	v_add_f32_dpp v22, v22, v22 row_ror:4 row_mask:0xf bank_mask:0xf bound_ctrl:1
	s_nop 0
	s_nop 0
	v_add_f32_dpp v22, v22, v22 row_ror:8 row_mask:0xf bank_mask:0xf bound_ctrl:1
	v_mov_b32_e32 v23, v22
	s_nop 1
	v_permlane16_swap_b32_e32 v22, v23
	v_add_f32_e32 v54, v22, v23
	s_nop 0
	v_add_f32_dpp v22, v56, v56 quad_perm:[1,0,3,2] row_mask:0xf bank_mask:0xf bound_ctrl:1
	v_mov_b32_e32 v66, v54
	s_nop 0
	v_add_f32_dpp v22, v22, v22 quad_perm:[2,3,0,1] row_mask:0xf bank_mask:0xf bound_ctrl:1
	s_nop 0
	s_nop 0
	v_add_f32_dpp v22, v22, v22 row_ror:4 row_mask:0xf bank_mask:0xf bound_ctrl:1
	s_nop 0
	s_nop 0
	v_add_f32_dpp v22, v22, v22 row_ror:8 row_mask:0xf bank_mask:0xf bound_ctrl:1
	v_mov_b32_e32 v23, v22
	s_nop 1
	v_permlane16_swap_b32_e32 v22, v23
	v_add_f32_e32 v56, v22, v23
	s_nop 0
	v_add_f32_dpp v22, v58, v58 quad_perm:[1,0,3,2] row_mask:0xf bank_mask:0xf bound_ctrl:1
	v_mov_b32_e32 v67, v56
	s_nop 0
	v_add_f32_dpp v22, v22, v22 quad_perm:[2,3,0,1] row_mask:0xf bank_mask:0xf bound_ctrl:1
	s_nop 0
	s_nop 0
	v_add_f32_dpp v22, v22, v22 row_ror:4 row_mask:0xf bank_mask:0xf bound_ctrl:1
	s_nop 0
	s_nop 0
	v_add_f32_dpp v22, v22, v22 row_ror:8 row_mask:0xf bank_mask:0xf bound_ctrl:1
	v_mov_b32_e32 v23, v22
	s_nop 1
	v_permlane16_swap_b32_e32 v22, v23
	v_add_f32_e32 v58, v22, v23
	s_nop 0
	v_add_f32_dpp v22, v60, v60 quad_perm:[1,0,3,2] row_mask:0xf bank_mask:0xf bound_ctrl:1
	v_cndmask_b32_e64 v60, 3, v48, s[8:9]
	v_mov_b32_e32 v48, 0xff800000
	v_cmp_eq_u32_e64 s[10:11], 0, v60
	v_cmp_nlg_f32_e64 s[12:13], v20, v48
	s_or_b64 s[10:11], s[10:11], s[12:13]
	v_cndmask_b32_e64 v20, v20, v48, s[10:11]
	v_cmp_ne_u32_e64 s[12:13], 1, v60
	v_cmp_gt_f32_e64 s[14:15], v21, v20
	s_and_b64 s[12:13], s[12:13], s[14:15]
	v_cndmask_b32_e64 v20, v20, v21, s[12:13]
	v_add_f32_dpp v22, v22, v22 quad_perm:[2,3,0,1] row_mask:0xf bank_mask:0xf bound_ctrl:1
	v_cmp_ne_u32_e64 s[14:15], 2, v60
	v_cmp_gt_f32_e64 s[16:17], v79, v20
	v_add_f32_dpp v22, v22, v22 row_ror:4 row_mask:0xf bank_mask:0xf bound_ctrl:1
	s_and_b64 s[14:15], s[14:15], s[16:17]
	v_cndmask_b32_e64 v20, v20, v79, s[14:15]
	v_add_f32_dpp v22, v22, v22 row_ror:8 row_mask:0xf bank_mask:0xf bound_ctrl:1
	v_mov_b32_e32 v23, v22
	v_cmp_gt_f32_e64 s[16:17], v80, v20
	s_nop 0
	v_permlane16_swap_b32_e32 v22, v23
	s_and_b64 s[16:17], s[8:9], s[16:17]
	v_add_f32_e32 v22, v22, v23
	v_cndmask_b32_e64 v20, v20, v80, s[16:17]
	v_mov_b32_e32 v68, v58
	v_mov_b32_e32 v23, v22
	v_add_f32_e32 v62, v62, v20
	s_nop 0
	s_nop 0
	s_nop 0
	s_nop 0
	v_mov_b32_e32 v16, 1
	v_cmp_lg_f32_e64 s[18:19], v62, v48
	v_mov_b32_e32 v21, 0
	v_mov_b32_e32 v20, 0
	s_and_saveexec_b64 s[38:39], s[18:19]
	s_cbranch_execz .LBB0_911
	v_cndmask_b32_e64 v20, v18, 0, s[10:11]
	v_cndmask_b32_e64 v16, 0, 1, s[12:13]
	v_cndmask_b32_e64 v20, v20, v19, s[12:13]
	v_cndmask_b32_e32 v18, v18, v19, vcc
	v_cndmask_b32_e64 v16, v16, 2, s[14:15]
	v_cndmask_b32_e64 v20, v20, v70, s[14:15]
	v_cndmask_b32_e64 v18, v18, v70, s[6:7]
	v_cndmask_b32_e64 v16, v16, 3, s[16:17]
	v_cndmask_b32_e64 v35, v20, v72, s[16:17]
	v_cndmask_b32_e64 v21, v72, v18, s[8:9]
	v_mov_b32_e32 v20, v60
	v_mov_b32_e32 v48, v62
